# v40: v39 + nt on single-use loads: down-proj epilogue residual rows, SGU X/gu rows, merged-branch GEMM epilogue gates and mid-K ga gates
# baseline (speedup 1.0000x reference)
; #define GAS __attribute__((address_space(1)))
; #define LAS __attribute__((address_space(3)))
; __device__ __forceinline__ unsigned pk2(float lo, float hi) { return pg8::cvt_pk_bf16(lo, hi); }
; __device__ __forceinline__ void sgu_unit(Frame& F, int unit) {
;     ...
;     __syncthreads();
; #pragma unroll
;     for (int i = 0; i < 8; ++i) *(LAS v4u*)(L + (rs_ + 16 * i) * 512 + q_ * 16) = *(const GAS v4u*)(F.PROJ + (size_t)(r0 + rs_ + 16 * i) * PNP + PGV + c0 + 8 * q_);
;     { const f32x4 q = *(const GAS f32x4*)(F.RS + r0 + 4 * q_);
; #pragma unroll
;       for (int i = 0; i < 8; ++i) { const int t_ = rs_ + 16 * i; const f32x4 wv = *(const GAS f32x4*)(F.sgw + ((size_t)(g * GMC + t_)) * GMC + 4 * q_);
;           const int sb = 4 * q_; v2u o;
;           o.x = pk2(sb + 0 <= t_ ? wv.x * q.x : 0.f, sb + 1 <= t_ ? wv.y * q.y : 0.f); o.y = pk2(sb + 2 <= t_ ? wv.z * q.z : 0.f, sb + 3 <= t_ ? wv.w * q.w : 0.f);
;           *(LAS v2u*)(L + SG_WOFF + t_ * SG_STR + 8 * q_) = o; } }
.LBB0_1330:
	s_and_b32 s74, s33, 0xffffff80
	s_and_b32 s83, s82, 7
	v_or_b32_e32 v128, s74, v1
	v_mad_i64_i32 v[2:3], s[0:1], v128, s77, v[108:109]
	s_lshl_b32 s84, s83, 9
	s_mov_b32 s85, s73
	v_lshl_add_u64 v[2:3], v[2:3], 0, s[84:85]
	v_lshl_add_u64 v[2:3], v[2:3], 0, v[110:111]
	v_add_co_u32_e64 v4, s[0:1], s78, v2
	s_nop 1
	v_addc_co_u32_e64 v5, s[0:1], 0, v3, s[0:1]
	s_barrier
	global_load_dwordx4 v[28:31], v[4:5], off offset:2048 nt
	v_or_b32_e32 v126, 16, v128
	v_or_b32_e32 v124, 32, v128
	v_or_b32_e32 v122, 48, v128
	v_or_b32_e32 v120, 64, v128
	v_or_b32_e32 v118, 0x50, v128
	v_or_b32_e32 v116, 0x60, v128
	v_or_b32_e32 v114, 0x70, v128
	s_ashr_i32 s75, s74, 31
	v_ashrrev_i32_e32 v129, 31, v128
	s_lshl_b32 s72, s83, 8
	v_ashrrev_i32_e32 v127, 31, v126
	v_ashrrev_i32_e32 v125, 31, v124
	v_ashrrev_i32_e32 v123, 31, v122
	v_ashrrev_i32_e32 v121, 31, v120
	v_ashrrev_i32_e32 v119, 31, v118
	v_ashrrev_i32_e32 v117, 31, v116
	v_ashrrev_i32_e32 v115, 31, v114
	v_readlane_b32 s89, v248, 15
	s_add_i32 s82, s82, s89
	s_add_i32 s33, s33, s76
	v_mad_i64_i32 v[4:5], s[0:1], v126, s77, v[108:109]
	v_lshl_add_u64 v[4:5], v[4:5], 0, s[84:85]
	v_lshl_add_u64 v[4:5], v[4:5], 0, v[110:111]
	v_add_co_u32_e64 v26, s[0:1], s78, v4
	s_nop 1
	v_addc_co_u32_e64 v27, s[0:1], 0, v5, s[0:1]
	global_load_dwordx4 v[32:35], v[26:27], off offset:2048 nt
	v_mad_i64_i32 v[6:7], s[0:1], v124, s77, v[108:109]
	v_lshl_add_u64 v[6:7], v[6:7], 0, s[84:85]
	v_lshl_add_u64 v[6:7], v[6:7], 0, v[110:111]
	v_add_co_u32_e64 v26, s[0:1], s78, v6
	s_nop 1
	v_addc_co_u32_e64 v27, s[0:1], 0, v7, s[0:1]
	global_load_dwordx4 v[36:39], v[26:27], off offset:2048 nt
	v_mad_i64_i32 v[8:9], s[0:1], v122, s77, v[108:109]
	v_lshl_add_u64 v[8:9], v[8:9], 0, s[84:85]
	v_lshl_add_u64 v[8:9], v[8:9], 0, v[110:111]
	v_add_co_u32_e64 v26, s[0:1], s78, v8
	s_nop 1
	v_addc_co_u32_e64 v27, s[0:1], 0, v9, s[0:1]
	global_load_dwordx4 v[40:43], v[26:27], off offset:2048 nt
	v_mad_i64_i32 v[10:11], s[0:1], v120, s77, v[108:109]
	v_lshl_add_u64 v[10:11], v[10:11], 0, s[84:85]
	v_lshl_add_u64 v[10:11], v[10:11], 0, v[110:111]
	v_add_co_u32_e64 v26, s[0:1], s78, v10
	s_nop 1
	v_addc_co_u32_e64 v27, s[0:1], 0, v11, s[0:1]
	global_load_dwordx4 v[44:47], v[26:27], off offset:2048 nt
	v_mad_i64_i32 v[12:13], s[0:1], v118, s77, v[108:109]
	v_lshl_add_u64 v[12:13], v[12:13], 0, s[84:85]
	v_lshl_add_u64 v[12:13], v[12:13], 0, v[110:111]
	v_add_co_u32_e64 v26, s[0:1], s78, v12
	s_nop 1
	v_addc_co_u32_e64 v27, s[0:1], 0, v13, s[0:1]
	global_load_dwordx4 v[48:51], v[26:27], off offset:2048 nt
	v_mad_i64_i32 v[14:15], s[0:1], v116, s77, v[108:109]
	v_lshl_add_u64 v[14:15], v[14:15], 0, s[84:85]
	v_lshl_add_u64 v[14:15], v[14:15], 0, v[110:111]
	v_add_co_u32_e64 v26, s[0:1], s78, v14
	s_nop 1
	v_addc_co_u32_e64 v27, s[0:1], 0, v15, s[0:1]
	global_load_dwordx4 v[52:55], v[26:27], off offset:2048 nt
	v_mad_i64_i32 v[16:17], s[0:1], v114, s77, v[108:109]
	v_lshl_add_u64 v[16:17], v[16:17], 0, s[84:85]
	v_lshl_add_u64 v[16:17], v[16:17], 0, v[110:111]
	v_add_co_u32_e64 v26, s[0:1], s78, v16
	s_nop 1
	v_addc_co_u32_e64 v27, s[0:1], 0, v17, s[0:1]
	global_load_dwordx4 v[56:59], v[26:27], off offset:2048 nt
	s_lshl_b32 s0, s83, 7
	v_or_b32_e32 v113, s0, v1
	v_lshl_add_u64 v[18:19], s[74:75], 2, v[102:103]
	global_load_dwordx4 v[18:21], v[18:19], off
	v_lshlrev_b32_e32 v100, 9, v113
	v_lshl_add_u64 v[22:23], v[104:105], 0, v[100:101]
	global_load_dwordx4 v[60:63], v[22:23], off
	v_or_b32_e32 v22, s0, v130
	v_lshlrev_b32_e32 v100, 9, v22
	v_lshl_add_u64 v[22:23], v[104:105], 0, v[100:101]
	global_load_dwordx4 v[64:67], v[22:23], off
	v_or_b32_e32 v22, s0, v131
	v_lshlrev_b32_e32 v100, 9, v22
	v_lshl_add_u64 v[22:23], v[104:105], 0, v[100:101]
	global_load_dwordx4 v[68:71], v[22:23], off
	v_or_b32_e32 v22, s0, v132
	v_lshlrev_b32_e32 v100, 9, v22
	v_lshl_add_u64 v[22:23], v[104:105], 0, v[100:101]
	global_load_dwordx4 v[72:75], v[22:23], off
	v_or_b32_e32 v22, s0, v133
	v_lshlrev_b32_e32 v100, 9, v22
	v_lshl_add_u64 v[22:23], v[104:105], 0, v[100:101]
	global_load_dwordx4 v[76:79], v[22:23], off
	v_or_b32_e32 v22, s0, v134
	v_lshlrev_b32_e32 v100, 9, v22
	v_lshl_add_u64 v[22:23], v[104:105], 0, v[100:101]
	global_load_dwordx4 v[80:83], v[22:23], off
	v_or_b32_e32 v22, s0, v135
	v_lshlrev_b32_e32 v100, 9, v22
	v_lshl_add_u64 v[22:23], v[104:105], 0, v[100:101]
	global_load_dwordx4 v[84:87], v[22:23], off
	v_or_b32_e32 v22, s0, v136
	v_lshlrev_b32_e32 v100, 9, v22
	v_lshl_add_u64 v[22:23], v[104:105], 0, v[100:101]
	global_load_dwordx4 v[88:91], v[22:23], off
	s_waitcnt vmcnt(16)
	ds_write_b128 v139, v[28:31]
	s_waitcnt vmcnt(15)
	ds_write_b128 v140, v[32:35]
	s_waitcnt vmcnt(14)
	ds_write_b128 v141, v[36:39]
	s_waitcnt vmcnt(13)
	ds_write_b128 v142, v[40:43]
	s_waitcnt vmcnt(12)
	ds_write_b128 v143, v[44:47]
	s_waitcnt vmcnt(11)
	ds_write_b128 v144, v[48:51]
	s_waitcnt vmcnt(10)
	ds_write_b128 v145, v[52:55]
	s_waitcnt vmcnt(9)
	ds_write_b128 v146, v[56:59]
	s_waitcnt vmcnt(7)
	v_mul_f32_e32 v22, v18, v60
	v_mul_f32_e32 v23, v19, v61
	v_cndmask_b32_e64 v22, v22, 0, s[70:71]
	v_cndmask_b32_e64 v23, 0, v23, s[4:5]
	v_cvt_pk_bf16_f32 v22, v22, v23
	v_mul_f32_e32 v23, v20, v62
	v_cndmask_b32_e64 v23, v23, 0, s[6:7]
	v_mul_f32_e32 v24, v21, v63
	v_cndmask_b32_e64 v24, v24, 0, s[86:87]
	v_cvt_pk_bf16_f32 v23, v23, v24
	ds_write_b64 v147, v[22:23]
	s_waitcnt vmcnt(6)
	v_mul_f32_e32 v22, v18, v64
	v_mul_f32_e32 v23, v19, v65
	v_cndmask_b32_e64 v22, v22, 0, s[90:91]
	v_cndmask_b32_e64 v23, 0, v23, s[92:93]
	v_cvt_pk_bf16_f32 v22, v22, v23
	v_mul_f32_e32 v23, v20, v66
	v_cndmask_b32_e64 v23, v23, 0, s[94:95]
	v_mul_f32_e32 v24, v21, v67
	v_cndmask_b32_e64 v24, v24, 0, s[96:97]
	v_cvt_pk_bf16_f32 v23, v23, v24
	ds_write_b64 v147, v[22:23] offset:4352
	s_waitcnt vmcnt(5)
; #define GAS __attribute__((address_space(1)))
; #define LAS __attribute__((address_space(3)))
; __device__ __forceinline__ unsigned pk2(float lo, float hi) { return pg8::cvt_pk_bf16(lo, hi); }
; __device__ __forceinline__ void sgu_unit(Frame& F, int unit) {
;     ...
;       for (int i = 0; i < 8; ++i) { const int t_ = rs_ + 16 * i; const f32x4 wv = *(const GAS f32x4*)(F.sgw + ((size_t)(g * GMC + t_)) * GMC + 4 * q_);
;           const int sb = 4 * q_; v2u o;
;           o.x = pk2(sb + 0 <= t_ ? wv.x * q.x : 0.f, sb + 1 <= t_ ? wv.y * q.y : 0.f); o.y = pk2(sb + 2 <= t_ ? wv.z * q.z : 0.f, sb + 3 <= t_ ? wv.w * q.w : 0.f);
;           *(LAS v2u*)(L + SG_WOFF + t_ * SG_STR + 8 * q_) = o; } }
;     __syncthreads();
;     v4u uu[8];
; #pragma unroll
;     for (int i = 0; i < 8; ++i) uu[i] = *(const GAS v4u*)(F.PROJ + (size_t)(r0 + rs_ + 16 * i) * PNP + PGU + c0 + 8 * q_);
;     f32x16 acc[4];
; #pragma unroll
;     for (int tb = 0; tb < 4; ++tb)
; #pragma unroll
;         for (int r = 0; r < 16; ++r) acc[tb][r] = 0.f;
;     const LAS unsigned char* xb = L + hi * 8 * 512 + 2 * (32 * w + l31);
;     const LAS unsigned char* wa = L + SG_WOFF + l31 * SG_STR + hi * 16;
; #pragma unroll
;     for (int ks = 0; ks < 8; ++ks) {
;         v4u xw;
; #pragma unroll
;         for (int j = 0; j < 4; ++j) { const unsigned lo = *(const LAS unsigned short*)(xb + (16 * ks + 2 * j) * 512), hh = *(const LAS unsigned short*)(xb + (16 * ks + 2 * j + 1) * 512); xw[j] = lo | (hh << 16); }
;         const bf16x8 xf = __builtin_bit_cast(bf16x8, xw);
; #pragma unroll
;         for (int tb = 0; tb < 4; ++tb) if (ks < 2 * (tb + 1)) { const bf16x8 wf = *(const LAS bf16x8*)(wa + tb * 32 * SG_STR + ks * 32); acc[tb] = __builtin_amdgcn_mfma_f32_32x32x16_bf16(wf, xf, acc[tb], 0, 0, 0); } }
	v_mul_f32_e32 v22, v18, v68
	v_mul_f32_e32 v23, v19, v69
	v_cndmask_b32_e64 v22, v22, 0, vcc
	v_cndmask_b32_e64 v23, 0, v23, s[2:3]
	v_cvt_pk_bf16_f32 v22, v22, v23
	v_mul_f32_e32 v23, v20, v70
	v_cndmask_b32_e64 v23, v23, 0, s[20:21]
	v_mul_f32_e32 v24, v21, v71
	v_cndmask_b32_e64 v24, v24, 0, s[22:23]
	v_cvt_pk_bf16_f32 v23, v23, v24
	ds_write_b64 v147, v[22:23] offset:8704
	s_waitcnt vmcnt(4)
	v_mul_f32_e32 v22, v18, v72
	v_mul_f32_e32 v23, v19, v73
	v_cndmask_b32_e64 v22, v22, 0, s[24:25]
	v_cndmask_b32_e64 v23, 0, v23, s[26:27]
	v_cvt_pk_bf16_f32 v22, v22, v23
	v_mul_f32_e32 v23, v20, v74
	v_cndmask_b32_e64 v23, v23, 0, s[28:29]
	v_mul_f32_e32 v24, v21, v75
	v_cndmask_b32_e64 v24, v24, 0, s[30:31]
	v_cvt_pk_bf16_f32 v23, v23, v24
	ds_write_b64 v147, v[22:23] offset:13056
	s_waitcnt vmcnt(3)
	v_mul_f32_e32 v22, v18, v76
	v_mul_f32_e32 v23, v19, v77
	v_cndmask_b32_e64 v22, v22, 0, s[34:35]
	v_cndmask_b32_e64 v23, 0, v23, s[36:37]
	v_cvt_pk_bf16_f32 v22, v22, v23
	v_mul_f32_e32 v23, v20, v78
	v_cndmask_b32_e64 v23, v23, 0, s[38:39]
	v_mul_f32_e32 v24, v21, v79
	v_cndmask_b32_e64 v24, v24, 0, s[40:41]
	v_cvt_pk_bf16_f32 v23, v23, v24
	ds_write_b64 v147, v[22:23] offset:17408
	s_waitcnt vmcnt(2)
	v_mul_f32_e32 v22, v18, v80
	v_mul_f32_e32 v23, v19, v81
	v_cndmask_b32_e64 v22, v22, 0, s[42:43]
	v_cndmask_b32_e64 v23, 0, v23, s[66:67]
	v_cvt_pk_bf16_f32 v22, v22, v23
	v_mul_f32_e32 v23, v20, v82
	v_cndmask_b32_e64 v23, v23, 0, s[46:47]
	v_mul_f32_e32 v24, v21, v83
	v_cndmask_b32_e64 v24, v24, 0, s[48:49]
	v_cvt_pk_bf16_f32 v23, v23, v24
	ds_write_b64 v147, v[22:23] offset:21760
	s_waitcnt vmcnt(1)
	v_mul_f32_e32 v22, v18, v84
	v_mul_f32_e32 v23, v19, v85
	v_cndmask_b32_e64 v22, v22, 0, s[50:51]
	v_cndmask_b32_e64 v23, 0, v23, s[52:53]
	v_cvt_pk_bf16_f32 v22, v22, v23
	v_mul_f32_e32 v23, v20, v86
	v_cndmask_b32_e64 v23, v23, 0, s[54:55]
	v_mul_f32_e32 v24, v21, v87
	v_cndmask_b32_e64 v24, v24, 0, s[56:57]
	v_cvt_pk_bf16_f32 v23, v23, v24
	ds_write_b64 v147, v[22:23] offset:26112
	s_waitcnt vmcnt(0)
	v_add_co_u32_e64 v2, s[0:1], s79, v2
	v_mul_f32_e32 v18, v18, v88
	v_mul_f32_e32 v19, v19, v89
	v_cndmask_b32_e64 v18, v18, 0, s[58:59]
	v_cndmask_b32_e64 v19, 0, v19, s[60:61]
	v_cvt_pk_bf16_f32 v18, v18, v19
	v_mul_f32_e32 v19, v20, v90
	v_cndmask_b32_e64 v19, v19, 0, s[62:63]
	v_mul_f32_e32 v20, v21, v91
	v_addc_co_u32_e64 v3, s[0:1], 0, v3, s[0:1]
	v_cndmask_b32_e64 v20, v20, 0, s[64:65]
	v_cvt_pk_bf16_f32 v19, v19, v20
	ds_write_b64 v147, v[18:19] offset:30464
	s_waitcnt lgkmcnt(0)
	s_barrier
	global_load_dwordx4 v[94:97], v[2:3], off offset:2048 nt
	v_add_co_u32_e64 v2, s[0:1], s79, v4
	s_nop 1
	v_addc_co_u32_e64 v3, s[0:1], 0, v5, s[0:1]
	global_load_dwordx4 v[90:93], v[2:3], off offset:2048 nt
	v_add_co_u32_e64 v2, s[0:1], s79, v6
	s_nop 1
	v_addc_co_u32_e64 v3, s[0:1], 0, v7, s[0:1]
	global_load_dwordx4 v[86:89], v[2:3], off offset:2048 nt
	v_add_co_u32_e64 v2, s[0:1], s79, v8
	s_nop 1
	v_addc_co_u32_e64 v3, s[0:1], 0, v9, s[0:1]
	global_load_dwordx4 v[82:85], v[2:3], off offset:2048 nt
	v_add_co_u32_e64 v2, s[0:1], s79, v10
	s_nop 1
	v_addc_co_u32_e64 v3, s[0:1], 0, v11, s[0:1]
	global_load_dwordx4 v[78:81], v[2:3], off offset:2048 nt
	v_add_co_u32_e64 v2, s[0:1], s79, v12
	s_nop 1
	v_addc_co_u32_e64 v3, s[0:1], 0, v13, s[0:1]
	global_load_dwordx4 v[74:77], v[2:3], off offset:2048 nt
	v_add_co_u32_e64 v2, s[0:1], s79, v14
	s_nop 1
	v_addc_co_u32_e64 v3, s[0:1], 0, v15, s[0:1]
	global_load_dwordx4 v[70:73], v[2:3], off offset:2048 nt
	v_add_co_u32_e64 v2, s[0:1], s79, v16
	s_nop 1
	v_addc_co_u32_e64 v3, s[0:1], 0, v17, s[0:1]
	global_load_dwordx4 v[66:69], v[2:3], off offset:2048 nt
	ds_read_u16 v2, v137
	ds_read_u16 v3, v137 offset:512
	s_lshl_b32 s0, s83, 10
	s_mov_b32 s1, s73
	s_cmpk_gt_i32 s82, 0x1ff
	s_waitcnt lgkmcnt(0)
	v_lshl_or_b32 v2, v3, 16, v2
	ds_read_u16 v3, v137 offset:1024
	ds_read_u16 v4, v137 offset:1536
	s_waitcnt lgkmcnt(0)
	v_lshl_or_b32 v3, v4, 16, v3
	ds_read_u16 v4, v137 offset:2048
	ds_read_u16 v5, v137 offset:2560
	s_waitcnt lgkmcnt(0)
	v_lshl_or_b32 v4, v5, 16, v4
	ds_read_u16 v5, v137 offset:3072
	ds_read_u16 v6, v137 offset:3584
	s_waitcnt lgkmcnt(0)
	v_lshl_or_b32 v5, v6, 16, v5
	ds_read_b128 v[6:9], v148
	ds_read_b128 v[150:153], v148 offset:32
	s_waitcnt lgkmcnt(1)
	v_mfma_f32_32x32x16_bf16 v[50:65], v[6:9], v[2:5], 0
	ds_read_b128 v[6:9], v148 offset:8704
	s_waitcnt lgkmcnt(0)
	v_mfma_f32_32x32x16_bf16 v[34:49], v[6:9], v[2:5], 0
	ds_read_b128 v[6:9], v148 offset:17408
	s_waitcnt lgkmcnt(0)
	v_mfma_f32_32x32x16_bf16 v[18:33], v[6:9], v[2:5], 0
	ds_read_b128 v[6:9], v148 offset:26112
	ds_read_u16 v100, v137 offset:8192
	ds_read_u16 v154, v137 offset:8704
	s_waitcnt lgkmcnt(0)
	v_lshl_or_b32 v154, v154, 16, v100
	ds_read_u16 v100, v137 offset:9216
	ds_read_u16 v155, v137 offset:9728
	v_mfma_f32_32x32x16_bf16 v[2:17], v[6:9], v[2:5], 0
	s_waitcnt lgkmcnt(0)
	v_lshl_or_b32 v155, v155, 16, v100
	ds_read_u16 v100, v137 offset:10240
	ds_read_u16 v156, v137 offset:10752
	s_waitcnt lgkmcnt(0)
	v_lshl_or_b32 v156, v156, 16, v100
	ds_read_u16 v100, v137 offset:11264
	ds_read_u16 v157, v137 offset:11776
	s_waitcnt lgkmcnt(0)
	v_lshl_or_b32 v157, v157, 16, v100
	s_nop 1
	v_mfma_f32_32x32x16_bf16 v[50:65], v[150:153], v[154:157], v[50:65]
	ds_read_b128 v[150:153], v148 offset:8736
	s_waitcnt lgkmcnt(0)
	v_mfma_f32_32x32x16_bf16 v[34:49], v[150:153], v[154:157], v[34:49]
	ds_read_b128 v[150:153], v148 offset:17440
	s_waitcnt lgkmcnt(0)
	v_mfma_f32_32x32x16_bf16 v[18:33], v[150:153], v[154:157], v[18:33]
	ds_read_b128 v[150:153], v148 offset:26144
	s_waitcnt lgkmcnt(0)
; #define LAS __attribute__((address_space(3)))
; __device__ __forceinline__ void sgu_unit(Frame& F, int unit) {
;     ...
; #pragma unroll
;     for (int ks = 0; ks < 8; ++ks) {
;         v4u xw;
; #pragma unroll
;         for (int j = 0; j < 4; ++j) { const unsigned lo = *(const LAS unsigned short*)(xb + (16 * ks + 2 * j) * 512), hh = *(const LAS unsigned short*)(xb + (16 * ks + 2 * j + 1) * 512); xw[j] = lo | (hh << 16); }
;         const bf16x8 xf = __builtin_bit_cast(bf16x8, xw);
; #pragma unroll
;         for (int tb = 0; tb < 4; ++tb) if (ks < 2 * (tb + 1)) { const bf16x8 wf = *(const LAS bf16x8*)(wa + tb * 32 * SG_STR + ks * 32); acc[tb] = __builtin_amdgcn_mfma_f32_32x32x16_bf16(wf, xf, acc[tb], 0, 0, 0); } }
	v_mfma_f32_32x32x16_bf16 v[2:17], v[150:153], v[154:157], v[2:17]
	ds_read_u16 v100, v137 offset:16384
	ds_read_u16 v150, v137 offset:16896
	s_waitcnt lgkmcnt(0)
	v_lshl_or_b32 v150, v150, 16, v100
	ds_read_u16 v100, v137 offset:17408
	ds_read_u16 v151, v137 offset:17920
	s_waitcnt lgkmcnt(0)
	v_lshl_or_b32 v151, v151, 16, v100
	ds_read_u16 v100, v137 offset:18432
	ds_read_u16 v152, v137 offset:18944
	s_waitcnt lgkmcnt(0)
	v_lshl_or_b32 v152, v152, 16, v100
	ds_read_u16 v100, v137 offset:19456
	ds_read_u16 v153, v137 offset:19968
	ds_read_b128 v[154:157], v148 offset:8768
	s_waitcnt lgkmcnt(1)
	v_lshl_or_b32 v153, v153, 16, v100
	s_waitcnt lgkmcnt(0)
	s_nop 0
	v_mfma_f32_32x32x16_bf16 v[34:49], v[154:157], v[150:153], v[34:49]
	ds_read_b128 v[154:157], v148 offset:17472
	s_waitcnt lgkmcnt(0)
	v_mfma_f32_32x32x16_bf16 v[18:33], v[154:157], v[150:153], v[18:33]
	ds_read_b128 v[154:157], v148 offset:26176
	s_waitcnt lgkmcnt(0)
	v_mfma_f32_32x32x16_bf16 v[2:17], v[154:157], v[150:153], v[2:17]
	ds_read_u16 v100, v137 offset:24576
	ds_read_u16 v150, v137 offset:25088
	s_waitcnt lgkmcnt(0)
	v_lshl_or_b32 v150, v150, 16, v100
	ds_read_u16 v100, v137 offset:25600
	ds_read_u16 v151, v137 offset:26112
	s_waitcnt lgkmcnt(0)
	v_lshl_or_b32 v151, v151, 16, v100
	ds_read_u16 v100, v137 offset:26624
	ds_read_u16 v152, v137 offset:27136
	s_waitcnt lgkmcnt(0)
	v_lshl_or_b32 v152, v152, 16, v100
	ds_read_u16 v100, v137 offset:27648
	ds_read_u16 v153, v137 offset:28160
	ds_read_b128 v[154:157], v148 offset:8800
	s_waitcnt lgkmcnt(1)
	v_lshl_or_b32 v153, v153, 16, v100
	s_waitcnt lgkmcnt(0)
	s_nop 0
	v_mfma_f32_32x32x16_bf16 v[34:49], v[154:157], v[150:153], v[34:49]
	ds_read_b128 v[154:157], v148 offset:17504
	s_waitcnt lgkmcnt(0)
	v_mfma_f32_32x32x16_bf16 v[18:33], v[154:157], v[150:153], v[18:33]
	ds_read_b128 v[154:157], v148 offset:26208
	s_waitcnt lgkmcnt(0)
	v_mfma_f32_32x32x16_bf16 v[2:17], v[154:157], v[150:153], v[2:17]
	ds_read_u16 v100, v137 offset:32768
	ds_read_u16 v150, v137 offset:33280
	s_waitcnt lgkmcnt(0)
	v_lshl_or_b32 v150, v150, 16, v100
	ds_read_u16 v100, v137 offset:33792
	ds_read_u16 v151, v137 offset:34304
	s_waitcnt lgkmcnt(0)
	v_lshl_or_b32 v151, v151, 16, v100
	ds_read_u16 v100, v137 offset:34816
	ds_read_u16 v152, v137 offset:35328
	s_waitcnt lgkmcnt(0)
	v_lshl_or_b32 v152, v152, 16, v100
	ds_read_u16 v100, v137 offset:35840
	ds_read_u16 v153, v137 offset:36352
	ds_read_b128 v[154:157], v148 offset:17536
	s_waitcnt lgkmcnt(1)
	v_lshl_or_b32 v153, v153, 16, v100
	s_waitcnt lgkmcnt(0)
	s_nop 0
	v_mfma_f32_32x32x16_bf16 v[18:33], v[154:157], v[150:153], v[18:33]
	ds_read_b128 v[154:157], v148 offset:26240
	s_waitcnt lgkmcnt(0)
	v_mfma_f32_32x32x16_bf16 v[2:17], v[154:157], v[150:153], v[2:17]
	ds_read_u16 v100, v137 offset:40960
	ds_read_u16 v150, v137 offset:41472
	s_waitcnt lgkmcnt(0)
	v_lshl_or_b32 v150, v150, 16, v100
	ds_read_u16 v100, v137 offset:41984
	ds_read_u16 v151, v137 offset:42496
	s_waitcnt lgkmcnt(0)
	v_lshl_or_b32 v151, v151, 16, v100
	ds_read_u16 v100, v137 offset:43008
	ds_read_u16 v152, v137 offset:43520
	s_waitcnt lgkmcnt(0)
	v_lshl_or_b32 v152, v152, 16, v100
	ds_read_u16 v100, v137 offset:44032
	ds_read_u16 v153, v137 offset:44544
	ds_read_b128 v[154:157], v148 offset:17568
	s_waitcnt lgkmcnt(1)
	v_lshl_or_b32 v153, v153, 16, v100
	s_waitcnt lgkmcnt(0)
	s_nop 0
	v_mfma_f32_32x32x16_bf16 v[18:33], v[154:157], v[150:153], v[18:33]
	ds_read_b128 v[154:157], v148 offset:26272
	s_waitcnt lgkmcnt(0)
	v_mfma_f32_32x32x16_bf16 v[2:17], v[154:157], v[150:153], v[2:17]
	ds_read_u16 v100, v137 offset:49152
	ds_read_u16 v150, v137 offset:49664
	s_waitcnt lgkmcnt(0)
	v_lshl_or_b32 v150, v150, 16, v100
	ds_read_u16 v100, v137 offset:50176
	ds_read_u16 v151, v137 offset:50688
	s_waitcnt lgkmcnt(0)
	v_lshl_or_b32 v151, v151, 16, v100
	ds_read_u16 v100, v137 offset:51200
	ds_read_u16 v152, v137 offset:51712
	s_waitcnt lgkmcnt(0)
	v_lshl_or_b32 v152, v152, 16, v100
	ds_read_u16 v100, v137 offset:52224
	ds_read_u16 v153, v137 offset:52736
	ds_read_b128 v[154:157], v148 offset:26304
	s_waitcnt lgkmcnt(1)
	v_lshl_or_b32 v153, v153, 16, v100
	s_waitcnt lgkmcnt(0)
	s_nop 0
	v_mfma_f32_32x32x16_bf16 v[2:17], v[154:157], v[150:153], v[2:17]
	ds_read_u16 v100, v137 offset:57344
	ds_read_u16 v150, v137 offset:57856
	s_waitcnt lgkmcnt(0)
	v_lshl_or_b32 v150, v150, 16, v100
	ds_read_u16 v100, v137 offset:58368
	ds_read_u16 v151, v137 offset:58880
	s_waitcnt lgkmcnt(0)
	v_lshl_or_b32 v151, v151, 16, v100
	ds_read_u16 v100, v137 offset:59392
	ds_read_u16 v152, v137 offset:59904
	s_waitcnt lgkmcnt(0)
	v_lshl_or_b32 v152, v152, 16, v100
	ds_read_u16 v100, v137 offset:60416
	ds_read_u16 v153, v137 offset:60928
	ds_read_b128 v[154:157], v148 offset:26336
	s_waitcnt lgkmcnt(0)
	s_barrier
; #define GAS __attribute__((address_space(1)))
; #define LAS __attribute__((address_space(3)))
; #define LDS_WAIT() asm volatile("s_waitcnt lgkmcnt(0)" ::: "memory")
; __device__ __forceinline__ unsigned f2bf(float f) { unsigned u = __builtin_bit_cast(unsigned, f); return (u + 0x7fffu + ((u >> 16) & 1u)) >> 16; }
; __device__ __forceinline__ void sgu_unit(Frame& F, int unit) {
;     ...
;     LDS_WAIT(); __builtin_amdgcn_s_barrier(); asm volatile("" ::: "memory");
;     { const int cl = 32 * w + l31;
; #pragma unroll
;       for (int tb = 0; tb < 4; ++tb)
; #pragma unroll
;           for (int r = 0; r < 16; ++r) { const int t = 32 * tb + (r & 3) + 8 * (r >> 2) + 4 * hi; *(LAS unsigned short*)(L + t * 512 + 2 * cl) = (unsigned short)f2bf(acc[tb][r]); } }
;     const f32x4 g0 = *(const GAS f32x4*)(F.sgg + c0 + 8 * q_), g1 = *(const GAS f32x4*)(F.sgg + c0 + 8 * q_ + 4);
;     LDS_WAIT(); __builtin_amdgcn_s_barrier(); asm volatile("" ::: "memory");
	s_waitcnt lgkmcnt(1)
	v_lshl_or_b32 v153, v153, 16, v100
	v_bfe_u32 v100, v50, 16, 1
	v_add3_u32 v50, v50, v100, s80
	ds_write_b16_d16_hi v138, v50
	v_bfe_u32 v50, v51, 16, 1
	v_add3_u32 v50, v51, v50, s80
	ds_write_b16_d16_hi v138, v50 offset:512
	v_bfe_u32 v50, v52, 16, 1
	v_add3_u32 v50, v52, v50, s80
	ds_write_b16_d16_hi v138, v50 offset:1024
	v_bfe_u32 v50, v53, 16, 1
	v_add3_u32 v50, v53, v50, s80
	ds_write_b16_d16_hi v138, v50 offset:1536
	v_bfe_u32 v50, v54, 16, 1
	v_add3_u32 v50, v54, v50, s80
	ds_write_b16_d16_hi v138, v50 offset:4096
	v_bfe_u32 v50, v55, 16, 1
	v_add3_u32 v50, v55, v50, s80
	ds_write_b16_d16_hi v138, v50 offset:4608
	v_bfe_u32 v50, v56, 16, 1
	v_add3_u32 v50, v56, v50, s80
	ds_write_b16_d16_hi v138, v50 offset:5120
	v_bfe_u32 v50, v57, 16, 1
	v_add3_u32 v50, v57, v50, s80
	ds_write_b16_d16_hi v138, v50 offset:5632
	v_bfe_u32 v50, v58, 16, 1
	v_add3_u32 v50, v58, v50, s80
	ds_write_b16_d16_hi v138, v50 offset:8192
	v_bfe_u32 v50, v59, 16, 1
	v_add3_u32 v50, v59, v50, s80
	ds_write_b16_d16_hi v138, v50 offset:8704
	v_bfe_u32 v50, v60, 16, 1
	v_add3_u32 v50, v60, v50, s80
	ds_write_b16_d16_hi v138, v50 offset:9216
	v_bfe_u32 v50, v61, 16, 1
	v_add3_u32 v50, v61, v50, s80
	ds_write_b16_d16_hi v138, v50 offset:9728
	v_bfe_u32 v50, v62, 16, 1
	v_add3_u32 v50, v62, v50, s80
	ds_write_b16_d16_hi v138, v50 offset:12288
	v_bfe_u32 v50, v63, 16, 1
	v_add3_u32 v50, v63, v50, s80
	ds_write_b16_d16_hi v138, v50 offset:12800
	v_bfe_u32 v50, v64, 16, 1
	v_add3_u32 v50, v64, v50, s80
	ds_write_b16_d16_hi v138, v50 offset:13312
	v_bfe_u32 v50, v65, 16, 1
	v_add3_u32 v50, v65, v50, s80
	ds_write_b16_d16_hi v138, v50 offset:13824
	v_bfe_u32 v50, v34, 16, 1
	v_add3_u32 v34, v34, v50, s80
	ds_write_b16_d16_hi v138, v34 offset:16384
	v_bfe_u32 v34, v35, 16, 1
	v_add3_u32 v34, v35, v34, s80
	ds_write_b16_d16_hi v138, v34 offset:16896
	v_bfe_u32 v34, v36, 16, 1
	v_add3_u32 v34, v36, v34, s80
	ds_write_b16_d16_hi v138, v34 offset:17408
	v_bfe_u32 v34, v37, 16, 1
	v_add3_u32 v34, v37, v34, s80
	ds_write_b16_d16_hi v138, v34 offset:17920
	v_bfe_u32 v34, v38, 16, 1
	v_add3_u32 v34, v38, v34, s80
	ds_write_b16_d16_hi v138, v34 offset:20480
	v_bfe_u32 v34, v39, 16, 1
	v_add3_u32 v34, v39, v34, s80
	ds_write_b16_d16_hi v138, v34 offset:20992
	v_bfe_u32 v34, v40, 16, 1
	v_add3_u32 v34, v40, v34, s80
	ds_write_b16_d16_hi v138, v34 offset:21504
	v_bfe_u32 v34, v41, 16, 1
	v_add3_u32 v34, v41, v34, s80
	ds_write_b16_d16_hi v138, v34 offset:22016
	v_bfe_u32 v34, v42, 16, 1
	v_add3_u32 v34, v42, v34, s80
	ds_write_b16_d16_hi v138, v34 offset:24576
	v_bfe_u32 v34, v43, 16, 1
	v_add3_u32 v34, v43, v34, s80
	ds_write_b16_d16_hi v138, v34 offset:25088
	v_bfe_u32 v34, v44, 16, 1
	v_add3_u32 v34, v44, v34, s80
	ds_write_b16_d16_hi v138, v34 offset:25600
	v_bfe_u32 v34, v45, 16, 1
	v_add3_u32 v34, v45, v34, s80
	ds_write_b16_d16_hi v138, v34 offset:26112
	v_bfe_u32 v34, v46, 16, 1
	v_add3_u32 v34, v46, v34, s80
	ds_write_b16_d16_hi v138, v34 offset:28672
	v_bfe_u32 v34, v47, 16, 1
	v_add3_u32 v34, v47, v34, s80
	ds_write_b16_d16_hi v138, v34 offset:29184
	v_bfe_u32 v34, v48, 16, 1
	v_add3_u32 v34, v48, v34, s80
	ds_write_b16_d16_hi v138, v34 offset:29696
	v_bfe_u32 v34, v49, 16, 1
	v_add3_u32 v34, v49, v34, s80
	ds_write_b16_d16_hi v138, v34 offset:30208
	v_bfe_u32 v34, v18, 16, 1
	v_add3_u32 v18, v18, v34, s80
	ds_write_b16_d16_hi v138, v18 offset:32768
	v_bfe_u32 v18, v19, 16, 1
	v_add3_u32 v18, v19, v18, s80
	ds_write_b16_d16_hi v138, v18 offset:33280
	v_bfe_u32 v18, v20, 16, 1
	v_add3_u32 v18, v20, v18, s80
	ds_write_b16_d16_hi v138, v18 offset:33792
	v_bfe_u32 v18, v21, 16, 1
	v_add3_u32 v18, v21, v18, s80
	ds_write_b16_d16_hi v138, v18 offset:34304
	v_bfe_u32 v18, v22, 16, 1
	v_add3_u32 v18, v22, v18, s80
	ds_write_b16_d16_hi v138, v18 offset:36864
	v_bfe_u32 v18, v23, 16, 1
	v_add3_u32 v18, v23, v18, s80
	ds_write_b16_d16_hi v138, v18 offset:37376
	v_bfe_u32 v18, v24, 16, 1
	v_add3_u32 v18, v24, v18, s80
	ds_write_b16_d16_hi v138, v18 offset:37888
	v_bfe_u32 v18, v25, 16, 1
	v_add3_u32 v18, v25, v18, s80
	ds_write_b16_d16_hi v138, v18 offset:38400
	v_bfe_u32 v18, v26, 16, 1
	v_add3_u32 v18, v26, v18, s80
	ds_write_b16_d16_hi v138, v18 offset:40960
	v_bfe_u32 v18, v27, 16, 1
	v_add3_u32 v18, v27, v18, s80
	ds_write_b16_d16_hi v138, v18 offset:41472
	v_bfe_u32 v18, v28, 16, 1
	v_add3_u32 v18, v28, v18, s80
	ds_write_b16_d16_hi v138, v18 offset:41984
	v_bfe_u32 v18, v29, 16, 1
	v_add3_u32 v18, v29, v18, s80
	s_waitcnt lgkmcnt(14)
	v_mfma_f32_32x32x16_bf16 v[2:17], v[154:157], v[150:153], v[2:17]
	ds_write_b16_d16_hi v138, v18 offset:42496
	v_bfe_u32 v18, v30, 16, 1
	v_add3_u32 v18, v30, v18, s80
	ds_write_b16_d16_hi v138, v18 offset:45056
	v_bfe_u32 v18, v31, 16, 1
	v_add3_u32 v18, v31, v18, s80
	ds_write_b16_d16_hi v138, v18 offset:45568
	v_bfe_u32 v18, v32, 16, 1
	v_add3_u32 v18, v32, v18, s80
	ds_write_b16_d16_hi v138, v18 offset:46080
	v_bfe_u32 v18, v33, 16, 1
	v_add3_u32 v18, v33, v18, s80
	ds_write_b16_d16_hi v138, v18 offset:46592
	v_bfe_u32 v18, v2, 16, 1
	v_add3_u32 v2, v2, v18, s80
	ds_write_b16_d16_hi v138, v2 offset:49152
	v_bfe_u32 v2, v3, 16, 1
	v_add3_u32 v2, v3, v2, s80
	ds_write_b16_d16_hi v138, v2 offset:49664
	v_bfe_u32 v2, v4, 16, 1
	v_add3_u32 v2, v4, v2, s80
	ds_write_b16_d16_hi v138, v2 offset:50176
	v_bfe_u32 v2, v5, 16, 1
	v_add3_u32 v2, v5, v2, s80
	ds_write_b16_d16_hi v138, v2 offset:50688
	v_bfe_u32 v2, v6, 16, 1
	v_add3_u32 v2, v6, v2, s80
	ds_write_b16_d16_hi v138, v2 offset:53248
	v_bfe_u32 v2, v7, 16, 1
	v_add3_u32 v2, v7, v2, s80
	ds_write_b16_d16_hi v138, v2 offset:53760
	v_bfe_u32 v2, v8, 16, 1
	v_add3_u32 v2, v8, v2, s80
	ds_write_b16_d16_hi v138, v2 offset:54272
	v_bfe_u32 v2, v9, 16, 1
	v_add3_u32 v2, v9, v2, s80
	ds_write_b16_d16_hi v138, v2 offset:54784
	v_bfe_u32 v2, v10, 16, 1
	v_add3_u32 v2, v10, v2, s80
	ds_write_b16_d16_hi v138, v2 offset:57344
	v_bfe_u32 v2, v11, 16, 1
	v_add3_u32 v2, v11, v2, s80
	ds_write_b16_d16_hi v138, v2 offset:57856
	v_bfe_u32 v2, v12, 16, 1
	v_add3_u32 v2, v12, v2, s80
	ds_write_b16_d16_hi v138, v2 offset:58368
	v_bfe_u32 v2, v13, 16, 1
	v_add3_u32 v2, v13, v2, s80
	ds_write_b16_d16_hi v138, v2 offset:58880
	v_bfe_u32 v2, v14, 16, 1
	v_add3_u32 v2, v14, v2, s80
	ds_write_b16_d16_hi v138, v2 offset:61440
	v_bfe_u32 v2, v15, 16, 1
	v_add3_u32 v2, v15, v2, s80
	ds_write_b16_d16_hi v138, v2 offset:61952
	v_bfe_u32 v2, v16, 16, 1
	v_add3_u32 v2, v16, v2, s80
	ds_write_b16_d16_hi v138, v2 offset:62464
	v_bfe_u32 v2, v17, 16, 1
	v_add3_u32 v2, v17, v2, s80
	ds_write_b16_d16_hi v138, v2 offset:62976
	v_lshl_add_u64 v[6:7], v[106:107], 0, s[0:1]
	global_load_dwordx4 v[2:5], v[6:7], off offset:16
	s_nop 0
	global_load_dwordx4 v[6:9], v[6:7], off
	s_waitcnt lgkmcnt(0)
	s_barrier
; #define GAS __attribute__((address_space(1)))
; #define LAS __attribute__((address_space(3)))
; __device__ __forceinline__ void sgu_unit(Frame& F, int unit) {
;     ...
; #pragma unroll
;     for (int i = 0; i < 8; ++i) { const v4u fw = *(const LAS v4u*)(L + (rs_ + 16 * i) * 512 + q_ * 16); const float bb = F.sgb[g * GMC + rs_ + 16 * i]; v2u o;
;         o.x = pk4_fp8(S_YB * bflo(uu[i].x) * (bflo(fw.x) * g0.x + bb), S_YB * bfhi(uu[i].x) * (bfhi(fw.x) * g0.y + bb), S_YB * bflo(uu[i].y) * (bflo(fw.y) * g0.z + bb), S_YB * bfhi(uu[i].y) * (bfhi(fw.y) * g0.w + bb));
;         o.y = pk4_fp8(S_YB * bflo(uu[i].z) * (bflo(fw.z) * g1.x + bb), S_YB * bfhi(uu[i].z) * (bfhi(fw.z) * g1.y + bb), S_YB * bflo(uu[i].w) * (bflo(fw.w) * g1.z + bb), S_YB * bfhi(uu[i].w) * (bfhi(fw.w) * g1.w + bb));
;         *(GAS v2u*)((unsigned char*)F.YA + (size_t)(r0 + rs_ + 16 * i) * (2 * ATTW) + ATTW + c0 + 8 * q_) = o; }
	v_lshlrev_b32_e32 v20, 2, v113
	global_load_dword v19, v20, s[8:9]
	ds_read_b128 v[10:13], v139
	s_waitcnt vmcnt(10)
	v_lshlrev_b32_e32 v14, 16, v94
	v_lshlrev_b32_e32 v16, 16, v95
	v_lshlrev_b32_e32 v22, 16, v97
	s_waitcnt lgkmcnt(0)
	v_lshlrev_b32_e32 v15, 16, v10
	v_lshlrev_b32_e32 v17, 16, v11
	v_and_b32_e32 v11, 0xffff0000, v11
	v_lshlrev_b32_e32 v23, 16, v13
	v_and_b32_e32 v13, 0xffff0000, v13
	s_waitcnt vmcnt(1)
	v_mov_b32_e32 v113, v6
	v_pk_mul_f32 v[14:15], v[112:113], v[14:15]
	s_waitcnt vmcnt(0)
	v_add_f32_e32 v6, v19, v15
	v_mul_f32_e32 v18, v14, v6
	v_and_b32_e32 v15, 0xffff0000, v10
	v_and_b32_e32 v14, 0xffff0000, v94
	v_mov_b32_e32 v6, v112
	v_pk_mul_f32 v[14:15], v[6:7], v[14:15]
	s_nop 0
	v_add_f32_e32 v10, v19, v15
	v_mul_f32_e32 v21, v14, v10
	v_mov_b32_e32 v14, v112
	v_mov_b32_e32 v15, v8
	v_pk_mul_f32 v[16:17], v[14:15], v[16:17]
	v_and_b32_e32 v10, 0xffff0000, v95
	v_add_f32_e32 v8, v19, v17
	v_mul_f32_e32 v16, v16, v8
	v_mov_b32_e32 v8, v112
	v_pk_mul_f32 v[10:11], v[8:9], v[10:11]
	v_med3_f32 v17, v21, s81, v149
	v_add_f32_e32 v11, v19, v11
	v_mul_f32_e32 v10, v10, v11
	v_med3_f32 v11, v18, s81, v149
	v_mov_b32_e32 v18, v101
	v_cvt_pk_fp8_f32 v18, v11, v17
	v_med3_f32 v11, v16, s81, v149
	v_med3_f32 v10, v10, s81, v149
	v_lshlrev_b32_e32 v16, 16, v96
	v_cvt_pk_fp8_f32 v18, v11, v10 op_sel:[0,0,1]
	v_lshlrev_b32_e32 v17, 16, v12
	v_mov_b32_e32 v10, v112
	v_mov_b32_e32 v11, v2
	v_pk_mul_f32 v[16:17], v[10:11], v[16:17]
	s_nop 0
	v_add_f32_e32 v2, v19, v17
	v_mul_f32_e32 v21, v16, v2
	v_and_b32_e32 v17, 0xffff0000, v12
	v_and_b32_e32 v16, 0xffff0000, v96
	v_mov_b32_e32 v2, v112
	v_pk_mul_f32 v[16:17], v[2:3], v[16:17]
	s_nop 0
	v_add_f32_e32 v12, v19, v17
	v_mul_f32_e32 v24, v16, v12
	v_mov_b32_e32 v16, v112
	v_mov_b32_e32 v17, v4
	v_pk_mul_f32 v[22:23], v[16:17], v[22:23]
	v_and_b32_e32 v12, 0xffff0000, v97
	v_add_f32_e32 v4, v19, v23
	v_mul_f32_e32 v22, v22, v4
	v_mov_b32_e32 v4, v112
	v_pk_mul_f32 v[12:13], v[4:5], v[12:13]
	s_nop 0
	v_add_f32_e32 v13, v19, v13
	v_mul_f32_e32 v12, v12, v13
	v_med3_f32 v13, v21, s81, v149
	v_med3_f32 v21, v24, s81, v149
	v_mov_b32_e32 v19, v101
	v_cvt_pk_fp8_f32 v19, v13, v21
	v_med3_f32 v13, v22, s81, v149
	v_med3_f32 v12, v12, s81, v149
	ds_read_b128 v[22:25], v140
	v_cvt_pk_fp8_f32 v19, v13, v12 op_sel:[0,0,1]
	v_lshlrev_b64 v[12:13], 12, v[128:129]
	v_lshl_add_u64 v[12:13], s[68:69], 0, v[12:13]
	v_lshl_add_u64 v[12:13], v[12:13], 0, s[72:73]
	v_lshl_add_u64 v[12:13], v[12:13], 0, v[98:99]
	global_store_dwordx2 v[12:13], v[18:19], off offset:2048
	global_load_dword v21, v20, s[8:9] offset:64
	v_lshlrev_b32_e32 v12, 16, v90
	s_waitcnt lgkmcnt(0)
	v_lshlrev_b32_e32 v13, 16, v22
	v_pk_mul_f32 v[12:13], v[112:113], v[12:13]
	s_waitcnt vmcnt(0)
	v_add_f32_e32 v13, v21, v13
	v_mul_f32_e32 v18, v12, v13
	v_and_b32_e32 v13, 0xffff0000, v22
	v_and_b32_e32 v12, 0xffff0000, v90
	v_pk_mul_f32 v[12:13], v[6:7], v[12:13]
	v_med3_f32 v18, v18, s81, v149
	v_add_f32_e32 v13, v21, v13
	v_mul_f32_e32 v19, v12, v13
	v_lshlrev_b32_e32 v12, 16, v91
	v_lshlrev_b32_e32 v13, 16, v23
	v_pk_mul_f32 v[12:13], v[14:15], v[12:13]
	v_med3_f32 v19, v19, s81, v149
	v_add_f32_e32 v13, v21, v13
	v_mul_f32_e32 v22, v12, v13
	v_and_b32_e32 v13, 0xffff0000, v23
	v_and_b32_e32 v12, 0xffff0000, v91
	v_pk_mul_f32 v[12:13], v[8:9], v[12:13]
	s_nop 0
	v_add_f32_e32 v13, v21, v13
	v_mul_f32_e32 v13, v12, v13
	v_mov_b32_e32 v12, v101
	v_cvt_pk_fp8_f32 v12, v18, v19
	v_med3_f32 v18, v22, s81, v149
	v_med3_f32 v13, v13, s81, v149
	v_lshlrev_b32_e32 v19, 16, v24
	v_cvt_pk_fp8_f32 v12, v18, v13 op_sel:[0,0,1]
	v_lshlrev_b32_e32 v18, 16, v92
	v_pk_mul_f32 v[18:19], v[10:11], v[18:19]
	s_nop 0
	v_add_f32_e32 v13, v21, v19
	v_mul_f32_e32 v13, v18, v13
	v_and_b32_e32 v19, 0xffff0000, v24
	v_and_b32_e32 v18, 0xffff0000, v92
	v_pk_mul_f32 v[18:19], v[2:3], v[18:19]
	s_nop 0
	v_add_f32_e32 v19, v21, v19
	v_mul_f32_e32 v22, v18, v19
	v_lshlrev_b32_e32 v18, 16, v93
	v_lshlrev_b32_e32 v19, 16, v25
	v_pk_mul_f32 v[18:19], v[16:17], v[18:19]
	s_nop 0
	v_add_f32_e32 v19, v21, v19
	v_mul_f32_e32 v23, v18, v19
	v_and_b32_e32 v19, 0xffff0000, v25
	v_and_b32_e32 v18, 0xffff0000, v93
	v_pk_mul_f32 v[18:19], v[4:5], v[18:19]
	s_nop 0
	v_add_f32_e32 v19, v21, v19
	v_mul_f32_e32 v18, v18, v19
	v_med3_f32 v19, v13, s81, v149
	v_med3_f32 v21, v22, s81, v149
	v_mov_b32_e32 v13, v101
	v_cvt_pk_fp8_f32 v13, v19, v21
	v_med3_f32 v19, v23, s81, v149
	v_med3_f32 v18, v18, s81, v149
	ds_read_b128 v[22:25], v141
	v_cvt_pk_fp8_f32 v13, v19, v18 op_sel:[0,0,1]
	v_lshlrev_b64 v[18:19], 12, v[126:127]
	v_lshl_add_u64 v[18:19], s[68:69], 0, v[18:19]
	v_lshl_add_u64 v[18:19], v[18:19], 0, s[72:73]
	v_lshl_add_u64 v[18:19], v[18:19], 0, v[98:99]
	global_store_dwordx2 v[18:19], v[12:13], off offset:2048
	global_load_dword v21, v20, s[8:9] offset:128
	v_lshlrev_b32_e32 v12, 16, v86
	s_waitcnt lgkmcnt(0)
	v_lshlrev_b32_e32 v13, 16, v22
	v_pk_mul_f32 v[12:13], v[112:113], v[12:13]
	s_waitcnt vmcnt(0)
; #define GAS __attribute__((address_space(1)))
; #define LAS __attribute__((address_space(3)))
; __device__ __forceinline__ void sgu_unit(Frame& F, int unit) {
;     ...
; #pragma unroll
;     for (int i = 0; i < 8; ++i) { const v4u fw = *(const LAS v4u*)(L + (rs_ + 16 * i) * 512 + q_ * 16); const float bb = F.sgb[g * GMC + rs_ + 16 * i]; v2u o;
;         o.x = pk4_fp8(S_YB * bflo(uu[i].x) * (bflo(fw.x) * g0.x + bb), S_YB * bfhi(uu[i].x) * (bfhi(fw.x) * g0.y + bb), S_YB * bflo(uu[i].y) * (bflo(fw.y) * g0.z + bb), S_YB * bfhi(uu[i].y) * (bfhi(fw.y) * g0.w + bb));
;         o.y = pk4_fp8(S_YB * bflo(uu[i].z) * (bflo(fw.z) * g1.x + bb), S_YB * bfhi(uu[i].z) * (bfhi(fw.z) * g1.y + bb), S_YB * bflo(uu[i].w) * (bflo(fw.w) * g1.z + bb), S_YB * bfhi(uu[i].w) * (bfhi(fw.w) * g1.w + bb));
;         *(GAS v2u*)((unsigned char*)F.YA + (size_t)(r0 + rs_ + 16 * i) * (2 * ATTW) + ATTW + c0 + 8 * q_) = o; }
	v_add_f32_e32 v13, v21, v13
	v_mul_f32_e32 v18, v12, v13
	v_and_b32_e32 v13, 0xffff0000, v22
	v_and_b32_e32 v12, 0xffff0000, v86
	v_pk_mul_f32 v[12:13], v[6:7], v[12:13]
	v_med3_f32 v18, v18, s81, v149
	v_add_f32_e32 v13, v21, v13
	v_mul_f32_e32 v19, v12, v13
	v_lshlrev_b32_e32 v12, 16, v87
	v_lshlrev_b32_e32 v13, 16, v23
	v_pk_mul_f32 v[12:13], v[14:15], v[12:13]
	v_med3_f32 v19, v19, s81, v149
	v_add_f32_e32 v13, v21, v13
	v_mul_f32_e32 v22, v12, v13
	v_and_b32_e32 v13, 0xffff0000, v23
	v_and_b32_e32 v12, 0xffff0000, v87
	v_pk_mul_f32 v[12:13], v[8:9], v[12:13]
	s_nop 0
	v_add_f32_e32 v13, v21, v13
	v_mul_f32_e32 v13, v12, v13
	v_mov_b32_e32 v12, v101
	v_cvt_pk_fp8_f32 v12, v18, v19
	v_med3_f32 v18, v22, s81, v149
	v_med3_f32 v13, v13, s81, v149
	v_lshlrev_b32_e32 v19, 16, v24
	v_cvt_pk_fp8_f32 v12, v18, v13 op_sel:[0,0,1]
	v_lshlrev_b32_e32 v18, 16, v88
	v_pk_mul_f32 v[18:19], v[10:11], v[18:19]
	s_nop 0
	v_add_f32_e32 v13, v21, v19
	v_mul_f32_e32 v13, v18, v13
	v_and_b32_e32 v19, 0xffff0000, v24
	v_and_b32_e32 v18, 0xffff0000, v88
	v_pk_mul_f32 v[18:19], v[2:3], v[18:19]
	s_nop 0
	v_add_f32_e32 v19, v21, v19
	v_mul_f32_e32 v22, v18, v19
	v_lshlrev_b32_e32 v18, 16, v89
	v_lshlrev_b32_e32 v19, 16, v25
	v_pk_mul_f32 v[18:19], v[16:17], v[18:19]
	s_nop 0
	v_add_f32_e32 v19, v21, v19
	v_mul_f32_e32 v23, v18, v19
	v_and_b32_e32 v19, 0xffff0000, v25
	v_and_b32_e32 v18, 0xffff0000, v89
	v_pk_mul_f32 v[18:19], v[4:5], v[18:19]
	s_nop 0
	v_add_f32_e32 v19, v21, v19
	v_mul_f32_e32 v18, v18, v19
	v_med3_f32 v19, v13, s81, v149
	v_med3_f32 v21, v22, s81, v149
	v_mov_b32_e32 v13, v101
	v_cvt_pk_fp8_f32 v13, v19, v21
	v_med3_f32 v19, v23, s81, v149
	v_med3_f32 v18, v18, s81, v149
	ds_read_b128 v[22:25], v142
	v_cvt_pk_fp8_f32 v13, v19, v18 op_sel:[0,0,1]
	v_lshlrev_b64 v[18:19], 12, v[124:125]
	v_lshl_add_u64 v[18:19], s[68:69], 0, v[18:19]
	v_lshl_add_u64 v[18:19], v[18:19], 0, s[72:73]
	v_lshl_add_u64 v[18:19], v[18:19], 0, v[98:99]
	global_store_dwordx2 v[18:19], v[12:13], off offset:2048
	global_load_dword v21, v20, s[8:9] offset:192
	v_lshlrev_b32_e32 v12, 16, v82
	s_waitcnt lgkmcnt(0)
	v_lshlrev_b32_e32 v13, 16, v22
	v_pk_mul_f32 v[12:13], v[112:113], v[12:13]
	s_waitcnt vmcnt(0)
	v_add_f32_e32 v13, v21, v13
	v_mul_f32_e32 v18, v12, v13
	v_and_b32_e32 v13, 0xffff0000, v22
	v_and_b32_e32 v12, 0xffff0000, v82
	v_pk_mul_f32 v[12:13], v[6:7], v[12:13]
	v_med3_f32 v18, v18, s81, v149
	v_add_f32_e32 v13, v21, v13
	v_mul_f32_e32 v19, v12, v13
	v_lshlrev_b32_e32 v12, 16, v83
	v_lshlrev_b32_e32 v13, 16, v23
	v_pk_mul_f32 v[12:13], v[14:15], v[12:13]
	v_med3_f32 v19, v19, s81, v149
	v_add_f32_e32 v13, v21, v13
	v_mul_f32_e32 v22, v12, v13
	v_and_b32_e32 v13, 0xffff0000, v23
	v_and_b32_e32 v12, 0xffff0000, v83
	v_pk_mul_f32 v[12:13], v[8:9], v[12:13]
	s_nop 0
	v_add_f32_e32 v13, v21, v13
	v_mul_f32_e32 v13, v12, v13
	v_mov_b32_e32 v12, v101
	v_cvt_pk_fp8_f32 v12, v18, v19
	v_med3_f32 v18, v22, s81, v149
	v_med3_f32 v13, v13, s81, v149
	v_lshlrev_b32_e32 v19, 16, v24
	v_cvt_pk_fp8_f32 v12, v18, v13 op_sel:[0,0,1]
	v_lshlrev_b32_e32 v18, 16, v84
	v_pk_mul_f32 v[18:19], v[10:11], v[18:19]
	s_nop 0
	v_add_f32_e32 v13, v21, v19
	v_mul_f32_e32 v13, v18, v13
	v_and_b32_e32 v19, 0xffff0000, v24
	v_and_b32_e32 v18, 0xffff0000, v84
	v_pk_mul_f32 v[18:19], v[2:3], v[18:19]
	s_nop 0
	v_add_f32_e32 v19, v21, v19
	v_mul_f32_e32 v22, v18, v19
	v_lshlrev_b32_e32 v18, 16, v85
	v_lshlrev_b32_e32 v19, 16, v25
	v_pk_mul_f32 v[18:19], v[16:17], v[18:19]
	s_nop 0
	v_add_f32_e32 v19, v21, v19
	v_mul_f32_e32 v23, v18, v19
	v_and_b32_e32 v19, 0xffff0000, v25
	v_and_b32_e32 v18, 0xffff0000, v85
	v_pk_mul_f32 v[18:19], v[4:5], v[18:19]
	s_nop 0
	v_add_f32_e32 v19, v21, v19
	v_mul_f32_e32 v18, v18, v19
	v_med3_f32 v19, v13, s81, v149
	v_med3_f32 v21, v22, s81, v149
	v_mov_b32_e32 v13, v101
	v_cvt_pk_fp8_f32 v13, v19, v21
	v_med3_f32 v19, v23, s81, v149
	v_med3_f32 v18, v18, s81, v149
	ds_read_b128 v[22:25], v143
	v_cvt_pk_fp8_f32 v13, v19, v18 op_sel:[0,0,1]
	v_lshlrev_b64 v[18:19], 12, v[122:123]
	v_lshl_add_u64 v[18:19], s[68:69], 0, v[18:19]
	v_lshl_add_u64 v[18:19], v[18:19], 0, s[72:73]
	v_lshl_add_u64 v[18:19], v[18:19], 0, v[98:99]
	global_store_dwordx2 v[18:19], v[12:13], off offset:2048
	global_load_dword v21, v20, s[8:9] offset:256
	v_lshlrev_b32_e32 v12, 16, v78
	s_waitcnt lgkmcnt(0)
	v_lshlrev_b32_e32 v13, 16, v22
	v_pk_mul_f32 v[12:13], v[112:113], v[12:13]
	s_waitcnt vmcnt(0)
	v_add_f32_e32 v13, v21, v13
	v_mul_f32_e32 v18, v12, v13
	v_and_b32_e32 v13, 0xffff0000, v22
	v_and_b32_e32 v12, 0xffff0000, v78
	v_pk_mul_f32 v[12:13], v[6:7], v[12:13]
	v_med3_f32 v18, v18, s81, v149
	v_add_f32_e32 v13, v21, v13
	v_mul_f32_e32 v19, v12, v13
	v_lshlrev_b32_e32 v12, 16, v79
	v_lshlrev_b32_e32 v13, 16, v23
	v_pk_mul_f32 v[12:13], v[14:15], v[12:13]
	v_med3_f32 v19, v19, s81, v149
	v_add_f32_e32 v13, v21, v13
	v_mul_f32_e32 v22, v12, v13
	v_and_b32_e32 v13, 0xffff0000, v23
	v_and_b32_e32 v12, 0xffff0000, v79
	v_pk_mul_f32 v[12:13], v[8:9], v[12:13]
	s_nop 0
	v_add_f32_e32 v13, v21, v13
	v_mul_f32_e32 v13, v12, v13
	v_mov_b32_e32 v12, v101
	v_cvt_pk_fp8_f32 v12, v18, v19
	v_med3_f32 v18, v22, s81, v149
	v_med3_f32 v13, v13, s81, v149
	v_lshlrev_b32_e32 v19, 16, v24
	v_cvt_pk_fp8_f32 v12, v18, v13 op_sel:[0,0,1]
	v_lshlrev_b32_e32 v18, 16, v80
	v_pk_mul_f32 v[18:19], v[10:11], v[18:19]
	s_nop 0
	v_add_f32_e32 v13, v21, v19
	v_mul_f32_e32 v13, v18, v13
	v_and_b32_e32 v19, 0xffff0000, v24
	v_and_b32_e32 v18, 0xffff0000, v80
	v_pk_mul_f32 v[18:19], v[2:3], v[18:19]
	s_nop 0
	v_add_f32_e32 v19, v21, v19
	v_mul_f32_e32 v22, v18, v19
	v_lshlrev_b32_e32 v18, 16, v81
	v_lshlrev_b32_e32 v19, 16, v25
	v_pk_mul_f32 v[18:19], v[16:17], v[18:19]
	s_nop 0
	v_add_f32_e32 v19, v21, v19
	v_mul_f32_e32 v23, v18, v19
	v_and_b32_e32 v19, 0xffff0000, v25
	v_and_b32_e32 v18, 0xffff0000, v81
	v_pk_mul_f32 v[18:19], v[4:5], v[18:19]
	s_nop 0
	v_add_f32_e32 v19, v21, v19
	v_mul_f32_e32 v18, v18, v19
	v_med3_f32 v19, v13, s81, v149
	v_med3_f32 v21, v22, s81, v149
	v_mov_b32_e32 v13, v101
	v_cvt_pk_fp8_f32 v13, v19, v21
	v_med3_f32 v19, v23, s81, v149
	v_med3_f32 v18, v18, s81, v149
	ds_read_b128 v[22:25], v144
	v_cvt_pk_fp8_f32 v13, v19, v18 op_sel:[0,0,1]
	v_lshlrev_b64 v[18:19], 12, v[120:121]
	v_lshl_add_u64 v[18:19], s[68:69], 0, v[18:19]
	v_lshl_add_u64 v[18:19], v[18:19], 0, s[72:73]
	v_lshl_add_u64 v[18:19], v[18:19], 0, v[98:99]
	global_store_dwordx2 v[18:19], v[12:13], off offset:2048
	global_load_dword v21, v20, s[8:9] offset:320
	v_lshlrev_b32_e32 v12, 16, v74
	s_waitcnt lgkmcnt(0)
; #define GAS __attribute__((address_space(1)))
; #define LAS __attribute__((address_space(3)))
; __device__ __forceinline__ void sgu_unit(Frame& F, int unit) {
;     ...
; #pragma unroll
;     for (int i = 0; i < 8; ++i) { const v4u fw = *(const LAS v4u*)(L + (rs_ + 16 * i) * 512 + q_ * 16); const float bb = F.sgb[g * GMC + rs_ + 16 * i]; v2u o;
;         o.x = pk4_fp8(S_YB * bflo(uu[i].x) * (bflo(fw.x) * g0.x + bb), S_YB * bfhi(uu[i].x) * (bfhi(fw.x) * g0.y + bb), S_YB * bflo(uu[i].y) * (bflo(fw.y) * g0.z + bb), S_YB * bfhi(uu[i].y) * (bfhi(fw.y) * g0.w + bb));
;         o.y = pk4_fp8(S_YB * bflo(uu[i].z) * (bflo(fw.z) * g1.x + bb), S_YB * bfhi(uu[i].z) * (bfhi(fw.z) * g1.y + bb), S_YB * bflo(uu[i].w) * (bflo(fw.w) * g1.z + bb), S_YB * bfhi(uu[i].w) * (bfhi(fw.w) * g1.w + bb));
;         *(GAS v2u*)((unsigned char*)F.YA + (size_t)(r0 + rs_ + 16 * i) * (2 * ATTW) + ATTW + c0 + 8 * q_) = o; }
; __global__ void __launch_bounds__(NWAVES * 64, 2) mega_fwd(Args args) {
;     ...
;         for (int u = blockIdx.x; u < 512; u += F.G) sgu_unit(F, u);
	v_lshlrev_b32_e32 v13, 16, v22
	v_pk_mul_f32 v[12:13], v[112:113], v[12:13]
	s_waitcnt vmcnt(0)
	v_add_f32_e32 v13, v21, v13
	v_mul_f32_e32 v18, v12, v13
	v_and_b32_e32 v13, 0xffff0000, v22
	v_and_b32_e32 v12, 0xffff0000, v74
	v_pk_mul_f32 v[12:13], v[6:7], v[12:13]
	v_med3_f32 v18, v18, s81, v149
	v_add_f32_e32 v13, v21, v13
	v_mul_f32_e32 v19, v12, v13
	v_lshlrev_b32_e32 v12, 16, v75
	v_lshlrev_b32_e32 v13, 16, v23
	v_pk_mul_f32 v[12:13], v[14:15], v[12:13]
	v_med3_f32 v19, v19, s81, v149
	v_add_f32_e32 v13, v21, v13
	v_mul_f32_e32 v22, v12, v13
	v_and_b32_e32 v13, 0xffff0000, v23
	v_and_b32_e32 v12, 0xffff0000, v75
	v_pk_mul_f32 v[12:13], v[8:9], v[12:13]
	s_nop 0
	v_add_f32_e32 v13, v21, v13
	v_mul_f32_e32 v13, v12, v13
	v_mov_b32_e32 v12, v101
	v_cvt_pk_fp8_f32 v12, v18, v19
	v_med3_f32 v18, v22, s81, v149
	v_med3_f32 v13, v13, s81, v149
	v_lshlrev_b32_e32 v19, 16, v24
	v_cvt_pk_fp8_f32 v12, v18, v13 op_sel:[0,0,1]
	v_lshlrev_b32_e32 v18, 16, v76
	v_pk_mul_f32 v[18:19], v[10:11], v[18:19]
	s_nop 0
	v_add_f32_e32 v13, v21, v19
	v_mul_f32_e32 v13, v18, v13
	v_and_b32_e32 v19, 0xffff0000, v24
	v_and_b32_e32 v18, 0xffff0000, v76
	v_pk_mul_f32 v[18:19], v[2:3], v[18:19]
	s_nop 0
	v_add_f32_e32 v19, v21, v19
	v_mul_f32_e32 v22, v18, v19
	v_lshlrev_b32_e32 v18, 16, v77
	v_lshlrev_b32_e32 v19, 16, v25
	v_pk_mul_f32 v[18:19], v[16:17], v[18:19]
	s_nop 0
	v_add_f32_e32 v19, v21, v19
	v_mul_f32_e32 v23, v18, v19
	v_and_b32_e32 v19, 0xffff0000, v25
	v_and_b32_e32 v18, 0xffff0000, v77
	v_pk_mul_f32 v[18:19], v[4:5], v[18:19]
	s_nop 0
	v_add_f32_e32 v19, v21, v19
	v_mul_f32_e32 v18, v18, v19
	v_med3_f32 v19, v13, s81, v149
	v_med3_f32 v21, v22, s81, v149
	v_mov_b32_e32 v13, v101
	v_cvt_pk_fp8_f32 v13, v19, v21
	v_med3_f32 v19, v23, s81, v149
	v_med3_f32 v18, v18, s81, v149
	ds_read_b128 v[22:25], v145
	v_cvt_pk_fp8_f32 v13, v19, v18 op_sel:[0,0,1]
	v_lshlrev_b64 v[18:19], 12, v[118:119]
	v_lshl_add_u64 v[18:19], s[68:69], 0, v[18:19]
	v_lshl_add_u64 v[18:19], v[18:19], 0, s[72:73]
	v_lshl_add_u64 v[18:19], v[18:19], 0, v[98:99]
	global_store_dwordx2 v[18:19], v[12:13], off offset:2048
	global_load_dword v21, v20, s[8:9] offset:384
	v_lshlrev_b32_e32 v12, 16, v70
	s_waitcnt lgkmcnt(0)
	v_lshlrev_b32_e32 v13, 16, v22
	v_pk_mul_f32 v[12:13], v[112:113], v[12:13]
	s_waitcnt vmcnt(0)
	v_add_f32_e32 v13, v21, v13
	v_mul_f32_e32 v18, v12, v13
	v_and_b32_e32 v13, 0xffff0000, v22
	v_and_b32_e32 v12, 0xffff0000, v70
	v_pk_mul_f32 v[12:13], v[6:7], v[12:13]
	v_med3_f32 v18, v18, s81, v149
	v_add_f32_e32 v13, v21, v13
	v_mul_f32_e32 v19, v12, v13
	v_lshlrev_b32_e32 v12, 16, v71
	v_lshlrev_b32_e32 v13, 16, v23
	v_pk_mul_f32 v[12:13], v[14:15], v[12:13]
	v_med3_f32 v19, v19, s81, v149
	v_add_f32_e32 v13, v21, v13
	v_mul_f32_e32 v22, v12, v13
	v_and_b32_e32 v13, 0xffff0000, v23
	v_and_b32_e32 v12, 0xffff0000, v71
	v_pk_mul_f32 v[12:13], v[8:9], v[12:13]
	s_nop 0
	v_add_f32_e32 v13, v21, v13
	v_mul_f32_e32 v13, v12, v13
	v_mov_b32_e32 v12, v101
	v_cvt_pk_fp8_f32 v12, v18, v19
	v_med3_f32 v18, v22, s81, v149
	v_med3_f32 v13, v13, s81, v149
	v_lshlrev_b32_e32 v19, 16, v24
	v_cvt_pk_fp8_f32 v12, v18, v13 op_sel:[0,0,1]
	v_lshlrev_b32_e32 v18, 16, v72
	v_pk_mul_f32 v[18:19], v[10:11], v[18:19]
	s_nop 0
	v_add_f32_e32 v13, v21, v19
	v_mul_f32_e32 v13, v18, v13
	v_and_b32_e32 v19, 0xffff0000, v24
	v_and_b32_e32 v18, 0xffff0000, v72
	v_pk_mul_f32 v[18:19], v[2:3], v[18:19]
	s_nop 0
	v_add_f32_e32 v19, v21, v19
	v_mul_f32_e32 v22, v18, v19
	v_lshlrev_b32_e32 v18, 16, v73
	v_lshlrev_b32_e32 v19, 16, v25
	v_pk_mul_f32 v[18:19], v[16:17], v[18:19]
	s_nop 0
	v_add_f32_e32 v19, v21, v19
	v_mul_f32_e32 v23, v18, v19
	v_and_b32_e32 v19, 0xffff0000, v25
	v_and_b32_e32 v18, 0xffff0000, v73
	v_pk_mul_f32 v[18:19], v[4:5], v[18:19]
	s_nop 0
	v_add_f32_e32 v19, v21, v19
	v_mul_f32_e32 v18, v18, v19
	v_med3_f32 v19, v13, s81, v149
	v_med3_f32 v21, v22, s81, v149
	v_mov_b32_e32 v13, v101
	v_cvt_pk_fp8_f32 v13, v19, v21
	v_med3_f32 v19, v23, s81, v149
	v_med3_f32 v18, v18, s81, v149
	ds_read_b128 v[22:25], v146
	v_cvt_pk_fp8_f32 v13, v19, v18 op_sel:[0,0,1]
	v_lshlrev_b64 v[18:19], 12, v[116:117]
	v_lshl_add_u64 v[18:19], s[68:69], 0, v[18:19]
	v_lshl_add_u64 v[18:19], v[18:19], 0, s[72:73]
	v_lshl_add_u64 v[18:19], v[18:19], 0, v[98:99]
	global_store_dwordx2 v[18:19], v[12:13], off offset:2048
	global_load_dword v18, v20, s[8:9] offset:448
	v_lshlrev_b32_e32 v12, 16, v66
	s_waitcnt lgkmcnt(0)
	v_lshlrev_b32_e32 v13, 16, v22
	v_pk_mul_f32 v[12:13], v[112:113], v[12:13]
	s_waitcnt vmcnt(0)
	v_add_f32_e32 v13, v18, v13
	v_mul_f32_e32 v19, v12, v13
	v_and_b32_e32 v13, 0xffff0000, v22
	v_and_b32_e32 v12, 0xffff0000, v66
	v_pk_mul_f32 v[6:7], v[6:7], v[12:13]
	s_nop 0
	v_add_f32_e32 v7, v18, v7
	v_mul_f32_e32 v12, v6, v7
	v_lshlrev_b32_e32 v6, 16, v67
	v_lshlrev_b32_e32 v7, 16, v23
	v_pk_mul_f32 v[6:7], v[14:15], v[6:7]
	s_nop 0
	v_add_f32_e32 v7, v18, v7
	v_mul_f32_e32 v13, v6, v7
	v_and_b32_e32 v7, 0xffff0000, v23
	v_and_b32_e32 v6, 0xffff0000, v67
	v_pk_mul_f32 v[6:7], v[8:9], v[6:7]
	v_med3_f32 v8, v19, s81, v149
	v_add_f32_e32 v7, v18, v7
	v_mul_f32_e32 v7, v6, v7
	v_med3_f32 v9, v12, s81, v149
	v_mov_b32_e32 v6, v101
	v_cvt_pk_fp8_f32 v6, v8, v9
	v_med3_f32 v8, v13, s81, v149
	v_med3_f32 v7, v7, s81, v149
	v_lshlrev_b32_e32 v9, 16, v24
	v_cvt_pk_fp8_f32 v6, v8, v7 op_sel:[0,0,1]
	v_lshlrev_b32_e32 v8, 16, v68
	v_pk_mul_f32 v[8:9], v[10:11], v[8:9]
	s_nop 0
	v_add_f32_e32 v7, v18, v9
	v_mul_f32_e32 v7, v8, v7
	v_and_b32_e32 v9, 0xffff0000, v24
	v_and_b32_e32 v8, 0xffff0000, v68
	v_pk_mul_f32 v[2:3], v[2:3], v[8:9]
	s_nop 0
	v_add_f32_e32 v3, v18, v3
	v_mul_f32_e32 v8, v2, v3
	v_lshlrev_b32_e32 v2, 16, v69
	v_lshlrev_b32_e32 v3, 16, v25
	v_pk_mul_f32 v[2:3], v[16:17], v[2:3]
	s_nop 0
	v_add_f32_e32 v3, v18, v3
	v_mul_f32_e32 v9, v2, v3
	v_and_b32_e32 v3, 0xffff0000, v25
	v_and_b32_e32 v2, 0xffff0000, v69
	v_pk_mul_f32 v[2:3], v[4:5], v[2:3]
	v_med3_f32 v4, v8, s81, v149
	v_add_f32_e32 v3, v18, v3
	v_mul_f32_e32 v2, v2, v3
	v_med3_f32 v3, v7, s81, v149
	v_mov_b32_e32 v7, v101
	v_cvt_pk_fp8_f32 v7, v3, v4
	v_med3_f32 v3, v9, s81, v149
	v_med3_f32 v2, v2, s81, v149
	v_cvt_pk_fp8_f32 v7, v3, v2 op_sel:[0,0,1]
	v_lshlrev_b64 v[2:3], 12, v[114:115]
	v_lshl_add_u64 v[2:3], s[68:69], 0, v[2:3]
	v_lshl_add_u64 v[2:3], v[2:3], 0, s[72:73]
	v_lshl_add_u64 v[2:3], v[2:3], 0, v[98:99]
	global_store_dwordx2 v[2:3], v[6:7], off offset:2048
	s_cbranch_scc0 .LBB0_1330

; #define MG_LOAD(G_, s_) do { const bf16* q_ = pb + (size_t)(((s_) >> 2) * 128 + ((s_) & 3) * 16) * PNP; G_[0] = *(const GAS v4u*)(q_ + PGA); G_[1] = *(const GAS v4u*)(q_ + PGB); G_[2] = *(const GAS v4u*)(q_ + PGA + 128); G_[3] = *(const GAS v4u*)(q_ + PGB + 128); } while (0)
;     ...
;             if constexpr (Epi::MIDK) { if (t == nt / 2) { if constexpr (ES == 1) asm volatile("s_nop 15\n\ts_nop 15" ::: "memory"); E.mid(acc, cur, wr, wc, fr, fq); } }
;     __device__ __forceinline__ void mid(f32x4 (&acc)[2][2][4][2], const Unit& u, int wr, int wc, int fr, int fq) const {
;         const bf16* pb = P + (size_t)(u.pm * 256 + wr * 64 + fr) * PNP + (u.pn * 256 + wc * 32 + 8 * fq);
;         asm volatile("" : "+v"(pb));
;         v4u A0[4], A1[4];
;     ...
;         MG_LOAD(A0, 0); MG_LOAD(A1, 1); MG_APPLY(A0, 0); MG_LOAD(A0, 2); MG_APPLY(A1, 1); MG_LOAD(A1, 3); MG_APPLY(A0, 2); MG_LOAD(A0, 4); MG_APPLY(A1, 3); MG_LOAD(A1, 5);
;         MG_APPLY(A0, 4); MG_LOAD(A0, 6); MG_APPLY(A1, 5); MG_LOAD(A1, 7); MG_APPLY(A0, 6); MG_APPLY(A1, 7);
.LBB0_1709:
	s_cmpk_lg_i32 s30, 0x800
	s_cbranch_scc1 .LBB0_1708
	v_mov_b64_e32 v[28:29], v[204:205]
	s_nop 15
	s_nop 15
	s_mov_b32 s34, 0x118000
	v_add_co_u32_e32 v2, vcc, 0x4000, v28
	s_nop 1
	v_addc_co_u32_e32 v3, vcc, 0, v29, vcc
	v_add_co_u32_e32 v4, vcc, 0x6000, v28
	global_load_dwordx4 v[158:161], v[2:3], off offset:2048 nt
	s_nop 0
	v_addc_co_u32_e32 v5, vcc, 0, v29, vcc
	global_load_dwordx4 v[162:165], v[4:5], off offset:2048
	global_load_dwordx4 v[18:21], v[2:3], off offset:2304 nt
	global_load_dwordx4 v[22:25], v[4:5], off offset:2304
	v_add_co_u32_e32 v2, vcc, 0x8e000, v28
	s_waitcnt vmcnt(3)
	v_lshlrev_b32_e32 v168, 16, v158
	v_addc_co_u32_e32 v3, vcc, 0, v29, vcc
	global_load_dwordx4 v[10:13], v[2:3], off offset:2048 nt
	v_add_co_u32_e32 v6, vcc, 0x90000, v28
	s_waitcnt vmcnt(3)
	v_lshlrev_b32_e32 v27, 16, v162
	s_nop 0
	v_addc_co_u32_e32 v7, vcc, 0, v29, vcc
	global_load_dwordx4 v[14:17], v[6:7], off offset:2048
	s_nop 0
	global_load_dwordx4 v[2:5], v[2:3], off offset:2304 nt
	s_nop 0
	global_load_dwordx4 v[6:9], v[6:7], off offset:2304
	v_max_f32_e32 v27, v27, v27
	v_max_f32_e32 v27, 0xda24260, v27
	v_rcp_f32_e32 v166, v27
	v_and_b32_e32 v27, 0xffff0000, v162
	v_max_f32_e32 v27, v27, v27
	v_max_f32_e32 v27, 0xda24260, v27
	v_rcp_f32_e32 v167, v27
	v_lshlrev_b32_e32 v27, 16, v163
	v_max_f32_e32 v27, v27, v27
	v_max_f32_e32 v27, 0xda24260, v27
	v_rcp_f32_e32 v162, v27
	v_and_b32_e32 v27, 0xffff0000, v163
	v_max_f32_e32 v27, v27, v27
	v_max_f32_e32 v27, 0xda24260, v27
	v_rcp_f32_e32 v163, v27
	v_and_b32_e32 v169, 0xffff0000, v158
	v_lshlrev_b32_e32 v158, 16, v159
	v_and_b32_e32 v159, 0xffff0000, v159
	v_lshlrev_b32_e32 v27, 16, v164
	v_pk_mul_f32 v[158:159], v[158:159], 0.5 op_sel_hi:[1,0]
	v_max_f32_e32 v27, v27, v27
	v_pk_mul_f32 v[158:159], v[158:159], v[162:163]
	v_max_f32_e32 v27, 0xda24260, v27
	v_pk_mul_f32 v[156:157], v[156:157], v[158:159]
	v_rcp_f32_e32 v158, v27
	v_and_b32_e32 v27, 0xffff0000, v164
	v_max_f32_e32 v27, v27, v27
	v_max_f32_e32 v27, 0xda24260, v27
	v_rcp_f32_e32 v159, v27
	v_lshlrev_b32_e32 v27, 16, v165
	v_lshlrev_b32_e32 v162, 16, v160
	v_and_b32_e32 v163, 0xffff0000, v160
	v_max_f32_e32 v27, v27, v27
	v_pk_mul_f32 v[162:163], v[162:163], 0.5 op_sel_hi:[1,0]
	v_max_f32_e32 v27, 0xda24260, v27
	v_pk_mul_f32 v[158:159], v[162:163], v[158:159]
	v_rcp_f32_e32 v162, v27
	v_and_b32_e32 v27, 0xffff0000, v165
	v_max_f32_e32 v27, v27, v27
	v_max_f32_e32 v27, 0xda24260, v27
	v_rcp_f32_e32 v163, v27
	v_lshlrev_b32_e32 v160, 16, v161
	v_and_b32_e32 v161, 0xffff0000, v161
	v_pk_mul_f32 v[160:161], v[160:161], 0.5 op_sel_hi:[1,0]
	s_waitcnt vmcnt(4)
	v_lshlrev_b32_e32 v27, 16, v22
	v_pk_mul_f32 v[160:161], v[160:161], v[162:163]
	v_and_b32_e32 v22, 0xffff0000, v22
	v_pk_mul_f32 v[152:153], v[152:153], v[160:161]
	v_lshlrev_b32_e32 v160, 16, v18
	v_and_b32_e32 v161, 0xffff0000, v18
	v_lshlrev_b32_e32 v18, 16, v23
	v_max_f32_e32 v22, v22, v22
	v_max_f32_e32 v18, v18, v18
	v_max_f32_e32 v22, 0xda24260, v22
	v_max_f32_e32 v18, 0xda24260, v18
	v_pk_mul_f32 v[150:151], v[150:151], v[158:159]
	v_rcp_f32_e32 v159, v22
	v_rcp_f32_e32 v22, v18
	v_and_b32_e32 v18, 0xffff0000, v23
	v_max_f32_e32 v18, v18, v18
	v_max_f32_e32 v18, 0xda24260, v18
	v_rcp_f32_e32 v23, v18
	v_lshlrev_b32_e32 v18, 16, v19
	v_and_b32_e32 v19, 0xffff0000, v19
	v_pk_mul_f32 v[18:19], v[18:19], 0.5 op_sel_hi:[1,0]
	v_max_f32_e32 v27, v27, v27
	v_pk_mul_f32 v[18:19], v[18:19], v[22:23]
	v_max_f32_e32 v27, 0xda24260, v27
	v_pk_mul_f32 v[148:149], v[148:149], v[18:19]
	v_lshlrev_b32_e32 v18, 16, v24
	v_and_b32_e32 v19, 0xffff0000, v24
	v_max_f32_e32 v18, v18, v18
	v_max_f32_e32 v19, v19, v19
	v_max_f32_e32 v18, 0xda24260, v18
	v_max_f32_e32 v19, 0xda24260, v19
	v_rcp_f32_e32 v18, v18
	v_rcp_f32_e32 v19, v19
	v_rcp_f32_e32 v158, v27
	v_lshlrev_b32_e32 v22, 16, v20
	v_and_b32_e32 v23, 0xffff0000, v20
	v_lshlrev_b32_e32 v20, 16, v25
	s_waitcnt vmcnt(2)
	v_lshlrev_b32_e32 v27, 16, v14
	v_and_b32_e32 v14, 0xffff0000, v14
	v_lshlrev_b32_e32 v164, 16, v10
	v_and_b32_e32 v165, 0xffff0000, v10
	v_lshlrev_b32_e32 v10, 16, v15
	v_max_f32_e32 v20, v20, v20
	v_max_f32_e32 v14, v14, v14
	v_max_f32_e32 v10, v10, v10
	v_pk_mul_f32 v[22:23], v[22:23], 0.5 op_sel_hi:[1,0]
	v_max_f32_e32 v20, 0xda24260, v20
	v_max_f32_e32 v14, 0xda24260, v14
	v_max_f32_e32 v10, 0xda24260, v10
	v_pk_mul_f32 v[18:19], v[22:23], v[18:19]
	v_rcp_f32_e32 v22, v20
	v_and_b32_e32 v20, 0xffff0000, v25
	v_rcp_f32_e32 v163, v14
	v_rcp_f32_e32 v14, v10
	v_and_b32_e32 v10, 0xffff0000, v15
	v_max_f32_e32 v20, v20, v20
	v_max_f32_e32 v10, v10, v10
	v_max_f32_e32 v20, 0xda24260, v20
	v_max_f32_e32 v10, 0xda24260, v10
	v_rcp_f32_e32 v23, v20
	v_rcp_f32_e32 v15, v10
	v_lshlrev_b32_e32 v20, 16, v21
	v_and_b32_e32 v21, 0xffff0000, v21
	v_pk_mul_f32 v[142:143], v[142:143], v[18:19]
	v_add_co_u32_e32 v18, vcc, s34, v28
	v_lshlrev_b32_e32 v10, 16, v11
	v_and_b32_e32 v11, 0xffff0000, v11
	v_pk_mul_f32 v[20:21], v[20:21], 0.5 op_sel_hi:[1,0]
	v_addc_co_u32_e32 v19, vcc, 0, v29, vcc
	s_mov_b32 s34, 0x11a000
	v_pk_mul_f32 v[10:11], v[10:11], 0.5 op_sel_hi:[1,0]
	v_pk_mul_f32 v[168:169], v[168:169], 0.5 op_sel_hi:[1,0]
	v_pk_mul_f32 v[160:161], v[160:161], 0.5 op_sel_hi:[1,0]
	v_pk_mul_f32 v[20:21], v[20:21], v[22:23]
	v_add_co_u32_e32 v22, vcc, s34, v28
	v_pk_mul_f32 v[10:11], v[10:11], v[14:15]
	v_pk_mul_f32 v[166:167], v[168:169], v[166:167]
	v_pk_mul_f32 v[158:159], v[160:161], v[158:159]
	v_addc_co_u32_e32 v23, vcc, 0, v29, vcc
	v_pk_mul_f32 v[140:141], v[140:141], v[10:11]
	v_lshlrev_b32_e32 v10, 16, v16
	v_and_b32_e32 v11, 0xffff0000, v16
	v_pk_mul_f32 v[154:155], v[154:155], v[166:167]
	v_pk_mul_f32 v[146:147], v[146:147], v[158:159]
	v_pk_mul_f32 v[144:145], v[144:145], v[20:21]
	global_load_dwordx4 v[158:161], v[18:19], off offset:2048 nt
	global_load_dwordx4 v[166:169], v[22:23], off offset:2048
	s_nop 0
	global_load_dwordx4 v[18:21], v[18:19], off offset:2304 nt
	s_nop 0
	global_load_dwordx4 v[22:25], v[22:23], off offset:2304
	v_max_f32_e32 v10, v10, v10
	v_max_f32_e32 v11, v11, v11
	v_max_f32_e32 v10, 0xda24260, v10
	v_max_f32_e32 v11, 0xda24260, v11
	v_rcp_f32_e32 v10, v10
	v_rcp_f32_e32 v11, v11
	v_lshlrev_b32_e32 v14, 16, v12
	v_and_b32_e32 v15, 0xffff0000, v12
	v_lshlrev_b32_e32 v12, 16, v17
	v_max_f32_e32 v12, v12, v12
	v_pk_mul_f32 v[14:15], v[14:15], 0.5 op_sel_hi:[1,0]
	v_max_f32_e32 v12, 0xda24260, v12
	v_pk_mul_f32 v[10:11], v[14:15], v[10:11]
	v_rcp_f32_e32 v14, v12
	v_and_b32_e32 v12, 0xffff0000, v17
	v_max_f32_e32 v12, v12, v12
	v_max_f32_e32 v12, 0xda24260, v12
	v_rcp_f32_e32 v15, v12
	v_lshlrev_b32_e32 v12, 16, v13
	v_and_b32_e32 v13, 0xffff0000, v13
	v_pk_mul_f32 v[12:13], v[12:13], 0.5 op_sel_hi:[1,0]
	v_pk_mul_f32 v[134:135], v[134:135], v[10:11]
	v_pk_mul_f32 v[12:13], v[12:13], v[14:15]
	s_waitcnt vmcnt(4)
; #define MG_LOAD(G_, s_) do { const bf16* q_ = pb + (size_t)(((s_) >> 2) * 128 + ((s_) & 3) * 16) * PNP; G_[0] = *(const GAS v4u*)(q_ + PGA); G_[1] = *(const GAS v4u*)(q_ + PGB); G_[2] = *(const GAS v4u*)(q_ + PGA + 128); G_[3] = *(const GAS v4u*)(q_ + PGB + 128); } while (0)
;     __device__ __forceinline__ void mid(f32x4 (&acc)[2][2][4][2], const Unit& u, int wr, int wc, int fr, int fq) const {
;     ...
;         MG_LOAD(A0, 0); MG_LOAD(A1, 1); MG_APPLY(A0, 0); MG_LOAD(A0, 2); MG_APPLY(A1, 1); MG_LOAD(A1, 3); MG_APPLY(A0, 2); MG_LOAD(A0, 4); MG_APPLY(A1, 3); MG_LOAD(A1, 5);
;         MG_APPLY(A0, 4); MG_LOAD(A0, 6); MG_APPLY(A1, 5); MG_LOAD(A1, 7); MG_APPLY(A0, 6); MG_APPLY(A1, 7);
	v_lshlrev_b32_e32 v10, 16, v6
	v_pk_mul_f32 v[136:137], v[136:137], v[12:13]
	v_and_b32_e32 v6, 0xffff0000, v6
	v_lshlrev_b32_e32 v12, 16, v2
	v_and_b32_e32 v13, 0xffff0000, v2
	v_lshlrev_b32_e32 v2, 16, v7
	v_max_f32_e32 v6, v6, v6
	v_max_f32_e32 v2, v2, v2
	v_max_f32_e32 v6, 0xda24260, v6
	v_max_f32_e32 v2, 0xda24260, v2
	v_rcp_f32_e32 v11, v6
	v_rcp_f32_e32 v6, v2
	v_and_b32_e32 v2, 0xffff0000, v7
	v_max_f32_e32 v2, v2, v2
	v_max_f32_e32 v2, 0xda24260, v2
	v_rcp_f32_e32 v7, v2
	v_lshlrev_b32_e32 v2, 16, v3
	v_and_b32_e32 v3, 0xffff0000, v3
	v_pk_mul_f32 v[2:3], v[2:3], 0.5 op_sel_hi:[1,0]
	v_max_f32_e32 v27, v27, v27
	v_pk_mul_f32 v[2:3], v[2:3], v[6:7]
	v_lshlrev_b32_e32 v6, 16, v4
	v_pk_mul_f32 v[132:133], v[132:133], v[2:3]
	v_lshlrev_b32_e32 v2, 16, v8
	v_and_b32_e32 v3, 0xffff0000, v8
	v_max_f32_e32 v2, v2, v2
	v_max_f32_e32 v3, v3, v3
	v_max_f32_e32 v2, 0xda24260, v2
	v_max_f32_e32 v3, 0xda24260, v3
	v_rcp_f32_e32 v2, v2
	v_rcp_f32_e32 v3, v3
	v_and_b32_e32 v7, 0xffff0000, v4
	v_lshlrev_b32_e32 v4, 16, v9
	v_max_f32_e32 v4, v4, v4
	v_pk_mul_f32 v[6:7], v[6:7], 0.5 op_sel_hi:[1,0]
	v_max_f32_e32 v4, 0xda24260, v4
	v_pk_mul_f32 v[2:3], v[6:7], v[2:3]
	v_rcp_f32_e32 v6, v4
	v_and_b32_e32 v4, 0xffff0000, v9
	v_max_f32_e32 v4, v4, v4
	v_max_f32_e32 v10, v10, v10
	v_max_f32_e32 v4, 0xda24260, v4
	v_max_f32_e32 v27, 0xda24260, v27
	v_max_f32_e32 v10, 0xda24260, v10
	v_rcp_f32_e32 v7, v4
	v_rcp_f32_e32 v162, v27
	v_rcp_f32_e32 v10, v10
	s_mov_b32 s34, 0x1a2000
	v_lshlrev_b32_e32 v4, 16, v5
	v_and_b32_e32 v5, 0xffff0000, v5
	v_pk_mul_f32 v[126:127], v[126:127], v[2:3]
	v_add_co_u32_e32 v2, vcc, s34, v28
	v_pk_mul_f32 v[4:5], v[4:5], 0.5 op_sel_hi:[1,0]
	s_nop 0
	v_addc_co_u32_e32 v3, vcc, 0, v29, vcc
	s_mov_b32 s34, 0x1a4000
	v_pk_mul_f32 v[164:165], v[164:165], 0.5 op_sel_hi:[1,0]
	v_pk_mul_f32 v[12:13], v[12:13], 0.5 op_sel_hi:[1,0]
	v_pk_mul_f32 v[4:5], v[4:5], v[6:7]
	v_add_co_u32_e32 v6, vcc, s34, v28
	v_pk_mul_f32 v[162:163], v[164:165], v[162:163]
	v_pk_mul_f32 v[10:11], v[12:13], v[10:11]
	v_addc_co_u32_e32 v7, vcc, 0, v29, vcc
	v_pk_mul_f32 v[138:139], v[138:139], v[162:163]
	v_pk_mul_f32 v[130:131], v[130:131], v[10:11]
	v_pk_mul_f32 v[128:129], v[128:129], v[4:5]
	global_load_dwordx4 v[162:165], v[2:3], off offset:2048 nt
	global_load_dwordx4 v[170:173], v[6:7], off offset:2048
	s_nop 0
	global_load_dwordx4 v[2:5], v[2:3], off offset:2304 nt
	s_nop 0
	global_load_dwordx4 v[10:13], v[6:7], off offset:2304
	s_waitcnt vmcnt(6)
	v_lshlrev_b32_e32 v6, 16, v166
	v_and_b32_e32 v7, 0xffff0000, v166
	v_max_f32_e32 v6, v6, v6
	v_max_f32_e32 v7, v7, v7
	v_max_f32_e32 v6, 0xda24260, v6
	v_max_f32_e32 v7, 0xda24260, v7
	v_rcp_f32_e32 v6, v6
	v_rcp_f32_e32 v7, v7
	v_lshlrev_b32_e32 v8, 16, v158
	v_and_b32_e32 v9, 0xffff0000, v158
	v_pk_mul_f32 v[8:9], v[8:9], 0.5 op_sel_hi:[1,0]
	v_lshlrev_b32_e32 v14, 16, v159
	v_pk_mul_f32 v[6:7], v[8:9], v[6:7]
	v_lshlrev_b32_e32 v8, 16, v167
	v_and_b32_e32 v9, 0xffff0000, v167
	v_max_f32_e32 v8, v8, v8
	v_max_f32_e32 v9, v9, v9
	v_max_f32_e32 v8, 0xda24260, v8
	v_max_f32_e32 v9, 0xda24260, v9
	v_rcp_f32_e32 v8, v8
	v_rcp_f32_e32 v9, v9
	v_pk_mul_f32 v[122:123], v[122:123], v[6:7]
	v_lshlrev_b32_e32 v6, 16, v168
	v_and_b32_e32 v7, 0xffff0000, v168
	v_max_f32_e32 v6, v6, v6
	v_max_f32_e32 v7, v7, v7
	v_and_b32_e32 v15, 0xffff0000, v159
	v_max_f32_e32 v6, 0xda24260, v6
	v_max_f32_e32 v7, 0xda24260, v7
	v_pk_mul_f32 v[14:15], v[14:15], 0.5 op_sel_hi:[1,0]
	v_rcp_f32_e32 v6, v6
	v_rcp_f32_e32 v7, v7
	v_pk_mul_f32 v[8:9], v[14:15], v[8:9]
	v_lshlrev_b32_e32 v14, 16, v161
	v_pk_mul_f32 v[124:125], v[124:125], v[8:9]
	v_lshlrev_b32_e32 v8, 16, v160
	v_and_b32_e32 v9, 0xffff0000, v160
	v_pk_mul_f32 v[8:9], v[8:9], 0.5 op_sel_hi:[1,0]
	v_and_b32_e32 v15, 0xffff0000, v161
	v_pk_mul_f32 v[6:7], v[8:9], v[6:7]
	v_lshlrev_b32_e32 v8, 16, v169
	v_and_b32_e32 v9, 0xffff0000, v169
	v_max_f32_e32 v8, v8, v8
	v_max_f32_e32 v9, v9, v9
	v_max_f32_e32 v8, 0xda24260, v8
	v_max_f32_e32 v9, 0xda24260, v9
	v_rcp_f32_e32 v8, v8
	v_rcp_f32_e32 v9, v9
	v_pk_mul_f32 v[118:119], v[118:119], v[6:7]
	s_waitcnt vmcnt(4)
	v_lshlrev_b32_e32 v6, 16, v22
	v_and_b32_e32 v7, 0xffff0000, v22
	v_max_f32_e32 v6, v6, v6
	v_max_f32_e32 v7, v7, v7
	v_max_f32_e32 v6, 0xda24260, v6
	v_max_f32_e32 v7, 0xda24260, v7
	v_pk_mul_f32 v[14:15], v[14:15], 0.5 op_sel_hi:[1,0]
	v_rcp_f32_e32 v6, v6
	v_rcp_f32_e32 v7, v7
	v_pk_mul_f32 v[8:9], v[14:15], v[8:9]
	v_lshlrev_b32_e32 v14, 16, v19
	v_pk_mul_f32 v[120:121], v[120:121], v[8:9]
	v_lshlrev_b32_e32 v8, 16, v18
	v_and_b32_e32 v9, 0xffff0000, v18
	v_pk_mul_f32 v[8:9], v[8:9], 0.5 op_sel_hi:[1,0]
	v_and_b32_e32 v15, 0xffff0000, v19
	v_pk_mul_f32 v[6:7], v[8:9], v[6:7]
	v_lshlrev_b32_e32 v8, 16, v23
	v_and_b32_e32 v9, 0xffff0000, v23
	v_max_f32_e32 v8, v8, v8
	v_max_f32_e32 v9, v9, v9
	v_max_f32_e32 v8, 0xda24260, v8
	v_max_f32_e32 v9, 0xda24260, v9
	v_rcp_f32_e32 v8, v8
	v_rcp_f32_e32 v9, v9
	v_pk_mul_f32 v[114:115], v[114:115], v[6:7]
	v_lshlrev_b32_e32 v6, 16, v24
	v_and_b32_e32 v7, 0xffff0000, v24
	v_max_f32_e32 v6, v6, v6
	v_max_f32_e32 v7, v7, v7
	v_max_f32_e32 v6, 0xda24260, v6
	v_max_f32_e32 v7, 0xda24260, v7
	v_pk_mul_f32 v[14:15], v[14:15], 0.5 op_sel_hi:[1,0]
	v_rcp_f32_e32 v6, v6
	v_rcp_f32_e32 v7, v7
	v_pk_mul_f32 v[8:9], v[14:15], v[8:9]
	s_mov_b32 s34, 0x454000
	v_pk_mul_f32 v[116:117], v[116:117], v[8:9]
	v_lshlrev_b32_e32 v8, 16, v20
	v_and_b32_e32 v9, 0xffff0000, v20
	v_pk_mul_f32 v[8:9], v[8:9], 0.5 op_sel_hi:[1,0]
	s_waitcnt vmcnt(2)
; #define MG_LOAD(G_, s_) do { const bf16* q_ = pb + (size_t)(((s_) >> 2) * 128 + ((s_) & 3) * 16) * PNP; G_[0] = *(const GAS v4u*)(q_ + PGA); G_[1] = *(const GAS v4u*)(q_ + PGB); G_[2] = *(const GAS v4u*)(q_ + PGA + 128); G_[3] = *(const GAS v4u*)(q_ + PGB + 128); } while (0)
;     __device__ __forceinline__ void mid(f32x4 (&acc)[2][2][4][2], const Unit& u, int wr, int wc, int fr, int fq) const {
;     ...
;         MG_LOAD(A0, 0); MG_LOAD(A1, 1); MG_APPLY(A0, 0); MG_LOAD(A0, 2); MG_APPLY(A1, 1); MG_LOAD(A1, 3); MG_APPLY(A0, 2); MG_LOAD(A0, 4); MG_APPLY(A1, 3); MG_LOAD(A1, 5);
;         MG_APPLY(A0, 4); MG_LOAD(A0, 6); MG_APPLY(A1, 5); MG_LOAD(A1, 7); MG_APPLY(A0, 6); MG_APPLY(A1, 7);
	v_lshlrev_b32_e32 v22, 16, v170
	v_pk_mul_f32 v[6:7], v[8:9], v[6:7]
	v_lshlrev_b32_e32 v8, 16, v25
	v_and_b32_e32 v9, 0xffff0000, v25
	v_max_f32_e32 v8, v8, v8
	v_max_f32_e32 v9, v9, v9
	v_max_f32_e32 v8, 0xda24260, v8
	v_max_f32_e32 v9, 0xda24260, v9
	v_rcp_f32_e32 v8, v8
	v_rcp_f32_e32 v9, v9
	v_and_b32_e32 v23, 0xffff0000, v170
	v_lshlrev_b32_e32 v14, 16, v21
	v_and_b32_e32 v15, 0xffff0000, v21
	v_pk_mul_f32 v[110:111], v[110:111], v[6:7]
	v_add_co_u32_e32 v6, vcc, s34, v28
	v_max_f32_e32 v22, v22, v22
	v_max_f32_e32 v23, v23, v23
	v_pk_mul_f32 v[14:15], v[14:15], 0.5 op_sel_hi:[1,0]
	v_addc_co_u32_e32 v7, vcc, 0, v29, vcc
	s_mov_b32 s34, 0x456000
	v_max_f32_e32 v22, 0xda24260, v22
	v_max_f32_e32 v23, 0xda24260, v23
	v_pk_mul_f32 v[8:9], v[14:15], v[8:9]
	global_load_dwordx4 v[18:21], v[6:7], off offset:2048 nt
	v_add_co_u32_e32 v14, vcc, s34, v28
	v_rcp_f32_e32 v22, v22
	v_rcp_f32_e32 v23, v23
	v_addc_co_u32_e32 v15, vcc, 0, v29, vcc
	v_pk_mul_f32 v[112:113], v[112:113], v[8:9]
	global_load_dwordx4 v[158:161], v[14:15], off offset:2048
	s_nop 0
	global_load_dwordx4 v[6:9], v[6:7], off offset:2304 nt
	s_nop 0
	global_load_dwordx4 v[14:17], v[14:15], off offset:2304
	v_lshlrev_b32_e32 v24, 16, v162
	v_and_b32_e32 v25, 0xffff0000, v162
	v_pk_mul_f32 v[24:25], v[24:25], 0.5 op_sel_hi:[1,0]
	v_lshlrev_b32_e32 v162, 16, v163
	v_pk_mul_f32 v[22:23], v[24:25], v[22:23]
	v_lshlrev_b32_e32 v24, 16, v171
	v_and_b32_e32 v25, 0xffff0000, v171
	v_max_f32_e32 v24, v24, v24
	v_max_f32_e32 v25, v25, v25
	v_max_f32_e32 v24, 0xda24260, v24
	v_max_f32_e32 v25, 0xda24260, v25
	v_rcp_f32_e32 v24, v24
	v_rcp_f32_e32 v25, v25
	v_pk_mul_f32 v[106:107], v[106:107], v[22:23]
	v_lshlrev_b32_e32 v22, 16, v172
	v_and_b32_e32 v23, 0xffff0000, v172
	v_max_f32_e32 v22, v22, v22
	v_max_f32_e32 v23, v23, v23
	v_and_b32_e32 v163, 0xffff0000, v163
	v_max_f32_e32 v22, 0xda24260, v22
	v_max_f32_e32 v23, 0xda24260, v23
	v_pk_mul_f32 v[162:163], v[162:163], 0.5 op_sel_hi:[1,0]
	v_rcp_f32_e32 v22, v22
	v_rcp_f32_e32 v23, v23
	v_pk_mul_f32 v[24:25], v[162:163], v[24:25]
	v_lshlrev_b32_e32 v162, 16, v165
	v_pk_mul_f32 v[108:109], v[108:109], v[24:25]
	v_lshlrev_b32_e32 v24, 16, v164
	v_and_b32_e32 v25, 0xffff0000, v164
	v_pk_mul_f32 v[24:25], v[24:25], 0.5 op_sel_hi:[1,0]
	v_and_b32_e32 v163, 0xffff0000, v165
	v_pk_mul_f32 v[22:23], v[24:25], v[22:23]
	v_lshlrev_b32_e32 v24, 16, v173
	v_and_b32_e32 v25, 0xffff0000, v173
	v_max_f32_e32 v24, v24, v24
	v_max_f32_e32 v25, v25, v25
	v_max_f32_e32 v24, 0xda24260, v24
	v_max_f32_e32 v25, 0xda24260, v25
	v_rcp_f32_e32 v24, v24
	v_rcp_f32_e32 v25, v25
	v_pk_mul_f32 v[162:163], v[162:163], 0.5 op_sel_hi:[1,0]
	v_pk_mul_f32 v[102:103], v[102:103], v[22:23]
	s_waitcnt vmcnt(4)
	v_lshlrev_b32_e32 v22, 16, v10
	v_pk_mul_f32 v[24:25], v[162:163], v[24:25]
	v_and_b32_e32 v10, 0xffff0000, v10
	v_pk_mul_f32 v[104:105], v[104:105], v[24:25]
	v_lshlrev_b32_e32 v24, 16, v2
	v_and_b32_e32 v25, 0xffff0000, v2
	v_lshlrev_b32_e32 v2, 16, v11
	v_max_f32_e32 v10, v10, v10
	v_max_f32_e32 v2, v2, v2
	v_max_f32_e32 v10, 0xda24260, v10
	v_max_f32_e32 v2, 0xda24260, v2
	v_rcp_f32_e32 v23, v10
	v_rcp_f32_e32 v10, v2
	v_and_b32_e32 v2, 0xffff0000, v11
	v_max_f32_e32 v2, v2, v2
	v_max_f32_e32 v2, 0xda24260, v2
	v_rcp_f32_e32 v11, v2
	v_lshlrev_b32_e32 v2, 16, v3
	v_and_b32_e32 v3, 0xffff0000, v3
	v_pk_mul_f32 v[2:3], v[2:3], 0.5 op_sel_hi:[1,0]
	v_max_f32_e32 v22, v22, v22
	v_pk_mul_f32 v[2:3], v[2:3], v[10:11]
	v_lshlrev_b32_e32 v10, 16, v4
	v_pk_mul_f32 v[100:101], v[100:101], v[2:3]
	v_lshlrev_b32_e32 v2, 16, v12
	v_and_b32_e32 v3, 0xffff0000, v12
	v_max_f32_e32 v2, v2, v2
	v_max_f32_e32 v3, v3, v3
	v_max_f32_e32 v2, 0xda24260, v2
	v_max_f32_e32 v3, 0xda24260, v3
	v_rcp_f32_e32 v2, v2
	v_rcp_f32_e32 v3, v3
	v_and_b32_e32 v11, 0xffff0000, v4
	v_lshlrev_b32_e32 v4, 16, v13
	v_max_f32_e32 v4, v4, v4
	v_pk_mul_f32 v[10:11], v[10:11], 0.5 op_sel_hi:[1,0]
	v_max_f32_e32 v4, 0xda24260, v4
	v_pk_mul_f32 v[2:3], v[10:11], v[2:3]
	v_rcp_f32_e32 v10, v4
	v_and_b32_e32 v4, 0xffff0000, v13
	v_max_f32_e32 v22, 0xda24260, v22
	v_max_f32_e32 v4, v4, v4
	v_rcp_f32_e32 v22, v22
	v_max_f32_e32 v4, 0xda24260, v4
	v_rcp_f32_e32 v11, v4
	s_mov_b32 s34, 0x4de000
	v_pk_mul_f32 v[24:25], v[24:25], 0.5 op_sel_hi:[1,0]
	v_lshlrev_b32_e32 v4, 16, v5
	v_and_b32_e32 v5, 0xffff0000, v5
	v_pk_mul_f32 v[94:95], v[94:95], v[2:3]
	v_add_co_u32_e32 v2, vcc, s34, v28
	v_pk_mul_f32 v[22:23], v[24:25], v[22:23]
	v_pk_mul_f32 v[4:5], v[4:5], 0.5 op_sel_hi:[1,0]
	v_addc_co_u32_e32 v3, vcc, 0, v29, vcc
	s_mov_b32 s34, 0x4e0000
	v_pk_mul_f32 v[98:99], v[98:99], v[22:23]
	v_pk_mul_f32 v[4:5], v[4:5], v[10:11]
	global_load_dwordx4 v[22:25], v[2:3], off offset:2048 nt
	v_add_co_u32_e32 v10, vcc, s34, v28
	v_pk_mul_f32 v[96:97], v[96:97], v[4:5]
	s_nop 0
	v_addc_co_u32_e32 v11, vcc, 0, v29, vcc
	global_load_dwordx4 v[162:165], v[10:11], off offset:2048
	s_nop 0
	global_load_dwordx4 v[2:5], v[2:3], off offset:2304 nt
	s_nop 0
	global_load_dwordx4 v[10:13], v[10:11], off offset:2304
	s_waitcnt vmcnt(6)
; #define MG_LOAD(G_, s_) do { const bf16* q_ = pb + (size_t)(((s_) >> 2) * 128 + ((s_) & 3) * 16) * PNP; G_[0] = *(const GAS v4u*)(q_ + PGA); G_[1] = *(const GAS v4u*)(q_ + PGB); G_[2] = *(const GAS v4u*)(q_ + PGA + 128); G_[3] = *(const GAS v4u*)(q_ + PGB + 128); } while (0)
;     __device__ __forceinline__ void mid(f32x4 (&acc)[2][2][4][2], const Unit& u, int wr, int wc, int fr, int fq) const {
;     ...
;         MG_LOAD(A0, 0); MG_LOAD(A1, 1); MG_APPLY(A0, 0); MG_LOAD(A0, 2); MG_APPLY(A1, 1); MG_LOAD(A1, 3); MG_APPLY(A0, 2); MG_LOAD(A0, 4); MG_APPLY(A1, 3); MG_LOAD(A1, 5);
;         MG_APPLY(A0, 4); MG_LOAD(A0, 6); MG_APPLY(A1, 5); MG_LOAD(A1, 7); MG_APPLY(A0, 6); MG_APPLY(A1, 7);
	v_lshlrev_b32_e32 v27, 16, v158
	v_lshlrev_b32_e32 v168, 16, v18
	v_and_b32_e32 v169, 0xffff0000, v18
	v_lshlrev_b32_e32 v18, 16, v159
	v_max_f32_e32 v27, v27, v27
	v_max_f32_e32 v18, v18, v18
	v_max_f32_e32 v27, 0xda24260, v27
	v_max_f32_e32 v18, 0xda24260, v18
	v_rcp_f32_e32 v166, v27
	v_and_b32_e32 v27, 0xffff0000, v158
	v_rcp_f32_e32 v158, v18
	v_and_b32_e32 v18, 0xffff0000, v159
	v_max_f32_e32 v18, v18, v18
	v_max_f32_e32 v18, 0xda24260, v18
	v_rcp_f32_e32 v159, v18
	v_lshlrev_b32_e32 v18, 16, v19
	v_and_b32_e32 v19, 0xffff0000, v19
	v_pk_mul_f32 v[18:19], v[18:19], 0.5 op_sel_hi:[1,0]
	v_max_f32_e32 v27, v27, v27
	v_pk_mul_f32 v[18:19], v[18:19], v[158:159]
	v_lshlrev_b32_e32 v158, 16, v20
	v_pk_mul_f32 v[92:93], v[92:93], v[18:19]
	v_lshlrev_b32_e32 v18, 16, v160
	v_and_b32_e32 v19, 0xffff0000, v160
	v_max_f32_e32 v18, v18, v18
	v_max_f32_e32 v19, v19, v19
	v_max_f32_e32 v18, 0xda24260, v18
	v_max_f32_e32 v19, 0xda24260, v19
	v_rcp_f32_e32 v18, v18
	v_rcp_f32_e32 v19, v19
	v_and_b32_e32 v159, 0xffff0000, v20
	v_lshlrev_b32_e32 v20, 16, v161
	v_max_f32_e32 v20, v20, v20
	v_pk_mul_f32 v[158:159], v[158:159], 0.5 op_sel_hi:[1,0]
	v_max_f32_e32 v20, 0xda24260, v20
	v_pk_mul_f32 v[18:19], v[158:159], v[18:19]
	v_rcp_f32_e32 v158, v20
	v_and_b32_e32 v20, 0xffff0000, v161
	v_max_f32_e32 v20, v20, v20
	v_max_f32_e32 v20, 0xda24260, v20
	v_rcp_f32_e32 v159, v20
	v_lshlrev_b32_e32 v20, 16, v21
	v_and_b32_e32 v21, 0xffff0000, v21
	v_pk_mul_f32 v[20:21], v[20:21], 0.5 op_sel_hi:[1,0]
	v_pk_mul_f32 v[86:87], v[86:87], v[18:19]
	v_pk_mul_f32 v[20:21], v[20:21], v[158:159]
	s_waitcnt vmcnt(4)
	v_lshlrev_b32_e32 v18, 16, v14
	v_pk_mul_f32 v[88:89], v[88:89], v[20:21]
	v_and_b32_e32 v14, 0xffff0000, v14
	v_lshlrev_b32_e32 v20, 16, v6
	v_and_b32_e32 v21, 0xffff0000, v6
	v_lshlrev_b32_e32 v6, 16, v15
	v_max_f32_e32 v14, v14, v14
	v_max_f32_e32 v6, v6, v6
	v_max_f32_e32 v14, 0xda24260, v14
	v_max_f32_e32 v6, 0xda24260, v6
	v_rcp_f32_e32 v19, v14
	v_rcp_f32_e32 v14, v6
	v_and_b32_e32 v6, 0xffff0000, v15
	v_max_f32_e32 v6, v6, v6
	v_max_f32_e32 v6, 0xda24260, v6
	v_rcp_f32_e32 v15, v6
	v_lshlrev_b32_e32 v6, 16, v7
	v_and_b32_e32 v7, 0xffff0000, v7
	v_pk_mul_f32 v[6:7], v[6:7], 0.5 op_sel_hi:[1,0]
	v_max_f32_e32 v27, 0xda24260, v27
	v_pk_mul_f32 v[6:7], v[6:7], v[14:15]
	v_lshlrev_b32_e32 v14, 16, v8
	v_pk_mul_f32 v[84:85], v[84:85], v[6:7]
	v_lshlrev_b32_e32 v6, 16, v16
	v_and_b32_e32 v7, 0xffff0000, v16
	v_max_f32_e32 v6, v6, v6
	v_max_f32_e32 v7, v7, v7
	v_max_f32_e32 v6, 0xda24260, v6
	v_max_f32_e32 v7, 0xda24260, v7
	v_rcp_f32_e32 v6, v6
	v_rcp_f32_e32 v7, v7
	v_and_b32_e32 v15, 0xffff0000, v8
	v_lshlrev_b32_e32 v8, 16, v17
	v_max_f32_e32 v8, v8, v8
	v_rcp_f32_e32 v167, v27
	v_pk_mul_f32 v[14:15], v[14:15], 0.5 op_sel_hi:[1,0]
	v_max_f32_e32 v8, 0xda24260, v8
	v_max_f32_e32 v18, v18, v18
	v_pk_mul_f32 v[6:7], v[14:15], v[6:7]
	v_rcp_f32_e32 v14, v8
	v_and_b32_e32 v8, 0xffff0000, v17
	v_max_f32_e32 v18, 0xda24260, v18
	v_max_f32_e32 v8, v8, v8
	v_pk_mul_f32 v[168:169], v[168:169], 0.5 op_sel_hi:[1,0]
	v_rcp_f32_e32 v18, v18
	v_max_f32_e32 v8, 0xda24260, v8
	v_pk_mul_f32 v[166:167], v[168:169], v[166:167]
	v_rcp_f32_e32 v15, v8
	s_waitcnt vmcnt(2)
	v_lshlrev_b32_e32 v27, 16, v162
	v_lshlrev_b32_e32 v168, 16, v22
	v_and_b32_e32 v169, 0xffff0000, v22
	v_lshlrev_b32_e32 v22, 16, v163
	s_mov_b32 s34, 0x568000
	v_max_f32_e32 v27, v27, v27
	v_max_f32_e32 v22, v22, v22
	v_pk_mul_f32 v[20:21], v[20:21], 0.5 op_sel_hi:[1,0]
	v_lshlrev_b32_e32 v8, 16, v9
	v_and_b32_e32 v9, 0xffff0000, v9
	v_pk_mul_f32 v[78:79], v[78:79], v[6:7]
	v_add_co_u32_e32 v6, vcc, s34, v28
	v_max_f32_e32 v27, 0xda24260, v27
	v_max_f32_e32 v22, 0xda24260, v22
	v_pk_mul_f32 v[90:91], v[90:91], v[166:167]
	v_pk_mul_f32 v[18:19], v[20:21], v[18:19]
	v_pk_mul_f32 v[8:9], v[8:9], 0.5 op_sel_hi:[1,0]
	v_addc_co_u32_e32 v7, vcc, 0, v29, vcc
	s_mov_b32 s34, 0x56a000
	v_rcp_f32_e32 v166, v27
	v_and_b32_e32 v27, 0xffff0000, v162
	v_rcp_f32_e32 v162, v22
	v_and_b32_e32 v22, 0xffff0000, v163
	v_pk_mul_f32 v[82:83], v[82:83], v[18:19]
	v_pk_mul_f32 v[8:9], v[8:9], v[14:15]
	global_load_dwordx4 v[18:21], v[6:7], off offset:2048 nt
	v_add_co_u32_e32 v14, vcc, s34, v28
	v_max_f32_e32 v22, v22, v22
	s_nop 0
	v_addc_co_u32_e32 v15, vcc, 0, v29, vcc
	v_max_f32_e32 v22, 0xda24260, v22
	v_pk_mul_f32 v[80:81], v[80:81], v[8:9]
	global_load_dwordx4 v[158:161], v[14:15], off offset:2048
	s_nop 0
	global_load_dwordx4 v[6:9], v[6:7], off offset:2304 nt
	s_nop 0
	global_load_dwordx4 v[14:17], v[14:15], off offset:2304
	v_rcp_f32_e32 v163, v22
	v_lshlrev_b32_e32 v22, 16, v23
	v_and_b32_e32 v23, 0xffff0000, v23
	v_pk_mul_f32 v[22:23], v[22:23], 0.5 op_sel_hi:[1,0]
	s_mov_b32 s34, 0x5f2000
	v_pk_mul_f32 v[22:23], v[22:23], v[162:163]
	v_lshlrev_b32_e32 v162, 16, v24
	v_pk_mul_f32 v[76:77], v[76:77], v[22:23]
	v_lshlrev_b32_e32 v22, 16, v164
	v_and_b32_e32 v23, 0xffff0000, v164
	v_max_f32_e32 v22, v22, v22
	v_max_f32_e32 v23, v23, v23
	v_max_f32_e32 v22, 0xda24260, v22
	v_max_f32_e32 v23, 0xda24260, v23
	v_rcp_f32_e32 v22, v22
	v_rcp_f32_e32 v23, v23
	v_and_b32_e32 v163, 0xffff0000, v24
	v_lshlrev_b32_e32 v24, 16, v165
	v_max_f32_e32 v24, v24, v24
	v_pk_mul_f32 v[162:163], v[162:163], 0.5 op_sel_hi:[1,0]
	v_max_f32_e32 v24, 0xda24260, v24
	v_pk_mul_f32 v[22:23], v[162:163], v[22:23]
	v_rcp_f32_e32 v162, v24
	v_and_b32_e32 v24, 0xffff0000, v165
	v_max_f32_e32 v24, v24, v24
	v_max_f32_e32 v24, 0xda24260, v24
	v_rcp_f32_e32 v163, v24
	v_lshlrev_b32_e32 v24, 16, v25
	v_and_b32_e32 v25, 0xffff0000, v25
	v_pk_mul_f32 v[24:25], v[24:25], 0.5 op_sel_hi:[1,0]
	v_pk_mul_f32 v[70:71], v[70:71], v[22:23]
	v_pk_mul_f32 v[24:25], v[24:25], v[162:163]
	s_waitcnt vmcnt(4)
; #define MG_LOAD(G_, s_) do { const bf16* q_ = pb + (size_t)(((s_) >> 2) * 128 + ((s_) & 3) * 16) * PNP; G_[0] = *(const GAS v4u*)(q_ + PGA); G_[1] = *(const GAS v4u*)(q_ + PGB); G_[2] = *(const GAS v4u*)(q_ + PGA + 128); G_[3] = *(const GAS v4u*)(q_ + PGB + 128); } while (0)
;     __device__ __forceinline__ void mid(f32x4 (&acc)[2][2][4][2], const Unit& u, int wr, int wc, int fr, int fq) const {
;     ...
;         MG_LOAD(A0, 0); MG_LOAD(A1, 1); MG_APPLY(A0, 0); MG_LOAD(A0, 2); MG_APPLY(A1, 1); MG_LOAD(A1, 3); MG_APPLY(A0, 2); MG_LOAD(A0, 4); MG_APPLY(A1, 3); MG_LOAD(A1, 5);
;         MG_APPLY(A0, 4); MG_LOAD(A0, 6); MG_APPLY(A1, 5); MG_LOAD(A1, 7); MG_APPLY(A0, 6); MG_APPLY(A1, 7);
	v_lshlrev_b32_e32 v22, 16, v10
	v_pk_mul_f32 v[72:73], v[72:73], v[24:25]
	v_and_b32_e32 v10, 0xffff0000, v10
	v_lshlrev_b32_e32 v24, 16, v2
	v_and_b32_e32 v25, 0xffff0000, v2
	v_lshlrev_b32_e32 v2, 16, v11
	v_max_f32_e32 v10, v10, v10
	v_max_f32_e32 v2, v2, v2
	v_max_f32_e32 v10, 0xda24260, v10
	v_max_f32_e32 v2, 0xda24260, v2
	v_rcp_f32_e32 v23, v10
	v_rcp_f32_e32 v10, v2
	v_and_b32_e32 v2, 0xffff0000, v11
	v_max_f32_e32 v2, v2, v2
	v_max_f32_e32 v2, 0xda24260, v2
	v_rcp_f32_e32 v11, v2
	v_lshlrev_b32_e32 v2, 16, v3
	v_and_b32_e32 v3, 0xffff0000, v3
	v_pk_mul_f32 v[2:3], v[2:3], 0.5 op_sel_hi:[1,0]
	v_max_f32_e32 v22, v22, v22
	v_pk_mul_f32 v[2:3], v[2:3], v[10:11]
	v_lshlrev_b32_e32 v10, 16, v4
	v_pk_mul_f32 v[68:69], v[68:69], v[2:3]
	v_lshlrev_b32_e32 v2, 16, v12
	v_and_b32_e32 v3, 0xffff0000, v12
	v_max_f32_e32 v2, v2, v2
	v_max_f32_e32 v3, v3, v3
	v_max_f32_e32 v2, 0xda24260, v2
	v_max_f32_e32 v3, 0xda24260, v3
	v_rcp_f32_e32 v2, v2
	v_rcp_f32_e32 v3, v3
	v_and_b32_e32 v11, 0xffff0000, v4
	v_lshlrev_b32_e32 v4, 16, v13
	v_max_f32_e32 v4, v4, v4
	v_pk_mul_f32 v[10:11], v[10:11], 0.5 op_sel_hi:[1,0]
	v_max_f32_e32 v4, 0xda24260, v4
	v_pk_mul_f32 v[2:3], v[10:11], v[2:3]
	v_rcp_f32_e32 v10, v4
	v_and_b32_e32 v4, 0xffff0000, v13
	v_max_f32_e32 v4, v4, v4
	v_max_f32_e32 v4, 0xda24260, v4
	v_max_f32_e32 v22, 0xda24260, v22
	v_rcp_f32_e32 v11, v4
	v_rcp_f32_e32 v22, v22
	v_lshlrev_b32_e32 v4, 16, v5
	v_and_b32_e32 v5, 0xffff0000, v5
	v_pk_mul_f32 v[62:63], v[62:63], v[2:3]
	v_add_co_u32_e32 v2, vcc, s34, v28
	v_pk_mul_f32 v[4:5], v[4:5], 0.5 op_sel_hi:[1,0]
	s_nop 0
	v_addc_co_u32_e32 v3, vcc, 0, v29, vcc
	s_mov_b32 s34, 0x5f4000
	v_pk_mul_f32 v[24:25], v[24:25], 0.5 op_sel_hi:[1,0]
	v_pk_mul_f32 v[4:5], v[4:5], v[10:11]
	v_add_co_u32_e32 v10, vcc, s34, v28
	v_pk_mul_f32 v[22:23], v[24:25], v[22:23]
	s_nop 0
	v_addc_co_u32_e32 v11, vcc, 0, v29, vcc
	v_pk_mul_f32 v[66:67], v[66:67], v[22:23]
	v_pk_mul_f32 v[64:65], v[64:65], v[4:5]
	global_load_dwordx4 v[22:25], v[2:3], off offset:2048 nt
	global_load_dwordx4 v[162:165], v[10:11], off offset:2048
	s_nop 0
	global_load_dwordx4 v[2:5], v[2:3], off offset:2304 nt
	s_nop 0
	global_load_dwordx4 v[10:13], v[10:11], off offset:2304
	v_max_f32_e32 v27, v27, v27
	v_max_f32_e32 v27, 0xda24260, v27
	v_rcp_f32_e32 v167, v27
	v_pk_mul_f32 v[168:169], v[168:169], 0.5 op_sel_hi:[1,0]
	s_waitcnt vmcnt(6)
	v_lshlrev_b32_e32 v27, 16, v158
	v_max_f32_e32 v27, v27, v27
	v_pk_mul_f32 v[166:167], v[168:169], v[166:167]
	v_max_f32_e32 v27, 0xda24260, v27
	v_pk_mul_f32 v[74:75], v[74:75], v[166:167]
	v_lshlrev_b32_e32 v166, 16, v18
	v_and_b32_e32 v167, 0xffff0000, v18
	v_lshlrev_b32_e32 v18, 16, v159
	v_max_f32_e32 v18, v18, v18
	v_max_f32_e32 v18, 0xda24260, v18
	v_rcp_f32_e32 v28, v27
	v_and_b32_e32 v27, 0xffff0000, v158
	v_rcp_f32_e32 v158, v18
	v_and_b32_e32 v18, 0xffff0000, v159
	v_max_f32_e32 v18, v18, v18
	v_max_f32_e32 v18, 0xda24260, v18
	v_rcp_f32_e32 v159, v18
	v_max_f32_e32 v27, v27, v27
	v_lshlrev_b32_e32 v18, 16, v19
	v_and_b32_e32 v19, 0xffff0000, v19
	v_max_f32_e32 v27, 0xda24260, v27
	v_pk_mul_f32 v[18:19], v[18:19], 0.5 op_sel_hi:[1,0]
	v_rcp_f32_e32 v29, v27
	v_pk_mul_f32 v[18:19], v[18:19], v[158:159]
	v_pk_mul_f32 v[166:167], v[166:167], 0.5 op_sel_hi:[1,0]
	v_pk_mul_f32 v[60:61], v[60:61], v[18:19]
	v_lshlrev_b32_e32 v18, 16, v160
	v_and_b32_e32 v19, 0xffff0000, v160
	v_max_f32_e32 v18, v18, v18
	v_max_f32_e32 v19, v19, v19
	v_max_f32_e32 v18, 0xda24260, v18
	v_max_f32_e32 v19, 0xda24260, v19
	v_pk_mul_f32 v[28:29], v[166:167], v[28:29]
	v_rcp_f32_e32 v18, v18
	v_rcp_f32_e32 v19, v19
	v_pk_mul_f32 v[58:59], v[58:59], v[28:29]
	v_lshlrev_b32_e32 v28, 16, v20
	v_and_b32_e32 v29, 0xffff0000, v20
	v_lshlrev_b32_e32 v20, 16, v161
	v_max_f32_e32 v20, v20, v20
	v_pk_mul_f32 v[28:29], v[28:29], 0.5 op_sel_hi:[1,0]
	v_max_f32_e32 v20, 0xda24260, v20
	v_pk_mul_f32 v[18:19], v[28:29], v[18:19]
	v_rcp_f32_e32 v28, v20
	v_and_b32_e32 v20, 0xffff0000, v161
	v_max_f32_e32 v20, v20, v20
	v_max_f32_e32 v20, 0xda24260, v20
	v_rcp_f32_e32 v29, v20
	v_lshlrev_b32_e32 v20, 16, v21
	v_and_b32_e32 v21, 0xffff0000, v21
	v_pk_mul_f32 v[20:21], v[20:21], 0.5 op_sel_hi:[1,0]
	v_pk_mul_f32 v[54:55], v[54:55], v[18:19]
	v_pk_mul_f32 v[20:21], v[20:21], v[28:29]
	s_waitcnt vmcnt(4)
; #define MG_LOAD(G_, s_) do { const bf16* q_ = pb + (size_t)(((s_) >> 2) * 128 + ((s_) & 3) * 16) * PNP; G_[0] = *(const GAS v4u*)(q_ + PGA); G_[1] = *(const GAS v4u*)(q_ + PGB); G_[2] = *(const GAS v4u*)(q_ + PGA + 128); G_[3] = *(const GAS v4u*)(q_ + PGB + 128); } while (0)
;     __device__ __forceinline__ void mid(f32x4 (&acc)[2][2][4][2], const Unit& u, int wr, int wc, int fr, int fq) const {
;     ...
;         MG_LOAD(A0, 0); MG_LOAD(A1, 1); MG_APPLY(A0, 0); MG_LOAD(A0, 2); MG_APPLY(A1, 1); MG_LOAD(A1, 3); MG_APPLY(A0, 2); MG_LOAD(A0, 4); MG_APPLY(A1, 3); MG_LOAD(A1, 5);
;         MG_APPLY(A0, 4); MG_LOAD(A0, 6); MG_APPLY(A1, 5); MG_LOAD(A1, 7); MG_APPLY(A0, 6); MG_APPLY(A1, 7);
	v_lshlrev_b32_e32 v18, 16, v14
	v_pk_mul_f32 v[56:57], v[56:57], v[20:21]
	v_and_b32_e32 v14, 0xffff0000, v14
	v_lshlrev_b32_e32 v20, 16, v6
	v_and_b32_e32 v21, 0xffff0000, v6
	v_lshlrev_b32_e32 v6, 16, v15
	v_max_f32_e32 v14, v14, v14
	v_max_f32_e32 v6, v6, v6
	v_max_f32_e32 v14, 0xda24260, v14
	v_max_f32_e32 v6, 0xda24260, v6
	v_rcp_f32_e32 v19, v14
	v_rcp_f32_e32 v14, v6
	v_and_b32_e32 v6, 0xffff0000, v15
	v_max_f32_e32 v6, v6, v6
	v_max_f32_e32 v6, 0xda24260, v6
	v_rcp_f32_e32 v15, v6
	v_lshlrev_b32_e32 v6, 16, v7
	v_and_b32_e32 v7, 0xffff0000, v7
	v_pk_mul_f32 v[6:7], v[6:7], 0.5 op_sel_hi:[1,0]
	v_max_f32_e32 v18, v18, v18
	v_pk_mul_f32 v[6:7], v[6:7], v[14:15]
	v_lshlrev_b32_e32 v14, 16, v8
	v_pk_mul_f32 v[52:53], v[52:53], v[6:7]
	v_lshlrev_b32_e32 v6, 16, v16
	v_and_b32_e32 v7, 0xffff0000, v16
	v_max_f32_e32 v6, v6, v6
	v_max_f32_e32 v7, v7, v7
	v_max_f32_e32 v6, 0xda24260, v6
	v_max_f32_e32 v7, 0xda24260, v7
	v_rcp_f32_e32 v6, v6
	v_rcp_f32_e32 v7, v7
	v_and_b32_e32 v15, 0xffff0000, v8
	v_lshlrev_b32_e32 v8, 16, v17
	v_max_f32_e32 v8, v8, v8
	v_pk_mul_f32 v[14:15], v[14:15], 0.5 op_sel_hi:[1,0]
	v_max_f32_e32 v8, 0xda24260, v8
	v_pk_mul_f32 v[6:7], v[14:15], v[6:7]
	v_rcp_f32_e32 v14, v8
	v_and_b32_e32 v8, 0xffff0000, v17
	v_max_f32_e32 v8, v8, v8
	v_max_f32_e32 v8, 0xda24260, v8
	v_rcp_f32_e32 v15, v8
	v_pk_mul_f32 v[46:47], v[46:47], v[6:7]
	s_waitcnt vmcnt(2)
	v_lshlrev_b32_e32 v6, 16, v162
	v_and_b32_e32 v7, 0xffff0000, v162
	v_max_f32_e32 v6, v6, v6
	v_max_f32_e32 v7, v7, v7
	v_lshlrev_b32_e32 v8, 16, v9
	v_and_b32_e32 v9, 0xffff0000, v9
	v_max_f32_e32 v6, 0xda24260, v6
	v_max_f32_e32 v7, 0xda24260, v7
	v_pk_mul_f32 v[8:9], v[8:9], 0.5 op_sel_hi:[1,0]
	v_rcp_f32_e32 v6, v6
	v_rcp_f32_e32 v7, v7
	v_pk_mul_f32 v[8:9], v[8:9], v[14:15]
	v_lshlrev_b32_e32 v14, 16, v23
	v_pk_mul_f32 v[48:49], v[48:49], v[8:9]
	v_lshlrev_b32_e32 v8, 16, v22
	v_and_b32_e32 v9, 0xffff0000, v22
	v_pk_mul_f32 v[8:9], v[8:9], 0.5 op_sel_hi:[1,0]
	v_and_b32_e32 v15, 0xffff0000, v23
	v_pk_mul_f32 v[6:7], v[8:9], v[6:7]
	v_lshlrev_b32_e32 v8, 16, v163
	v_and_b32_e32 v9, 0xffff0000, v163
	v_max_f32_e32 v8, v8, v8
	v_max_f32_e32 v9, v9, v9
	v_max_f32_e32 v8, 0xda24260, v8
	v_max_f32_e32 v9, 0xda24260, v9
	v_rcp_f32_e32 v8, v8
	v_rcp_f32_e32 v9, v9
	v_pk_mul_f32 v[42:43], v[42:43], v[6:7]
	v_lshlrev_b32_e32 v6, 16, v164
	v_and_b32_e32 v7, 0xffff0000, v164
	v_max_f32_e32 v6, v6, v6
	v_max_f32_e32 v7, v7, v7
	v_max_f32_e32 v6, 0xda24260, v6
	v_max_f32_e32 v7, 0xda24260, v7
	v_pk_mul_f32 v[14:15], v[14:15], 0.5 op_sel_hi:[1,0]
	v_rcp_f32_e32 v6, v6
	v_rcp_f32_e32 v7, v7
	v_pk_mul_f32 v[8:9], v[14:15], v[8:9]
	v_lshlrev_b32_e32 v14, 16, v25
	v_pk_mul_f32 v[44:45], v[44:45], v[8:9]
	v_lshlrev_b32_e32 v8, 16, v24
	v_and_b32_e32 v9, 0xffff0000, v24
	v_pk_mul_f32 v[8:9], v[8:9], 0.5 op_sel_hi:[1,0]
	v_and_b32_e32 v15, 0xffff0000, v25
	v_pk_mul_f32 v[6:7], v[8:9], v[6:7]
	v_lshlrev_b32_e32 v8, 16, v165
	v_and_b32_e32 v9, 0xffff0000, v165
	v_max_f32_e32 v8, v8, v8
	v_max_f32_e32 v9, v9, v9
	v_max_f32_e32 v8, 0xda24260, v8
	v_max_f32_e32 v9, 0xda24260, v9
	v_rcp_f32_e32 v8, v8
	v_rcp_f32_e32 v9, v9
	v_pk_mul_f32 v[38:39], v[38:39], v[6:7]
	s_waitcnt vmcnt(0)
	v_lshlrev_b32_e32 v6, 16, v10
	v_and_b32_e32 v7, 0xffff0000, v10
	v_max_f32_e32 v6, v6, v6
	v_max_f32_e32 v7, v7, v7
	v_pk_mul_f32 v[14:15], v[14:15], 0.5 op_sel_hi:[1,0]
	v_max_f32_e32 v6, 0xda24260, v6
	v_max_f32_e32 v7, 0xda24260, v7
	v_pk_mul_f32 v[8:9], v[14:15], v[8:9]
	v_rcp_f32_e32 v6, v6
	v_rcp_f32_e32 v7, v7
	v_pk_mul_f32 v[40:41], v[40:41], v[8:9]
	v_lshlrev_b32_e32 v8, 16, v2
	v_and_b32_e32 v9, 0xffff0000, v2
	v_lshlrev_b32_e32 v2, 16, v11
	v_max_f32_e32 v2, v2, v2
	v_pk_mul_f32 v[8:9], v[8:9], 0.5 op_sel_hi:[1,0]
	v_max_f32_e32 v2, 0xda24260, v2
	v_pk_mul_f32 v[6:7], v[8:9], v[6:7]
	v_rcp_f32_e32 v8, v2
	v_and_b32_e32 v2, 0xffff0000, v11
	v_max_f32_e32 v2, v2, v2
	v_max_f32_e32 v2, 0xda24260, v2
	v_rcp_f32_e32 v9, v2
	v_lshlrev_b32_e32 v2, 16, v3
	v_and_b32_e32 v3, 0xffff0000, v3
	v_pk_mul_f32 v[2:3], v[2:3], 0.5 op_sel_hi:[1,0]
	v_pk_mul_f32 v[34:35], v[34:35], v[6:7]
	v_pk_mul_f32 v[2:3], v[2:3], v[8:9]
	v_lshlrev_b32_e32 v6, 16, v4
	v_pk_mul_f32 v[36:37], v[36:37], v[2:3]
	v_lshlrev_b32_e32 v2, 16, v12
	v_and_b32_e32 v3, 0xffff0000, v12
	v_max_f32_e32 v2, v2, v2
	v_max_f32_e32 v3, v3, v3
	v_max_f32_e32 v2, 0xda24260, v2
	v_max_f32_e32 v3, 0xda24260, v3
	v_rcp_f32_e32 v2, v2
	v_rcp_f32_e32 v3, v3
	v_and_b32_e32 v7, 0xffff0000, v4
	v_lshlrev_b32_e32 v4, 16, v13
	v_max_f32_e32 v4, v4, v4
	v_pk_mul_f32 v[6:7], v[6:7], 0.5 op_sel_hi:[1,0]
	v_max_f32_e32 v4, 0xda24260, v4
	v_pk_mul_f32 v[2:3], v[6:7], v[2:3]
	v_rcp_f32_e32 v6, v4
	v_and_b32_e32 v4, 0xffff0000, v13
	v_max_f32_e32 v4, v4, v4
	v_max_f32_e32 v18, 0xda24260, v18
	v_max_f32_e32 v4, 0xda24260, v4
	v_rcp_f32_e32 v18, v18
	v_rcp_f32_e32 v7, v4
	v_lshlrev_b32_e32 v4, 16, v5
	v_and_b32_e32 v5, 0xffff0000, v5
	v_pk_mul_f32 v[20:21], v[20:21], 0.5 op_sel_hi:[1,0]
	v_pk_mul_f32 v[4:5], v[4:5], 0.5 op_sel_hi:[1,0]
	v_pk_mul_f32 v[18:19], v[20:21], v[18:19]
	v_pk_mul_f32 v[4:5], v[4:5], v[6:7]
	v_pk_mul_f32 v[50:51], v[50:51], v[18:19]
	v_pk_mul_f32 v[32:33], v[32:33], v[4:5]
	v_pk_mul_f32 v[30:31], v[30:31], v[2:3]
	s_branch .LBB0_1708

; #define ME_LOAD(G_, s_) do { const bf16* q_ = pb + (size_t)(((s_) >> 2) * 128 + ((s_) & 3) * 16) * PNP; G_[0] = *(const GAS v4u*)q_; G_[1] = *(const GAS v4u*)(q_ + 128); } while (0)
;     __device__ __forceinline__ void operator()(const f32x4 (&acc)[2][2][4][2], const Unit& u, int wr, int wc, int fr, int fq) const {
;         const float sc = cB * S_MRG;
;         const bf16* pb = P + (size_t)(u.pm * 256 + wr * 64 + fr) * PNP + (u.pn * 256 + wc * 32 + 8 * fq) + PGB;
;         unsigned char* ob = O + (size_t)(u.pm * 256 + wr * 64 + fr) * DM + (u.pn * 256 + wc * 32 + 8 * fq);
;         asm volatile("" : "+v"(pb), "+v"(ob));
;         v4u G0[2], G1[2];
;     ...
;         ME_LOAD(G0, 0); ME_LOAD(G1, 1); ME_STORE(G0, 0); ME_LOAD(G0, 2); ME_STORE(G1, 1); ME_LOAD(G1, 3); ME_STORE(G0, 2); ME_LOAD(G0, 4); ME_STORE(G1, 3); ME_LOAD(G1, 5);
;         ME_STORE(G0, 4); ME_LOAD(G0, 6); ME_STORE(G1, 5); ME_LOAD(G1, 7); ME_STORE(G0, 6); ME_STORE(G1, 7);
.LBB0_1713:
	v_lshlrev_b64 v[2:3], 12, v[200:201]
	s_mov_b64 s[28:29], 0x6800
	v_lshl_add_u64 v[2:3], s[6:7], 0, v[2:3]
	v_lshl_add_u64 v[16:17], v[204:205], 0, s[28:29]
	v_lshl_add_u64 v[14:15], v[2:3], 0, v[202:203]
	s_nop 15
	s_nop 15
	global_load_dwordx4 v[18:21], v[16:17], off nt
	global_load_dwordx4 v[10:13], v[16:17], off offset:256 nt
	v_add_co_u32_e32 v2, vcc, 0x8a000, v16
	s_mov_b32 s21, 0x114000
	s_nop 0
	v_addc_co_u32_e32 v3, vcc, 0, v17, vcc
	global_load_dwordx4 v[6:9], v[2:3], off nt
	s_nop 0
	global_load_dwordx4 v[2:5], v[2:3], off offset:256 nt
	s_mov_b64 s[28:29], -1
	s_waitcnt vmcnt(3)
	v_lshlrev_b32_e32 v22, 16, v18
	v_and_b32_e32 v18, 0xffff0000, v18
	v_max_f32_e32 v22, v22, v22
	v_max_f32_e32 v18, v18, v18
	v_max_f32_e32 v22, 0xda24260, v22
	v_max_f32_e32 v23, 0xda24260, v18
	v_pk_mul_f32 v[22:23], v[22:23], s[18:19] op_sel_hi:[1,0]
	v_lshlrev_b32_e32 v18, 16, v19
	v_and_b32_e32 v19, 0xffff0000, v19
	v_pk_mul_f32 v[22:23], v[154:155], v[22:23]
	v_max_f32_e32 v18, v18, v18
	v_max_f32_e32 v19, v19, v19
	v_lshlrev_b32_e32 v24, 16, v20
	v_and_b32_e32 v20, 0xffff0000, v20
	v_med3_f32 v27, v22, s51, v187
	v_med3_f32 v23, v23, s51, v187
	v_mov_b32_e32 v22, 0
	v_max_f32_e32 v18, 0xda24260, v18
	v_max_f32_e32 v19, 0xda24260, v19
	v_max_f32_e32 v24, v24, v24
	v_max_f32_e32 v20, v20, v20
	v_cvt_pk_fp8_f32 v22, v27, v23
	v_pk_mul_f32 v[18:19], v[18:19], s[18:19] op_sel_hi:[1,0]
	v_max_f32_e32 v24, 0xda24260, v24
	v_max_f32_e32 v25, 0xda24260, v20
	v_pk_mul_f32 v[18:19], v[156:157], v[18:19]
	v_pk_mul_f32 v[24:25], v[24:25], s[18:19] op_sel_hi:[1,0]
	v_lshlrev_b32_e32 v20, 16, v21
	v_and_b32_e32 v21, 0xffff0000, v21
	v_pk_mul_f32 v[24:25], v[150:151], v[24:25]
	v_med3_f32 v18, v18, s51, v187
	v_med3_f32 v19, v19, s51, v187
	v_max_f32_e32 v20, v20, v20
	v_max_f32_e32 v21, v21, v21
	v_cvt_pk_fp8_f32 v22, v18, v19 op_sel:[0,0,1]
	v_med3_f32 v18, v24, s51, v187
	v_med3_f32 v19, v25, s51, v187
	v_mov_b32_e32 v23, 0
	v_max_f32_e32 v20, 0xda24260, v20
	v_max_f32_e32 v21, 0xda24260, v21
	v_cvt_pk_fp8_f32 v23, v18, v19
	v_pk_mul_f32 v[20:21], v[20:21], s[18:19] op_sel_hi:[1,0]
	s_waitcnt vmcnt(1)
	v_lshlrev_b32_e32 v24, 16, v8
	v_pk_mul_f32 v[20:21], v[152:153], v[20:21]
	v_and_b32_e32 v8, 0xffff0000, v8
	v_med3_f32 v18, v20, s51, v187
	v_med3_f32 v19, v21, s51, v187
	v_cvt_pk_fp8_f32 v23, v18, v19 op_sel:[0,0,1]
	v_lshlrev_b32_e32 v18, 16, v10
	v_and_b32_e32 v10, 0xffff0000, v10
	v_max_f32_e32 v18, v18, v18
	v_max_f32_e32 v10, v10, v10
	v_max_f32_e32 v18, 0xda24260, v18
	v_max_f32_e32 v19, 0xda24260, v10
	v_pk_mul_f32 v[18:19], v[18:19], s[18:19] op_sel_hi:[1,0]
	v_lshlrev_b32_e32 v10, 16, v11
	v_and_b32_e32 v11, 0xffff0000, v11
	v_pk_mul_f32 v[18:19], v[146:147], v[18:19]
	global_store_dwordx2 v[14:15], v[22:23], off
	v_max_f32_e32 v10, v10, v10
	v_max_f32_e32 v11, v11, v11
	v_lshlrev_b32_e32 v20, 16, v12
	v_and_b32_e32 v12, 0xffff0000, v12
	v_med3_f32 v22, v18, s51, v187
	v_med3_f32 v19, v19, s51, v187
	v_mov_b32_e32 v18, 0
	v_max_f32_e32 v10, 0xda24260, v10
	v_max_f32_e32 v11, 0xda24260, v11
	v_max_f32_e32 v20, v20, v20
	v_max_f32_e32 v12, v12, v12
	v_cvt_pk_fp8_f32 v18, v22, v19
	v_pk_mul_f32 v[10:11], v[10:11], s[18:19] op_sel_hi:[1,0]
	v_max_f32_e32 v20, 0xda24260, v20
	v_max_f32_e32 v21, 0xda24260, v12
	v_pk_mul_f32 v[10:11], v[148:149], v[10:11]
	v_pk_mul_f32 v[20:21], v[20:21], s[18:19] op_sel_hi:[1,0]
	v_lshlrev_b32_e32 v12, 16, v13
	v_and_b32_e32 v13, 0xffff0000, v13
	v_pk_mul_f32 v[20:21], v[142:143], v[20:21]
	v_med3_f32 v10, v10, s51, v187
	v_med3_f32 v11, v11, s51, v187
	v_max_f32_e32 v12, v12, v12
	v_max_f32_e32 v13, v13, v13
	v_cvt_pk_fp8_f32 v18, v10, v11 op_sel:[0,0,1]
	v_med3_f32 v10, v20, s51, v187
	v_med3_f32 v11, v21, s51, v187
	v_mov_b32_e32 v19, 0
	v_max_f32_e32 v12, 0xda24260, v12
	v_max_f32_e32 v13, 0xda24260, v13
	v_cvt_pk_fp8_f32 v19, v10, v11
	v_pk_mul_f32 v[12:13], v[12:13], s[18:19] op_sel_hi:[1,0]
	v_lshlrev_b32_e32 v22, 16, v6
	v_pk_mul_f32 v[12:13], v[144:145], v[12:13]
	v_and_b32_e32 v6, 0xffff0000, v6
	v_med3_f32 v10, v12, s51, v187
	v_med3_f32 v11, v13, s51, v187
	v_cvt_pk_fp8_f32 v19, v10, v11 op_sel:[0,0,1]
	v_max_f32_e32 v22, v22, v22
	v_max_f32_e32 v6, v6, v6
	v_add_co_u32_e32 v10, vcc, s21, v16
	v_max_f32_e32 v22, 0xda24260, v22
	v_max_f32_e32 v23, 0xda24260, v6
	global_store_dwordx2 v[14:15], v[18:19], off offset:128
	v_addc_co_u32_e32 v11, vcc, 0, v17, vcc
	v_pk_mul_f32 v[22:23], v[22:23], s[18:19] op_sel_hi:[1,0]
	global_load_dwordx4 v[18:21], v[10:11], off nt
	s_nop 0
	global_load_dwordx4 v[10:13], v[10:11], off offset:256 nt
	v_lshlrev_b32_e32 v6, 16, v7
	v_and_b32_e32 v7, 0xffff0000, v7
	v_pk_mul_f32 v[22:23], v[138:139], v[22:23]
	v_max_f32_e32 v6, v6, v6
	v_max_f32_e32 v7, v7, v7
	v_med3_f32 v27, v22, s51, v187
	v_med3_f32 v23, v23, s51, v187
	v_mov_b32_e32 v22, 0
	v_max_f32_e32 v6, 0xda24260, v6
	v_max_f32_e32 v7, 0xda24260, v7
	v_max_f32_e32 v24, v24, v24
	v_max_f32_e32 v8, v8, v8
	v_cvt_pk_fp8_f32 v22, v27, v23
	v_pk_mul_f32 v[6:7], v[6:7], s[18:19] op_sel_hi:[1,0]
	v_max_f32_e32 v24, 0xda24260, v24
	v_max_f32_e32 v25, 0xda24260, v8
	v_pk_mul_f32 v[6:7], v[140:141], v[6:7]
	v_pk_mul_f32 v[24:25], v[24:25], s[18:19] op_sel_hi:[1,0]
	v_lshlrev_b32_e32 v8, 16, v9
	v_and_b32_e32 v9, 0xffff0000, v9
	v_pk_mul_f32 v[24:25], v[134:135], v[24:25]
	v_med3_f32 v6, v6, s51, v187
	v_med3_f32 v7, v7, s51, v187
	v_max_f32_e32 v8, v8, v8
	v_max_f32_e32 v9, v9, v9
	v_cvt_pk_fp8_f32 v22, v6, v7 op_sel:[0,0,1]
	v_med3_f32 v6, v24, s51, v187
	v_med3_f32 v7, v25, s51, v187
	v_mov_b32_e32 v23, 0
	v_max_f32_e32 v8, 0xda24260, v8
	v_max_f32_e32 v9, 0xda24260, v9
	v_cvt_pk_fp8_f32 v23, v6, v7
	v_pk_mul_f32 v[8:9], v[8:9], s[18:19] op_sel_hi:[1,0]
	s_mov_b32 s21, 0x10000
	v_pk_mul_f32 v[8:9], v[136:137], v[8:9]
	s_nop 0
	v_med3_f32 v6, v8, s51, v187
	v_med3_f32 v7, v9, s51, v187
	s_waitcnt vmcnt(4)
; #define ME_LOAD(G_, s_) do { const bf16* q_ = pb + (size_t)(((s_) >> 2) * 128 + ((s_) & 3) * 16) * PNP; G_[0] = *(const GAS v4u*)q_; G_[1] = *(const GAS v4u*)(q_ + 128); } while (0)
;     __device__ __forceinline__ void operator()(const f32x4 (&acc)[2][2][4][2], const Unit& u, int wr, int wc, int fr, int fq) const {
;         const float sc = cB * S_MRG;
;         const bf16* pb = P + (size_t)(u.pm * 256 + wr * 64 + fr) * PNP + (u.pn * 256 + wc * 32 + 8 * fq) + PGB;
;         unsigned char* ob = O + (size_t)(u.pm * 256 + wr * 64 + fr) * DM + (u.pn * 256 + wc * 32 + 8 * fq);
;         asm volatile("" : "+v"(pb), "+v"(ob));
;         v4u G0[2], G1[2];
;     ...
;         ME_LOAD(G0, 0); ME_LOAD(G1, 1); ME_STORE(G0, 0); ME_LOAD(G0, 2); ME_STORE(G1, 1); ME_LOAD(G1, 3); ME_STORE(G0, 2); ME_LOAD(G0, 4); ME_STORE(G1, 3); ME_LOAD(G1, 5);
;         ME_STORE(G0, 4); ME_LOAD(G0, 6); ME_STORE(G1, 5); ME_LOAD(G1, 7); ME_STORE(G0, 6); ME_STORE(G1, 7);
;     ...
;     }
	v_lshlrev_b32_e32 v8, 16, v2
	v_and_b32_e32 v2, 0xffff0000, v2
	v_cvt_pk_fp8_f32 v23, v6, v7 op_sel:[0,0,1]
	v_max_f32_e32 v8, v8, v8
	v_max_f32_e32 v2, v2, v2
	v_max_f32_e32 v8, 0xda24260, v8
	v_max_f32_e32 v9, 0xda24260, v2
	v_add_co_u32_e32 v6, vcc, s21, v14
	v_pk_mul_f32 v[8:9], v[8:9], s[18:19] op_sel_hi:[1,0]
	s_nop 0
	v_addc_co_u32_e32 v7, vcc, 0, v15, vcc
	v_lshlrev_b32_e32 v2, 16, v3
	v_and_b32_e32 v3, 0xffff0000, v3
	v_pk_mul_f32 v[8:9], v[130:131], v[8:9]
	global_store_dwordx2 v[6:7], v[22:23], off
	v_max_f32_e32 v2, v2, v2
	v_max_f32_e32 v3, v3, v3
	v_lshlrev_b32_e32 v22, 16, v4
	v_and_b32_e32 v4, 0xffff0000, v4
	v_med3_f32 v24, v8, s51, v187
	v_med3_f32 v9, v9, s51, v187
	v_mov_b32_e32 v8, 0
	v_max_f32_e32 v2, 0xda24260, v2
	v_max_f32_e32 v3, 0xda24260, v3
	v_max_f32_e32 v22, v22, v22
	v_max_f32_e32 v4, v4, v4
	v_cvt_pk_fp8_f32 v8, v24, v9
	v_pk_mul_f32 v[2:3], v[2:3], s[18:19] op_sel_hi:[1,0]
	v_max_f32_e32 v22, 0xda24260, v22
	v_max_f32_e32 v23, 0xda24260, v4
	v_pk_mul_f32 v[2:3], v[132:133], v[2:3]
	v_pk_mul_f32 v[22:23], v[22:23], s[18:19] op_sel_hi:[1,0]
	v_lshlrev_b32_e32 v4, 16, v5
	v_and_b32_e32 v5, 0xffff0000, v5
	v_pk_mul_f32 v[22:23], v[126:127], v[22:23]
	v_med3_f32 v2, v2, s51, v187
	v_med3_f32 v3, v3, s51, v187
	v_max_f32_e32 v4, v4, v4
	v_max_f32_e32 v5, v5, v5
	v_cvt_pk_fp8_f32 v8, v2, v3 op_sel:[0,0,1]
	v_med3_f32 v2, v22, s51, v187
	v_med3_f32 v3, v23, s51, v187
	v_mov_b32_e32 v9, 0
	v_max_f32_e32 v4, 0xda24260, v4
	v_max_f32_e32 v5, 0xda24260, v5
	v_cvt_pk_fp8_f32 v9, v2, v3
	v_pk_mul_f32 v[4:5], v[4:5], s[18:19] op_sel_hi:[1,0]
	s_mov_b32 s21, 0x19e000
	v_pk_mul_f32 v[4:5], v[128:129], v[4:5]
	s_nop 0
	v_med3_f32 v2, v4, s51, v187
	v_med3_f32 v3, v5, s51, v187
	v_cvt_pk_fp8_f32 v9, v2, v3 op_sel:[0,0,1]
	v_add_co_u32_e32 v2, vcc, s21, v16
	s_mov_b32 s21, 0x20000
	global_store_dwordx2 v[6:7], v[8:9], off offset:128
	v_addc_co_u32_e32 v3, vcc, 0, v17, vcc
	global_load_dwordx4 v[22:25], v[2:3], off nt
	s_nop 0
	global_load_dwordx4 v[2:5], v[2:3], off offset:256 nt
	s_waitcnt vmcnt(5)
	v_lshlrev_b32_e32 v6, 16, v18
	v_and_b32_e32 v7, 0xffff0000, v18
	v_max_f32_e32 v6, v6, v6
	v_max_f32_e32 v7, v7, v7
	v_max_f32_e32 v6, 0xda24260, v6
	v_max_f32_e32 v7, 0xda24260, v7
	v_pk_mul_f32 v[6:7], v[6:7], s[18:19] op_sel_hi:[1,0]
	v_lshlrev_b32_e32 v8, 16, v19
	v_and_b32_e32 v9, 0xffff0000, v19
	v_pk_mul_f32 v[6:7], v[122:123], v[6:7]
	v_max_f32_e32 v8, v8, v8
	v_max_f32_e32 v9, v9, v9
	v_lshlrev_b32_e32 v18, 16, v20
	v_and_b32_e32 v19, 0xffff0000, v20
	v_med3_f32 v27, v6, s51, v187
	v_med3_f32 v7, v7, s51, v187
	v_mov_b32_e32 v6, 0
	v_max_f32_e32 v8, 0xda24260, v8
	v_max_f32_e32 v9, 0xda24260, v9
	v_max_f32_e32 v18, v18, v18
	v_max_f32_e32 v19, v19, v19
	v_cvt_pk_fp8_f32 v6, v27, v7
	v_pk_mul_f32 v[8:9], v[8:9], s[18:19] op_sel_hi:[1,0]
	v_max_f32_e32 v18, 0xda24260, v18
	v_max_f32_e32 v19, 0xda24260, v19
	v_pk_mul_f32 v[8:9], v[124:125], v[8:9]
	v_pk_mul_f32 v[18:19], v[18:19], s[18:19] op_sel_hi:[1,0]
	v_lshlrev_b32_e32 v20, 16, v21
	v_and_b32_e32 v21, 0xffff0000, v21
	v_pk_mul_f32 v[18:19], v[118:119], v[18:19]
	v_med3_f32 v7, v8, s51, v187
	v_med3_f32 v8, v9, s51, v187
	v_max_f32_e32 v20, v20, v20
	v_max_f32_e32 v21, v21, v21
	v_cvt_pk_fp8_f32 v6, v7, v8 op_sel:[0,0,1]
	v_med3_f32 v8, v18, s51, v187
	v_med3_f32 v9, v19, s51, v187
	v_mov_b32_e32 v7, 0
	v_max_f32_e32 v20, 0xda24260, v20
	v_max_f32_e32 v21, 0xda24260, v21
	v_cvt_pk_fp8_f32 v7, v8, v9
	v_pk_mul_f32 v[20:21], v[20:21], s[18:19] op_sel_hi:[1,0]
	s_waitcnt vmcnt(4)
	v_lshlrev_b32_e32 v18, 16, v12
	v_pk_mul_f32 v[20:21], v[120:121], v[20:21]
	v_and_b32_e32 v12, 0xffff0000, v12
	v_med3_f32 v8, v20, s51, v187
	v_med3_f32 v9, v21, s51, v187
	v_cvt_pk_fp8_f32 v7, v8, v9 op_sel:[0,0,1]
	v_add_co_u32_e32 v8, vcc, s21, v14
	v_max_f32_e32 v18, v18, v18
	s_nop 0
	v_addc_co_u32_e32 v9, vcc, 0, v15, vcc
	global_store_dwordx2 v[8:9], v[6:7], off
	v_lshlrev_b32_e32 v6, 16, v10
	v_and_b32_e32 v7, 0xffff0000, v10
	v_max_f32_e32 v6, v6, v6
	v_max_f32_e32 v7, v7, v7
	v_max_f32_e32 v6, 0xda24260, v6
	v_max_f32_e32 v7, 0xda24260, v7
	v_pk_mul_f32 v[6:7], v[6:7], s[18:19] op_sel_hi:[1,0]
	v_lshlrev_b32_e32 v10, 16, v11
	v_and_b32_e32 v11, 0xffff0000, v11
	v_pk_mul_f32 v[6:7], v[114:115], v[6:7]
	v_max_f32_e32 v10, v10, v10
	v_max_f32_e32 v11, v11, v11
	v_med3_f32 v20, v6, s51, v187
	v_med3_f32 v7, v7, s51, v187
	v_mov_b32_e32 v6, 0
	v_max_f32_e32 v10, 0xda24260, v10
	v_max_f32_e32 v11, 0xda24260, v11
	v_max_f32_e32 v12, v12, v12
	v_cvt_pk_fp8_f32 v6, v20, v7
	v_pk_mul_f32 v[10:11], v[10:11], s[18:19] op_sel_hi:[1,0]
	v_max_f32_e32 v18, 0xda24260, v18
	v_max_f32_e32 v19, 0xda24260, v12
	v_pk_mul_f32 v[10:11], v[116:117], v[10:11]
	v_pk_mul_f32 v[18:19], v[18:19], s[18:19] op_sel_hi:[1,0]
	v_lshlrev_b32_e32 v12, 16, v13
	v_and_b32_e32 v13, 0xffff0000, v13
	v_pk_mul_f32 v[18:19], v[110:111], v[18:19]
	v_med3_f32 v7, v10, s51, v187
	v_med3_f32 v10, v11, s51, v187
	v_max_f32_e32 v12, v12, v12
	v_max_f32_e32 v13, v13, v13
	v_cvt_pk_fp8_f32 v6, v7, v10 op_sel:[0,0,1]
	v_med3_f32 v10, v18, s51, v187
	v_med3_f32 v11, v19, s51, v187
	v_mov_b32_e32 v7, 0
	v_max_f32_e32 v12, 0xda24260, v12
	v_max_f32_e32 v13, 0xda24260, v13
	v_cvt_pk_fp8_f32 v7, v10, v11
	s_waitcnt vmcnt(2)
; #define ME_LOAD(G_, s_) do { const bf16* q_ = pb + (size_t)(((s_) >> 2) * 128 + ((s_) & 3) * 16) * PNP; G_[0] = *(const GAS v4u*)q_; G_[1] = *(const GAS v4u*)(q_ + 128); } while (0)
;     __device__ __forceinline__ void operator()(const f32x4 (&acc)[2][2][4][2], const Unit& u, int wr, int wc, int fr, int fq) const {
;         const float sc = cB * S_MRG;
;         const bf16* pb = P + (size_t)(u.pm * 256 + wr * 64 + fr) * PNP + (u.pn * 256 + wc * 32 + 8 * fq) + PGB;
;         unsigned char* ob = O + (size_t)(u.pm * 256 + wr * 64 + fr) * DM + (u.pn * 256 + wc * 32 + 8 * fq);
;         asm volatile("" : "+v"(pb), "+v"(ob));
;         v4u G0[2], G1[2];
;     ...
;         ME_LOAD(G0, 0); ME_LOAD(G1, 1); ME_STORE(G0, 0); ME_LOAD(G0, 2); ME_STORE(G1, 1); ME_LOAD(G1, 3); ME_STORE(G0, 2); ME_LOAD(G0, 4); ME_STORE(G1, 3); ME_LOAD(G1, 5);
;         ME_STORE(G0, 4); ME_LOAD(G0, 6); ME_STORE(G1, 5); ME_LOAD(G1, 7); ME_STORE(G0, 6); ME_STORE(G1, 7);
;     ...
;     }
	v_lshlrev_b32_e32 v18, 16, v22
	v_and_b32_e32 v19, 0xffff0000, v22
	v_pk_mul_f32 v[12:13], v[12:13], s[18:19] op_sel_hi:[1,0]
	v_max_f32_e32 v18, v18, v18
	v_max_f32_e32 v19, v19, v19
	v_pk_mul_f32 v[12:13], v[112:113], v[12:13]
	v_max_f32_e32 v18, 0xda24260, v18
	v_max_f32_e32 v19, 0xda24260, v19
	v_med3_f32 v10, v12, s51, v187
	v_med3_f32 v11, v13, s51, v187
	v_pk_mul_f32 v[18:19], v[18:19], s[18:19] op_sel_hi:[1,0]
	v_cvt_pk_fp8_f32 v7, v10, v11 op_sel:[0,0,1]
	v_lshlrev_b32_e32 v20, 16, v23
	v_and_b32_e32 v21, 0xffff0000, v23
	v_pk_mul_f32 v[18:19], v[106:107], v[18:19]
	v_max_f32_e32 v20, v20, v20
	v_max_f32_e32 v21, v21, v21
	v_lshlrev_b32_e32 v22, 16, v24
	v_and_b32_e32 v23, 0xffff0000, v24
	v_med3_f32 v27, v18, s51, v187
	v_med3_f32 v19, v19, s51, v187
	v_mov_b32_e32 v18, 0
	v_max_f32_e32 v20, 0xda24260, v20
	v_max_f32_e32 v21, 0xda24260, v21
	v_max_f32_e32 v22, v22, v22
	v_max_f32_e32 v23, v23, v23
	v_cvt_pk_fp8_f32 v18, v27, v19
	s_mov_b32 s21, 0x450000
	v_pk_mul_f32 v[20:21], v[20:21], s[18:19] op_sel_hi:[1,0]
	v_max_f32_e32 v22, 0xda24260, v22
	v_max_f32_e32 v23, 0xda24260, v23
	global_store_dwordx2 v[8:9], v[6:7], off offset:128
	v_add_co_u32_e32 v6, vcc, s21, v16
	v_pk_mul_f32 v[20:21], v[108:109], v[20:21]
	v_pk_mul_f32 v[22:23], v[22:23], s[18:19] op_sel_hi:[1,0]
	v_addc_co_u32_e32 v7, vcc, 0, v17, vcc
	v_lshlrev_b32_e32 v24, 16, v25
	v_and_b32_e32 v25, 0xffff0000, v25
	v_pk_mul_f32 v[22:23], v[102:103], v[22:23]
	v_med3_f32 v19, v20, s51, v187
	v_med3_f32 v20, v21, s51, v187
	global_load_dwordx4 v[10:13], v[6:7], off nt
	s_nop 0
	global_load_dwordx4 v[6:9], v[6:7], off offset:256 nt
	v_max_f32_e32 v24, v24, v24
	v_max_f32_e32 v25, v25, v25
	v_cvt_pk_fp8_f32 v18, v19, v20 op_sel:[0,0,1]
	v_med3_f32 v20, v22, s51, v187
	v_med3_f32 v21, v23, s51, v187
	v_mov_b32_e32 v19, 0
	v_max_f32_e32 v24, 0xda24260, v24
	v_max_f32_e32 v25, 0xda24260, v25
	v_cvt_pk_fp8_f32 v19, v20, v21
	v_pk_mul_f32 v[24:25], v[24:25], s[18:19] op_sel_hi:[1,0]
	s_mov_b32 s21, 0x30000
	v_pk_mul_f32 v[24:25], v[104:105], v[24:25]
	s_waitcnt vmcnt(4)
	v_lshlrev_b32_e32 v22, 16, v4
	v_med3_f32 v20, v24, s51, v187
	v_med3_f32 v21, v25, s51, v187
	v_cvt_pk_fp8_f32 v19, v20, v21 op_sel:[0,0,1]
	v_add_co_u32_e32 v20, vcc, s21, v14
	v_and_b32_e32 v4, 0xffff0000, v4
	s_nop 0
	v_addc_co_u32_e32 v21, vcc, 0, v15, vcc
	global_store_dwordx2 v[20:21], v[18:19], off
	v_lshlrev_b32_e32 v18, 16, v2
	v_and_b32_e32 v2, 0xffff0000, v2
	v_max_f32_e32 v18, v18, v18
	v_max_f32_e32 v2, v2, v2
	v_max_f32_e32 v18, 0xda24260, v18
	v_max_f32_e32 v19, 0xda24260, v2
	v_pk_mul_f32 v[18:19], v[18:19], s[18:19] op_sel_hi:[1,0]
	v_lshlrev_b32_e32 v2, 16, v3
	v_and_b32_e32 v3, 0xffff0000, v3
	v_pk_mul_f32 v[18:19], v[98:99], v[18:19]
	v_max_f32_e32 v2, v2, v2
	v_max_f32_e32 v3, v3, v3
	v_med3_f32 v24, v18, s51, v187
	v_med3_f32 v19, v19, s51, v187
	v_mov_b32_e32 v18, 0
	v_max_f32_e32 v2, 0xda24260, v2
	v_max_f32_e32 v3, 0xda24260, v3
	v_max_f32_e32 v22, v22, v22
	v_max_f32_e32 v4, v4, v4
	v_cvt_pk_fp8_f32 v18, v24, v19
	v_pk_mul_f32 v[2:3], v[2:3], s[18:19] op_sel_hi:[1,0]
	v_max_f32_e32 v22, 0xda24260, v22
	v_max_f32_e32 v23, 0xda24260, v4
	v_pk_mul_f32 v[2:3], v[100:101], v[2:3]
	v_pk_mul_f32 v[22:23], v[22:23], s[18:19] op_sel_hi:[1,0]
	v_lshlrev_b32_e32 v4, 16, v5
	v_and_b32_e32 v5, 0xffff0000, v5
	v_pk_mul_f32 v[22:23], v[94:95], v[22:23]
	v_med3_f32 v2, v2, s51, v187
	v_med3_f32 v3, v3, s51, v187
	v_max_f32_e32 v4, v4, v4
	v_max_f32_e32 v5, v5, v5
	v_cvt_pk_fp8_f32 v18, v2, v3 op_sel:[0,0,1]
	v_med3_f32 v2, v22, s51, v187
	v_med3_f32 v3, v23, s51, v187
	v_mov_b32_e32 v19, 0
	v_max_f32_e32 v4, 0xda24260, v4
	v_max_f32_e32 v5, 0xda24260, v5
	v_cvt_pk_fp8_f32 v19, v2, v3
	v_pk_mul_f32 v[4:5], v[4:5], s[18:19] op_sel_hi:[1,0]
	s_mov_b32 s21, 0x4da000
	v_pk_mul_f32 v[4:5], v[96:97], v[4:5]
	s_waitcnt vmcnt(2)
	v_lshlrev_b32_e32 v22, 16, v10
	v_med3_f32 v2, v4, s51, v187
	v_med3_f32 v3, v5, s51, v187
	v_cvt_pk_fp8_f32 v19, v2, v3 op_sel:[0,0,1]
	v_add_co_u32_e32 v2, vcc, s21, v16
	v_and_b32_e32 v10, 0xffff0000, v10
	global_store_dwordx2 v[20:21], v[18:19], off offset:128
	v_addc_co_u32_e32 v3, vcc, 0, v17, vcc
	global_load_dwordx4 v[18:21], v[2:3], off nt
	s_nop 0
	global_load_dwordx4 v[2:5], v[2:3], off offset:256 nt
	v_max_f32_e32 v22, v22, v22
	v_max_f32_e32 v10, v10, v10
	v_max_f32_e32 v22, 0xda24260, v22
	v_max_f32_e32 v23, 0xda24260, v10
	v_pk_mul_f32 v[22:23], v[22:23], s[18:19] op_sel_hi:[1,0]
	v_lshlrev_b32_e32 v10, 16, v11
	v_and_b32_e32 v11, 0xffff0000, v11
	v_pk_mul_f32 v[22:23], v[90:91], v[22:23]
	v_max_f32_e32 v10, v10, v10
	v_max_f32_e32 v11, v11, v11
	v_lshlrev_b32_e32 v24, 16, v12
	v_and_b32_e32 v12, 0xffff0000, v12
	v_med3_f32 v27, v22, s51, v187
	v_med3_f32 v23, v23, s51, v187
	v_mov_b32_e32 v22, 0
	v_max_f32_e32 v10, 0xda24260, v10
	v_max_f32_e32 v11, 0xda24260, v11
	v_max_f32_e32 v24, v24, v24
	v_max_f32_e32 v12, v12, v12
	v_cvt_pk_fp8_f32 v22, v27, v23
	v_pk_mul_f32 v[10:11], v[10:11], s[18:19] op_sel_hi:[1,0]
	v_max_f32_e32 v24, 0xda24260, v24
	v_max_f32_e32 v25, 0xda24260, v12
	v_pk_mul_f32 v[10:11], v[92:93], v[10:11]
	v_pk_mul_f32 v[24:25], v[24:25], s[18:19] op_sel_hi:[1,0]
	v_lshlrev_b32_e32 v12, 16, v13
	v_and_b32_e32 v13, 0xffff0000, v13
	v_pk_mul_f32 v[24:25], v[86:87], v[24:25]
	v_med3_f32 v10, v10, s51, v187
	v_med3_f32 v11, v11, s51, v187
	v_max_f32_e32 v12, v12, v12
	v_max_f32_e32 v13, v13, v13
	v_cvt_pk_fp8_f32 v22, v10, v11 op_sel:[0,0,1]
	v_med3_f32 v10, v24, s51, v187
	v_med3_f32 v11, v25, s51, v187
	v_mov_b32_e32 v23, 0
	v_max_f32_e32 v12, 0xda24260, v12
	v_max_f32_e32 v13, 0xda24260, v13
	v_cvt_pk_fp8_f32 v23, v10, v11
	v_pk_mul_f32 v[12:13], v[12:13], s[18:19] op_sel_hi:[1,0]
	s_mov_b32 s21, 0x80000
	v_pk_mul_f32 v[12:13], v[88:89], v[12:13]
	s_nop 0
	v_med3_f32 v10, v12, s51, v187
	v_med3_f32 v11, v13, s51, v187
	s_waitcnt vmcnt(4)
; #define ME_LOAD(G_, s_) do { const bf16* q_ = pb + (size_t)(((s_) >> 2) * 128 + ((s_) & 3) * 16) * PNP; G_[0] = *(const GAS v4u*)q_; G_[1] = *(const GAS v4u*)(q_ + 128); } while (0)
;     __device__ __forceinline__ void operator()(const f32x4 (&acc)[2][2][4][2], const Unit& u, int wr, int wc, int fr, int fq) const {
;         const float sc = cB * S_MRG;
;         const bf16* pb = P + (size_t)(u.pm * 256 + wr * 64 + fr) * PNP + (u.pn * 256 + wc * 32 + 8 * fq) + PGB;
;         unsigned char* ob = O + (size_t)(u.pm * 256 + wr * 64 + fr) * DM + (u.pn * 256 + wc * 32 + 8 * fq);
;         asm volatile("" : "+v"(pb), "+v"(ob));
;         v4u G0[2], G1[2];
;     ...
;         ME_LOAD(G0, 0); ME_LOAD(G1, 1); ME_STORE(G0, 0); ME_LOAD(G0, 2); ME_STORE(G1, 1); ME_LOAD(G1, 3); ME_STORE(G0, 2); ME_LOAD(G0, 4); ME_STORE(G1, 3); ME_LOAD(G1, 5);
;         ME_STORE(G0, 4); ME_LOAD(G0, 6); ME_STORE(G1, 5); ME_LOAD(G1, 7); ME_STORE(G0, 6); ME_STORE(G1, 7);
;     ...
;     }
	v_lshlrev_b32_e32 v12, 16, v6
	v_and_b32_e32 v6, 0xffff0000, v6
	v_cvt_pk_fp8_f32 v23, v10, v11 op_sel:[0,0,1]
	v_max_f32_e32 v12, v12, v12
	v_max_f32_e32 v6, v6, v6
	v_max_f32_e32 v12, 0xda24260, v12
	v_max_f32_e32 v13, 0xda24260, v6
	v_add_co_u32_e32 v10, vcc, s21, v14
	v_pk_mul_f32 v[12:13], v[12:13], s[18:19] op_sel_hi:[1,0]
	s_nop 0
	v_addc_co_u32_e32 v11, vcc, 0, v15, vcc
	v_lshlrev_b32_e32 v6, 16, v7
	v_and_b32_e32 v7, 0xffff0000, v7
	v_pk_mul_f32 v[12:13], v[82:83], v[12:13]
	global_store_dwordx2 v[10:11], v[22:23], off
	v_max_f32_e32 v6, v6, v6
	v_max_f32_e32 v7, v7, v7
	v_lshlrev_b32_e32 v22, 16, v8
	v_and_b32_e32 v8, 0xffff0000, v8
	v_med3_f32 v24, v12, s51, v187
	v_med3_f32 v13, v13, s51, v187
	v_mov_b32_e32 v12, 0
	v_max_f32_e32 v6, 0xda24260, v6
	v_max_f32_e32 v7, 0xda24260, v7
	v_max_f32_e32 v22, v22, v22
	v_max_f32_e32 v8, v8, v8
	v_cvt_pk_fp8_f32 v12, v24, v13
	v_pk_mul_f32 v[6:7], v[6:7], s[18:19] op_sel_hi:[1,0]
	v_max_f32_e32 v22, 0xda24260, v22
	v_max_f32_e32 v23, 0xda24260, v8
	v_pk_mul_f32 v[6:7], v[84:85], v[6:7]
	v_pk_mul_f32 v[22:23], v[22:23], s[18:19] op_sel_hi:[1,0]
	v_lshlrev_b32_e32 v8, 16, v9
	v_and_b32_e32 v9, 0xffff0000, v9
	v_pk_mul_f32 v[22:23], v[78:79], v[22:23]
	v_med3_f32 v6, v6, s51, v187
	v_med3_f32 v7, v7, s51, v187
	v_max_f32_e32 v8, v8, v8
	v_max_f32_e32 v9, v9, v9
	v_cvt_pk_fp8_f32 v12, v6, v7 op_sel:[0,0,1]
	v_med3_f32 v6, v22, s51, v187
	v_med3_f32 v7, v23, s51, v187
	v_mov_b32_e32 v13, 0
	v_max_f32_e32 v8, 0xda24260, v8
	v_max_f32_e32 v9, 0xda24260, v9
	v_cvt_pk_fp8_f32 v13, v6, v7
	v_pk_mul_f32 v[8:9], v[8:9], s[18:19] op_sel_hi:[1,0]
	s_waitcnt vmcnt(2)
	v_lshlrev_b32_e32 v22, 16, v18
	v_pk_mul_f32 v[8:9], v[80:81], v[8:9]
	v_and_b32_e32 v18, 0xffff0000, v18
	v_med3_f32 v6, v8, s51, v187
	v_med3_f32 v7, v9, s51, v187
	v_cvt_pk_fp8_f32 v13, v6, v7 op_sel:[0,0,1]
	v_max_f32_e32 v22, v22, v22
	v_max_f32_e32 v18, v18, v18
	s_mov_b32 s21, 0x564000
	v_max_f32_e32 v22, 0xda24260, v22
	v_max_f32_e32 v23, 0xda24260, v18
	v_add_co_u32_e32 v6, vcc, s21, v16
	v_pk_mul_f32 v[22:23], v[22:23], s[18:19] op_sel_hi:[1,0]
	global_store_dwordx2 v[10:11], v[12:13], off offset:128
	v_addc_co_u32_e32 v7, vcc, 0, v17, vcc
	v_lshlrev_b32_e32 v18, 16, v19
	v_and_b32_e32 v19, 0xffff0000, v19
	v_pk_mul_f32 v[22:23], v[74:75], v[22:23]
	global_load_dwordx4 v[10:13], v[6:7], off nt
	s_nop 0
	global_load_dwordx4 v[6:9], v[6:7], off offset:256 nt
	v_max_f32_e32 v18, v18, v18
	v_max_f32_e32 v19, v19, v19
	v_lshlrev_b32_e32 v24, 16, v20
	v_and_b32_e32 v20, 0xffff0000, v20
	v_med3_f32 v27, v22, s51, v187
	v_med3_f32 v23, v23, s51, v187
	v_mov_b32_e32 v22, 0
	v_max_f32_e32 v18, 0xda24260, v18
	v_max_f32_e32 v19, 0xda24260, v19
	v_max_f32_e32 v24, v24, v24
	v_max_f32_e32 v20, v20, v20
	v_cvt_pk_fp8_f32 v22, v27, v23
	v_pk_mul_f32 v[18:19], v[18:19], s[18:19] op_sel_hi:[1,0]
	v_max_f32_e32 v24, 0xda24260, v24
	v_max_f32_e32 v25, 0xda24260, v20
	v_pk_mul_f32 v[18:19], v[76:77], v[18:19]
	v_pk_mul_f32 v[24:25], v[24:25], s[18:19] op_sel_hi:[1,0]
	v_lshlrev_b32_e32 v20, 16, v21
	v_and_b32_e32 v21, 0xffff0000, v21
	v_pk_mul_f32 v[24:25], v[70:71], v[24:25]
	v_med3_f32 v18, v18, s51, v187
	v_med3_f32 v19, v19, s51, v187
	v_max_f32_e32 v20, v20, v20
	v_max_f32_e32 v21, v21, v21
	v_cvt_pk_fp8_f32 v22, v18, v19 op_sel:[0,0,1]
	v_med3_f32 v18, v24, s51, v187
	v_med3_f32 v19, v25, s51, v187
	v_mov_b32_e32 v23, 0
	v_max_f32_e32 v20, 0xda24260, v20
	v_max_f32_e32 v21, 0xda24260, v21
	v_cvt_pk_fp8_f32 v23, v18, v19
	v_pk_mul_f32 v[20:21], v[20:21], s[18:19] op_sel_hi:[1,0]
	s_mov_b32 s21, 0x90000
	v_pk_mul_f32 v[20:21], v[72:73], v[20:21]
	s_nop 0
	v_med3_f32 v18, v20, s51, v187
	v_med3_f32 v19, v21, s51, v187
	s_waitcnt vmcnt(4)
	v_lshlrev_b32_e32 v20, 16, v2
	v_and_b32_e32 v2, 0xffff0000, v2
	v_cvt_pk_fp8_f32 v23, v18, v19 op_sel:[0,0,1]
	v_max_f32_e32 v20, v20, v20
	v_max_f32_e32 v2, v2, v2
	v_max_f32_e32 v20, 0xda24260, v20
	v_max_f32_e32 v21, 0xda24260, v2
	v_add_co_u32_e32 v18, vcc, s21, v14
	v_pk_mul_f32 v[20:21], v[20:21], s[18:19] op_sel_hi:[1,0]
	s_nop 0
	v_addc_co_u32_e32 v19, vcc, 0, v15, vcc
	v_lshlrev_b32_e32 v2, 16, v3
	v_and_b32_e32 v3, 0xffff0000, v3
	v_pk_mul_f32 v[20:21], v[66:67], v[20:21]
	global_store_dwordx2 v[18:19], v[22:23], off
	v_max_f32_e32 v2, v2, v2
	v_max_f32_e32 v3, v3, v3
	v_lshlrev_b32_e32 v22, 16, v4
	v_and_b32_e32 v4, 0xffff0000, v4
	v_med3_f32 v24, v20, s51, v187
	v_med3_f32 v21, v21, s51, v187
	v_mov_b32_e32 v20, 0
	v_max_f32_e32 v2, 0xda24260, v2
	v_max_f32_e32 v3, 0xda24260, v3
	v_max_f32_e32 v22, v22, v22
	v_max_f32_e32 v4, v4, v4
	v_cvt_pk_fp8_f32 v20, v24, v21
	v_pk_mul_f32 v[2:3], v[2:3], s[18:19] op_sel_hi:[1,0]
	v_max_f32_e32 v22, 0xda24260, v22
	v_max_f32_e32 v23, 0xda24260, v4
	v_pk_mul_f32 v[2:3], v[68:69], v[2:3]
	v_pk_mul_f32 v[22:23], v[22:23], s[18:19] op_sel_hi:[1,0]
	v_lshlrev_b32_e32 v4, 16, v5
	v_and_b32_e32 v5, 0xffff0000, v5
	v_pk_mul_f32 v[22:23], v[62:63], v[22:23]
	v_med3_f32 v2, v2, s51, v187
	v_med3_f32 v3, v3, s51, v187
	v_max_f32_e32 v4, v4, v4
	v_max_f32_e32 v5, v5, v5
	v_cvt_pk_fp8_f32 v20, v2, v3 op_sel:[0,0,1]
	v_med3_f32 v2, v22, s51, v187
	v_med3_f32 v3, v23, s51, v187
	v_mov_b32_e32 v21, 0
	v_max_f32_e32 v4, 0xda24260, v4
	v_max_f32_e32 v5, 0xda24260, v5
	v_cvt_pk_fp8_f32 v21, v2, v3
	v_pk_mul_f32 v[4:5], v[4:5], s[18:19] op_sel_hi:[1,0]
	s_mov_b32 s21, 0x5ee000
	v_pk_mul_f32 v[4:5], v[64:65], v[4:5]
	s_waitcnt vmcnt(2)
; #define ME_LOAD(G_, s_) do { const bf16* q_ = pb + (size_t)(((s_) >> 2) * 128 + ((s_) & 3) * 16) * PNP; G_[0] = *(const GAS v4u*)q_; G_[1] = *(const GAS v4u*)(q_ + 128); } while (0)
;     __device__ __forceinline__ void operator()(const f32x4 (&acc)[2][2][4][2], const Unit& u, int wr, int wc, int fr, int fq) const {
;         const float sc = cB * S_MRG;
;         const bf16* pb = P + (size_t)(u.pm * 256 + wr * 64 + fr) * PNP + (u.pn * 256 + wc * 32 + 8 * fq) + PGB;
;         unsigned char* ob = O + (size_t)(u.pm * 256 + wr * 64 + fr) * DM + (u.pn * 256 + wc * 32 + 8 * fq);
;         asm volatile("" : "+v"(pb), "+v"(ob));
;         v4u G0[2], G1[2];
;     ...
;         ME_LOAD(G0, 0); ME_LOAD(G1, 1); ME_STORE(G0, 0); ME_LOAD(G0, 2); ME_STORE(G1, 1); ME_LOAD(G1, 3); ME_STORE(G0, 2); ME_LOAD(G0, 4); ME_STORE(G1, 3); ME_LOAD(G1, 5);
;         ME_STORE(G0, 4); ME_LOAD(G0, 6); ME_STORE(G1, 5); ME_LOAD(G1, 7); ME_STORE(G0, 6); ME_STORE(G1, 7);
;     ...
;     }
	v_lshlrev_b32_e32 v22, 16, v12
	v_med3_f32 v2, v4, s51, v187
	v_med3_f32 v3, v5, s51, v187
	v_cvt_pk_fp8_f32 v21, v2, v3 op_sel:[0,0,1]
	v_add_co_u32_e32 v2, vcc, s21, v16
	v_and_b32_e32 v12, 0xffff0000, v12
	global_store_dwordx2 v[18:19], v[20:21], off offset:128
	v_addc_co_u32_e32 v3, vcc, 0, v17, vcc
	global_load_dwordx4 v[16:19], v[2:3], off nt
	s_nop 0
	global_load_dwordx4 v[2:5], v[2:3], off offset:256 nt
	v_lshlrev_b32_e32 v20, 16, v10
	v_and_b32_e32 v10, 0xffff0000, v10
	v_max_f32_e32 v20, v20, v20
	v_max_f32_e32 v10, v10, v10
	v_max_f32_e32 v20, 0xda24260, v20
	v_max_f32_e32 v21, 0xda24260, v10
	v_pk_mul_f32 v[20:21], v[20:21], s[18:19] op_sel_hi:[1,0]
	v_lshlrev_b32_e32 v10, 16, v11
	v_and_b32_e32 v11, 0xffff0000, v11
	v_pk_mul_f32 v[20:21], v[58:59], v[20:21]
	v_max_f32_e32 v10, v10, v10
	v_max_f32_e32 v11, v11, v11
	v_med3_f32 v24, v20, s51, v187
	v_med3_f32 v21, v21, s51, v187
	v_mov_b32_e32 v20, 0
	v_max_f32_e32 v10, 0xda24260, v10
	v_max_f32_e32 v11, 0xda24260, v11
	v_max_f32_e32 v22, v22, v22
	v_max_f32_e32 v12, v12, v12
	v_cvt_pk_fp8_f32 v20, v24, v21
	v_pk_mul_f32 v[10:11], v[10:11], s[18:19] op_sel_hi:[1,0]
	v_max_f32_e32 v22, 0xda24260, v22
	v_max_f32_e32 v23, 0xda24260, v12
	v_pk_mul_f32 v[10:11], v[60:61], v[10:11]
	v_pk_mul_f32 v[22:23], v[22:23], s[18:19] op_sel_hi:[1,0]
	v_lshlrev_b32_e32 v12, 16, v13
	v_and_b32_e32 v13, 0xffff0000, v13
	v_pk_mul_f32 v[22:23], v[54:55], v[22:23]
	v_med3_f32 v10, v10, s51, v187
	v_med3_f32 v11, v11, s51, v187
	v_max_f32_e32 v12, v12, v12
	v_max_f32_e32 v13, v13, v13
	v_cvt_pk_fp8_f32 v20, v10, v11 op_sel:[0,0,1]
	v_med3_f32 v10, v22, s51, v187
	v_med3_f32 v11, v23, s51, v187
	v_mov_b32_e32 v21, 0
	v_max_f32_e32 v12, 0xda24260, v12
	v_max_f32_e32 v13, 0xda24260, v13
	v_cvt_pk_fp8_f32 v21, v10, v11
	v_pk_mul_f32 v[12:13], v[12:13], s[18:19] op_sel_hi:[1,0]
	s_mov_b32 s21, 0xa0000
	v_pk_mul_f32 v[12:13], v[56:57], v[12:13]
	s_nop 0
	v_med3_f32 v10, v12, s51, v187
	v_med3_f32 v11, v13, s51, v187
	s_waitcnt vmcnt(4)
	v_lshlrev_b32_e32 v12, 16, v6
	v_and_b32_e32 v6, 0xffff0000, v6
	v_cvt_pk_fp8_f32 v21, v10, v11 op_sel:[0,0,1]
	v_max_f32_e32 v12, v12, v12
	v_max_f32_e32 v6, v6, v6
	v_max_f32_e32 v12, 0xda24260, v12
	v_max_f32_e32 v13, 0xda24260, v6
	v_add_co_u32_e32 v10, vcc, s21, v14
	v_pk_mul_f32 v[12:13], v[12:13], s[18:19] op_sel_hi:[1,0]
	s_nop 0
	v_addc_co_u32_e32 v11, vcc, 0, v15, vcc
	v_lshlrev_b32_e32 v6, 16, v7
	v_and_b32_e32 v7, 0xffff0000, v7
	v_pk_mul_f32 v[12:13], v[50:51], v[12:13]
	global_store_dwordx2 v[10:11], v[20:21], off
	v_max_f32_e32 v6, v6, v6
	v_max_f32_e32 v7, v7, v7
	v_lshlrev_b32_e32 v20, 16, v8
	v_and_b32_e32 v8, 0xffff0000, v8
	v_med3_f32 v22, v12, s51, v187
	v_med3_f32 v13, v13, s51, v187
	v_mov_b32_e32 v12, 0
	v_max_f32_e32 v6, 0xda24260, v6
	v_max_f32_e32 v7, 0xda24260, v7
	v_max_f32_e32 v20, v20, v20
	v_max_f32_e32 v8, v8, v8
	v_cvt_pk_fp8_f32 v12, v22, v13
	v_pk_mul_f32 v[6:7], v[6:7], s[18:19] op_sel_hi:[1,0]
	v_max_f32_e32 v20, 0xda24260, v20
	v_max_f32_e32 v21, 0xda24260, v8
	v_pk_mul_f32 v[6:7], v[52:53], v[6:7]
	v_pk_mul_f32 v[20:21], v[20:21], s[18:19] op_sel_hi:[1,0]
	v_lshlrev_b32_e32 v8, 16, v9
	v_and_b32_e32 v9, 0xffff0000, v9
	v_pk_mul_f32 v[20:21], v[46:47], v[20:21]
	v_med3_f32 v6, v6, s51, v187
	v_med3_f32 v7, v7, s51, v187
	v_max_f32_e32 v8, v8, v8
	v_max_f32_e32 v9, v9, v9
	v_cvt_pk_fp8_f32 v12, v6, v7 op_sel:[0,0,1]
	v_med3_f32 v6, v20, s51, v187
	v_med3_f32 v7, v21, s51, v187
	v_mov_b32_e32 v13, 0
	v_max_f32_e32 v8, 0xda24260, v8
	v_max_f32_e32 v9, 0xda24260, v9
	v_cvt_pk_fp8_f32 v13, v6, v7
	v_pk_mul_f32 v[8:9], v[8:9], s[18:19] op_sel_hi:[1,0]
	s_mov_b32 s21, 0xb0000
	v_pk_mul_f32 v[8:9], v[48:49], v[8:9]
	s_nop 0
	v_med3_f32 v6, v8, s51, v187
	v_med3_f32 v7, v9, s51, v187
	v_cvt_pk_fp8_f32 v13, v6, v7 op_sel:[0,0,1]
	s_waitcnt vmcnt(2)
; #define PG8_BAR __builtin_amdgcn_s_barrier()
; #define ME_LOAD(G_, s_) do { const bf16* q_ = pb + (size_t)(((s_) >> 2) * 128 + ((s_) & 3) * 16) * PNP; G_[0] = *(const GAS v4u*)q_; G_[1] = *(const GAS v4u*)(q_ + 128); } while (0)
;     ...
;         if constexpr (ALIGN_EPI) { if (wr == 0) PG8_BAR; }
;         if constexpr (ES == 1) asm volatile("s_nop 15\n\ts_nop 15" ::: "memory");
;         E(acc, cur, wr, wc, fr, fq); S.done(cur);
;         if (!has_next) break;
; #pragma unroll
;         for (int a = 0; a < 2; ++a)
; #pragma unroll
;             for (int b = 0; b < 2; ++b)
; #pragma unroll
;                 for (int m = 0; m < 4; ++m)
; #pragma unroll
;                     for (int n = 0; n < 2; ++n) acc[a][b][m][n] = (f32x4){0.f, 0.f, 0.f, 0.f};
;         cur = nxt; cA = nA; cB = nB; ++ui;
;         if constexpr (ALIGN_EPI) { if (wr == 1) PG8_BAR; }
;     __device__ __forceinline__ void operator()(const f32x4 (&acc)[2][2][4][2], const Unit& u, int wr, int wc, int fr, int fq) const {
;     ...
;         ME_LOAD(G0, 0); ME_LOAD(G1, 1); ME_STORE(G0, 0); ME_LOAD(G0, 2); ME_STORE(G1, 1); ME_LOAD(G1, 3); ME_STORE(G0, 2); ME_LOAD(G0, 4); ME_STORE(G1, 3); ME_LOAD(G1, 5);
;         ME_STORE(G0, 4); ME_LOAD(G0, 6); ME_STORE(G1, 5); ME_LOAD(G1, 7); ME_STORE(G0, 6); ME_STORE(G1, 7);
	v_lshlrev_b32_e32 v6, 16, v16
	v_and_b32_e32 v7, 0xffff0000, v16
	v_max_f32_e32 v6, v6, v6
	v_max_f32_e32 v7, v7, v7
	v_max_f32_e32 v6, 0xda24260, v6
	v_max_f32_e32 v7, 0xda24260, v7
	v_pk_mul_f32 v[6:7], v[6:7], s[18:19] op_sel_hi:[1,0]
	v_lshlrev_b32_e32 v8, 16, v17
	v_and_b32_e32 v9, 0xffff0000, v17
	v_pk_mul_f32 v[6:7], v[42:43], v[6:7]
	global_store_dwordx2 v[10:11], v[12:13], off offset:128
	v_max_f32_e32 v8, v8, v8
	v_max_f32_e32 v9, v9, v9
	v_lshlrev_b32_e32 v10, 16, v18
	v_and_b32_e32 v11, 0xffff0000, v18
	v_med3_f32 v16, v6, s51, v187
	v_med3_f32 v7, v7, s51, v187
	v_mov_b32_e32 v6, 0
	v_max_f32_e32 v8, 0xda24260, v8
	v_max_f32_e32 v9, 0xda24260, v9
	v_max_f32_e32 v10, v10, v10
	v_max_f32_e32 v11, v11, v11
	v_cvt_pk_fp8_f32 v6, v16, v7
	v_pk_mul_f32 v[8:9], v[8:9], s[18:19] op_sel_hi:[1,0]
	v_max_f32_e32 v10, 0xda24260, v10
	v_max_f32_e32 v11, 0xda24260, v11
	v_pk_mul_f32 v[8:9], v[44:45], v[8:9]
	v_pk_mul_f32 v[10:11], v[10:11], s[18:19] op_sel_hi:[1,0]
	v_lshlrev_b32_e32 v12, 16, v19
	v_and_b32_e32 v13, 0xffff0000, v19
	v_pk_mul_f32 v[10:11], v[38:39], v[10:11]
	v_med3_f32 v7, v8, s51, v187
	v_med3_f32 v8, v9, s51, v187
	v_max_f32_e32 v12, v12, v12
	v_max_f32_e32 v13, v13, v13
	v_cvt_pk_fp8_f32 v6, v7, v8 op_sel:[0,0,1]
	v_med3_f32 v8, v10, s51, v187
	v_med3_f32 v9, v11, s51, v187
	v_mov_b32_e32 v7, 0
	v_max_f32_e32 v12, 0xda24260, v12
	v_max_f32_e32 v13, 0xda24260, v13
	v_cvt_pk_fp8_f32 v7, v8, v9
	v_pk_mul_f32 v[12:13], v[12:13], s[18:19] op_sel_hi:[1,0]
	s_waitcnt vmcnt(2)
	v_lshlrev_b32_e32 v10, 16, v4
	v_pk_mul_f32 v[12:13], v[40:41], v[12:13]
	v_and_b32_e32 v4, 0xffff0000, v4
	v_med3_f32 v8, v12, s51, v187
	v_med3_f32 v9, v13, s51, v187
	v_cvt_pk_fp8_f32 v7, v8, v9 op_sel:[0,0,1]
	v_add_co_u32_e32 v8, vcc, s21, v14
	v_max_f32_e32 v10, v10, v10
	s_nop 0
	v_addc_co_u32_e32 v9, vcc, 0, v15, vcc
	global_store_dwordx2 v[8:9], v[6:7], off
	v_lshlrev_b32_e32 v6, 16, v2
	v_and_b32_e32 v2, 0xffff0000, v2
	v_max_f32_e32 v6, v6, v6
	v_max_f32_e32 v2, v2, v2
	v_max_f32_e32 v6, 0xda24260, v6
	v_max_f32_e32 v7, 0xda24260, v2
	v_pk_mul_f32 v[6:7], v[6:7], s[18:19] op_sel_hi:[1,0]
	v_lshlrev_b32_e32 v2, 16, v3
	v_and_b32_e32 v3, 0xffff0000, v3
	v_pk_mul_f32 v[6:7], v[34:35], v[6:7]
	v_max_f32_e32 v2, v2, v2
	v_max_f32_e32 v3, v3, v3
	v_med3_f32 v12, v6, s51, v187
	v_med3_f32 v7, v7, s51, v187
	v_mov_b32_e32 v6, 0
	v_max_f32_e32 v2, 0xda24260, v2
	v_max_f32_e32 v3, 0xda24260, v3
	v_max_f32_e32 v4, v4, v4
	v_cvt_pk_fp8_f32 v6, v12, v7
	v_pk_mul_f32 v[2:3], v[2:3], s[18:19] op_sel_hi:[1,0]
	v_max_f32_e32 v10, 0xda24260, v10
	v_max_f32_e32 v11, 0xda24260, v4
	v_pk_mul_f32 v[2:3], v[36:37], v[2:3]
	v_pk_mul_f32 v[10:11], v[10:11], s[18:19] op_sel_hi:[1,0]
	v_lshlrev_b32_e32 v4, 16, v5
	v_and_b32_e32 v5, 0xffff0000, v5
	v_pk_mul_f32 v[10:11], v[30:31], v[10:11]
	v_med3_f32 v2, v2, s51, v187
	v_med3_f32 v3, v3, s51, v187
	v_max_f32_e32 v4, v4, v4
	v_max_f32_e32 v5, v5, v5
	v_cvt_pk_fp8_f32 v6, v2, v3 op_sel:[0,0,1]
	v_med3_f32 v2, v10, s51, v187
	v_med3_f32 v3, v11, s51, v187
	v_mov_b32_e32 v7, 0
	v_max_f32_e32 v4, 0xda24260, v4
	v_max_f32_e32 v5, 0xda24260, v5
	v_cvt_pk_fp8_f32 v7, v2, v3
	v_pk_mul_f32 v[4:5], v[4:5], s[18:19] op_sel_hi:[1,0]
	s_andn2_b64 vcc, exec, s[2:3]
	v_pk_mul_f32 v[4:5], v[32:33], v[4:5]
	s_nop 0
	v_med3_f32 v2, v4, s51, v187
	v_med3_f32 v3, v5, s51, v187
	v_cvt_pk_fp8_f32 v7, v2, v3 op_sel:[0,0,1]
	global_store_dwordx2 v[8:9], v[6:7], off offset:128
	s_cbranch_vccnz .LBB0_1700
	s_andn2_b64 vcc, exec, s[0:1]
	s_cbranch_vccnz .LBB0_1699
	s_barrier
	s_branch .LBB0_1699

; #define GAS __attribute__((address_space(1)))
;     ...
;         if constexpr (ES == 1) asm volatile("s_nop 15\n\ts_nop 15" ::: "memory");
;     __device__ __forceinline__ void operator()(const f32x4 (&acc)[2][2][4][2], const Unit& u, int wr, int wc, int fr, int fq) const {
;         const int row0 = u.pm * 256 + wr * 64 + fr, col0 = u.pn * 256 + wc * 32 + 4 * fq; const float* gp = gate + (u.pm >> 3) * MODW + col0;
;         f32x4 gv[2][2];
; #pragma unroll
;         for (int bj = 0; bj < 2; ++bj)
; #pragma unroll
;             for (int n = 0; n < 2; ++n) gv[bj][n] = *(const GAS f32x4*)(gp + bj * 128 + n * 16) * scale;
;         size_t off0 = (size_t)row0 * DM + col0; asm volatile("" : "+v"(off0));
;         f32x4 B0[4], B1[4];
;     ...
;         ER_LOAD(B0, 0); ER_LOAD(B1, 1); ER_STORE(B0, 0); ER_LOAD(B0, 2); ER_STORE(B1, 1); ER_LOAD(B1, 3); ER_STORE(B0, 2); ER_LOAD(B0, 4); ER_STORE(B1, 3); ER_LOAD(B1, 5);
;         ER_STORE(B0, 4); ER_LOAD(B0, 6); ER_STORE(B1, 5); ER_LOAD(B1, 7); ER_STORE(B0, 6); ER_STORE(B1, 7);
.LBB0_2651:
	s_lshr_b32 s44, s79, 3
	s_mulk_i32 s44, 0x6000
	s_ashr_i32 s45, s44, 31
	s_lshl_b64 s[44:45], s[44:45], 2
	v_lshl_or_b32 v0, s80, 8, v182
	s_add_u32 s44, s57, s44
	s_addc_u32 s45, s58, s45
	v_ashrrev_i32_e32 v1, 31, v0
	s_nop 15
	s_nop 15
	v_lshl_add_u64 v[10:11], v[0:1], 2, s[44:45]
	global_load_dwordx4 v[2:5], v[10:11], off
	global_load_dwordx4 v[6:9], v[10:11], off offset:64
	global_load_dwordx4 v[20:23], v[10:11], off offset:512
	global_load_dwordx4 v[24:27], v[10:11], off offset:576
	v_lshl_add_u32 v10, s79, 8, v180
	v_ashrrev_i32_e32 v11, 31, v10
	v_lshlrev_b64 v[10:11], 12, v[10:11]
	v_readlane_b32 s44, v248, 6
	v_lshl_add_u64 v[0:1], v[10:11], 0, v[0:1]
	v_readlane_b32 s45, v248, 7
	v_readlane_b32 s92, v248, 14
	v_readlane_b32 s89, v248, 15
	v_lshl_add_u64 v[18:19], v[0:1], 1, s[44:45]
	v_add_co_u32_e32 v10, vcc, s64, v18
	global_load_dwordx2 v[28:29], v[18:19], off nt
	global_load_dwordx2 v[30:31], v[18:19], off offset:32 nt
	global_load_dwordx2 v[172:173], v[18:19], off offset:256 nt
	global_load_dwordx2 v[174:175], v[18:19], off offset:288 nt
	v_addc_co_u32_e32 v11, vcc, 0, v19, vcc
	global_load_dwordx2 v[176:177], v[10:11], off nt
	v_lshl_add_u64 v[10:11], v[18:19], 0, s[14:15]
	global_load_dwordx2 v[178:179], v[10:11], off offset:32 nt
	global_load_dwordx2 v[186:187], v[10:11], off offset:256 nt
	global_load_dwordx2 v[188:189], v[10:11], off offset:288 nt
	v_readlane_b32 s44, v249, 0
	v_readlane_b32 s50, v249, 6
	v_readlane_b32 s51, v249, 7
	v_add_co_u32_e32 v192, vcc, s65, v18
	s_nop 0
	v_lshl_add_u64 v[0:1], v[0:1], 2, s[50:51]
	v_addc_co_u32_e32 v193, vcc, 0, v19, vcc
	v_lshl_add_u64 v[190:191], v[18:19], 0, s[16:17]
	v_readlane_b32 s45, v249, 1
	v_readlane_b32 s46, v249, 2
	v_readlane_b32 s47, v249, 3
	v_readlane_b32 s48, v249, 4
	v_readlane_b32 s49, v249, 5
	s_waitcnt vmcnt(11)
	v_pk_mul_f32 v[14:15], v[4:5], s[12:13] op_sel_hi:[1,0]
	v_pk_mul_f32 v[16:17], v[2:3], s[12:13] op_sel_hi:[1,0]
	s_waitcnt vmcnt(10)
	v_pk_mul_f32 v[12:13], v[8:9], s[12:13] op_sel_hi:[1,0]
	v_pk_mul_f32 v[10:11], v[6:7], s[12:13] op_sel_hi:[1,0]
	s_waitcnt vmcnt(9)
	v_pk_mul_f32 v[8:9], v[22:23], s[12:13] op_sel_hi:[1,0]
	v_pk_mul_f32 v[6:7], v[20:21], s[12:13] op_sel_hi:[1,0]
	s_waitcnt vmcnt(8)
	v_pk_mul_f32 v[4:5], v[26:27], s[12:13] op_sel_hi:[1,0]
	v_pk_mul_f32 v[2:3], v[24:25], s[12:13] op_sel_hi:[1,0]
	s_waitcnt vmcnt(7)
	v_lshlrev_b32_e32 v20, 16, v28
	v_and_b32_e32 v21, 0xffff0000, v28
	v_lshlrev_b32_e32 v22, 16, v29
	v_and_b32_e32 v23, 0xffff0000, v29
	s_waitcnt vmcnt(6)
	v_lshlrev_b32_e32 v24, 16, v30
	v_and_b32_e32 v25, 0xffff0000, v30
	v_lshlrev_b32_e32 v26, 16, v31
	v_and_b32_e32 v27, 0xffff0000, v31
	s_waitcnt vmcnt(5)
	v_lshlrev_b32_e32 v28, 16, v172
	v_and_b32_e32 v29, 0xffff0000, v172
	v_lshlrev_b32_e32 v30, 16, v173
	v_and_b32_e32 v31, 0xffff0000, v173
	s_waitcnt vmcnt(4)
	v_lshlrev_b32_e32 v172, 16, v174
	v_and_b32_e32 v173, 0xffff0000, v174
	v_lshlrev_b32_e32 v174, 16, v175
	v_and_b32_e32 v175, 0xffff0000, v175
	s_waitcnt vmcnt(3)
	v_lshlrev_b32_e32 v194, 16, v176
	v_and_b32_e32 v195, 0xffff0000, v176
	v_lshlrev_b32_e32 v176, 16, v177
	v_and_b32_e32 v177, 0xffff0000, v177
	v_pk_fma_f32 v[22:23], v[158:159], v[14:15], v[22:23]
	v_pk_fma_f32 v[20:21], v[156:157], v[16:17], v[20:21]
	v_pk_fma_f32 v[26:27], v[154:155], v[12:13], v[26:27]
	v_pk_fma_f32 v[24:25], v[152:153], v[10:11], v[24:25]
	v_pk_fma_f32 v[30:31], v[150:151], v[8:9], v[30:31]
	v_pk_fma_f32 v[28:29], v[148:149], v[6:7], v[28:29]
	v_pk_fma_f32 v[146:147], v[146:147], v[4:5], v[174:175]
	v_pk_fma_f32 v[144:145], v[144:145], v[2:3], v[172:173]
	global_store_dwordx4 v[0:1], v[20:23], off
	global_store_dwordx4 v[0:1], v[24:27], off offset:64
	global_store_dwordx4 v[0:1], v[28:31], off offset:512
	global_store_dwordx4 v[0:1], v[144:147], off offset:576
	v_pk_fma_f32 v[22:23], v[142:143], v[14:15], v[176:177]
	v_add_co_u32_e32 v142, vcc, s65, v0
	s_waitcnt vmcnt(6)
	v_lshlrev_b32_e32 v196, 16, v178
	v_and_b32_e32 v197, 0xffff0000, v178
	v_lshlrev_b32_e32 v178, 16, v179
	v_and_b32_e32 v179, 0xffff0000, v179
	v_pk_fma_f32 v[20:21], v[140:141], v[16:17], v[194:195]
	v_addc_co_u32_e32 v143, vcc, 0, v1, vcc
	s_waitcnt vmcnt(5)
	v_lshlrev_b32_e32 v198, 16, v186
	v_and_b32_e32 v199, 0xffff0000, v186
	v_lshlrev_b32_e32 v186, 16, v187
	v_and_b32_e32 v187, 0xffff0000, v187
	global_load_dwordx2 v[24:25], v[192:193], off nt
	global_load_dwordx2 v[26:27], v[190:191], off offset:32 nt
	global_load_dwordx2 v[28:29], v[190:191], off offset:256 nt
	global_load_dwordx2 v[30:31], v[190:191], off offset:288 nt
	v_lshl_add_u64 v[140:141], v[0:1], 0, s[16:17]
	global_store_dwordx4 v[142:143], v[20:23], off
	s_waitcnt vmcnt(9)
	v_lshlrev_b32_e32 v200, 16, v188
	v_and_b32_e32 v201, 0xffff0000, v188
	v_pk_fma_f32 v[22:23], v[138:139], v[12:13], v[178:179]
	v_pk_fma_f32 v[20:21], v[136:137], v[10:11], v[196:197]
	v_lshlrev_b32_e32 v188, 16, v189
	v_and_b32_e32 v189, 0xffff0000, v189
	global_store_dwordx4 v[140:141], v[20:23], off offset:64
	v_lshl_add_u64 v[136:137], v[18:19], 0, s[22:23]
	s_waitcnt vmcnt(4)
;     __device__ __forceinline__ void operator()(const f32x4 (&acc)[2][2][4][2], const Unit& u, int wr, int wc, int fr, int fq) const {
;     ...
;         ER_LOAD(B0, 0); ER_LOAD(B1, 1); ER_STORE(B0, 0); ER_LOAD(B0, 2); ER_STORE(B1, 1); ER_LOAD(B1, 3); ER_STORE(B0, 2); ER_LOAD(B0, 4); ER_STORE(B1, 3); ER_LOAD(B1, 5);
;         ER_STORE(B0, 4); ER_LOAD(B0, 6); ER_STORE(B1, 5); ER_LOAD(B1, 7); ER_STORE(B0, 6); ER_STORE(B1, 7);
	v_lshlrev_b32_e32 v142, 16, v26
	v_pk_fma_f32 v[22:23], v[134:135], v[8:9], v[186:187]
	v_pk_fma_f32 v[20:21], v[132:133], v[6:7], v[198:199]
	global_store_dwordx4 v[140:141], v[20:23], off offset:512
	v_and_b32_e32 v143, 0xffff0000, v26
	v_lshlrev_b32_e32 v26, 16, v27
	v_pk_fma_f32 v[22:23], v[130:131], v[4:5], v[188:189]
	v_pk_fma_f32 v[20:21], v[128:129], v[2:3], v[200:201]
	global_store_dwordx4 v[140:141], v[20:23], off offset:576
	v_lshlrev_b32_e32 v140, 16, v24
	v_and_b32_e32 v141, 0xffff0000, v24
	v_add_co_u32_e32 v20, vcc, s66, v18
	v_lshl_add_u64 v[22:23], v[18:19], 0, s[18:19]
	s_nop 0
	v_addc_co_u32_e32 v21, vcc, 0, v19, vcc
	global_load_dwordx2 v[20:21], v[20:21], off nt
	s_nop 0
	global_load_dwordx2 v[128:129], v[22:23], off offset:32 nt
	global_load_dwordx2 v[130:131], v[22:23], off offset:256 nt
	s_nop 0
	global_load_dwordx2 v[22:23], v[22:23], off offset:288 nt
	v_add_co_u32_e32 v134, vcc, s67, v0
	v_lshlrev_b32_e32 v24, 16, v25
	s_nop 0
	v_addc_co_u32_e32 v135, vcc, 0, v1, vcc
	v_add_co_u32_e32 v138, vcc, s68, v18
	v_and_b32_e32 v25, 0xffff0000, v25
	s_nop 0
	v_addc_co_u32_e32 v139, vcc, 0, v19, vcc
	v_and_b32_e32 v27, 0xffff0000, v27
	s_waitcnt vmcnt(9)
	v_lshlrev_b32_e32 v144, 16, v28
	v_and_b32_e32 v145, 0xffff0000, v28
	v_lshlrev_b32_e32 v28, 16, v29
	v_and_b32_e32 v29, 0xffff0000, v29
	s_waitcnt vmcnt(8)
	v_lshlrev_b32_e32 v146, 16, v30
	v_and_b32_e32 v147, 0xffff0000, v30
	v_lshlrev_b32_e32 v148, 16, v31
	v_and_b32_e32 v149, 0xffff0000, v31
	v_lshl_add_u64 v[132:133], v[0:1], 0, s[20:21]
	v_pk_fma_f32 v[26:27], v[122:123], v[12:13], v[26:27]
	v_pk_fma_f32 v[30:31], v[118:119], v[8:9], v[28:29]
	v_pk_fma_f32 v[28:29], v[116:117], v[6:7], v[144:145]
	v_pk_fma_f32 v[114:115], v[114:115], v[4:5], v[148:149]
	v_pk_fma_f32 v[112:113], v[112:113], v[2:3], v[146:147]
	s_waitcnt vmcnt(2)
	v_lshlrev_b32_e32 v154, 16, v128
	v_lshlrev_b32_e32 v150, 16, v20
	v_and_b32_e32 v151, 0xffff0000, v20
	v_lshlrev_b32_e32 v152, 16, v21
	v_and_b32_e32 v153, 0xffff0000, v21
	s_waitcnt vmcnt(0)
	v_lshlrev_b32_e32 v158, 16, v22
	v_and_b32_e32 v159, 0xffff0000, v22
	v_lshlrev_b32_e32 v172, 16, v23
	v_and_b32_e32 v173, 0xffff0000, v23
	v_pk_fma_f32 v[22:23], v[126:127], v[14:15], v[24:25]
	v_pk_fma_f32 v[20:21], v[124:125], v[16:17], v[140:141]
	v_pk_fma_f32 v[24:25], v[120:121], v[10:11], v[142:143]
	global_store_dwordx4 v[134:135], v[20:23], off
	global_store_dwordx4 v[132:133], v[24:27], off offset:64
	global_store_dwordx4 v[132:133], v[28:31], off offset:512
	global_store_dwordx4 v[132:133], v[112:115], off offset:576
	v_pk_fma_f32 v[22:23], v[110:111], v[14:15], v[152:153]
	v_add_co_u32_e32 v110, vcc, s69, v0
	v_and_b32_e32 v155, 0xffff0000, v128
	v_lshlrev_b32_e32 v128, 16, v129
	v_and_b32_e32 v129, 0xffff0000, v129
	v_pk_fma_f32 v[20:21], v[108:109], v[16:17], v[150:151]
	v_addc_co_u32_e32 v111, vcc, 0, v1, vcc
	v_lshlrev_b32_e32 v156, 16, v130
	v_and_b32_e32 v157, 0xffff0000, v130
	v_lshlrev_b32_e32 v130, 16, v131
	v_and_b32_e32 v131, 0xffff0000, v131
	global_load_dwordx2 v[24:25], v[138:139], off nt
	global_load_dwordx2 v[26:27], v[136:137], off offset:32 nt
	global_load_dwordx2 v[28:29], v[136:137], off offset:256 nt
	global_load_dwordx2 v[30:31], v[136:137], off offset:288 nt
	v_lshl_add_u64 v[108:109], v[0:1], 0, s[24:25]
	global_store_dwordx4 v[110:111], v[20:23], off
	s_waitcnt vmcnt(2)
	v_lshlrev_b32_e32 v110, 16, v28
	v_pk_fma_f32 v[22:23], v[106:107], v[12:13], v[128:129]
	v_pk_fma_f32 v[20:21], v[104:105], v[10:11], v[154:155]
	global_store_dwordx4 v[108:109], v[20:23], off offset:64
	v_lshlrev_b32_e32 v106, 16, v24
	v_and_b32_e32 v107, 0xffff0000, v24
	v_pk_fma_f32 v[22:23], v[102:103], v[8:9], v[130:131]
	v_pk_fma_f32 v[20:21], v[100:101], v[6:7], v[156:157]
	global_store_dwordx4 v[108:109], v[20:23], off offset:512
	v_lshlrev_b32_e32 v24, 16, v25
	v_and_b32_e32 v25, 0xffff0000, v25
	v_pk_fma_f32 v[22:23], v[98:99], v[4:5], v[172:173]
	v_pk_fma_f32 v[20:21], v[96:97], v[2:3], v[158:159]
	global_store_dwordx4 v[108:109], v[20:23], off offset:576
	v_lshlrev_b32_e32 v108, 16, v26
	v_and_b32_e32 v109, 0xffff0000, v26
	v_add_co_u32_e32 v20, vcc, s70, v18
	v_lshl_add_u64 v[22:23], v[18:19], 0, s[26:27]
	s_nop 0
	v_addc_co_u32_e32 v21, vcc, 0, v19, vcc
	global_load_dwordx2 v[20:21], v[20:21], off nt
	s_nop 0
	global_load_dwordx2 v[96:97], v[22:23], off offset:32 nt
	global_load_dwordx2 v[98:99], v[22:23], off offset:256 nt
	s_nop 0
	global_load_dwordx2 v[22:23], v[22:23], off offset:288 nt
	v_add_co_u32_e32 v102, vcc, s71, v0
	v_lshlrev_b32_e32 v26, 16, v27
	s_nop 0
	v_addc_co_u32_e32 v103, vcc, 0, v1, vcc
	v_and_b32_e32 v27, 0xffff0000, v27
	v_and_b32_e32 v111, 0xffff0000, v28
	v_lshlrev_b32_e32 v28, 16, v29
	v_and_b32_e32 v29, 0xffff0000, v29
	s_waitcnt vmcnt(8)
	v_lshlrev_b32_e32 v112, 16, v30
	v_and_b32_e32 v113, 0xffff0000, v30
	v_lshlrev_b32_e32 v114, 16, v31
	v_and_b32_e32 v115, 0xffff0000, v31
	v_lshl_add_u64 v[100:101], v[0:1], 0, s[28:29]
	v_pk_fma_f32 v[26:27], v[90:91], v[12:13], v[26:27]
	v_pk_fma_f32 v[30:31], v[86:87], v[8:9], v[28:29]
	v_pk_fma_f32 v[28:29], v[84:85], v[6:7], v[110:111]
	v_pk_fma_f32 v[82:83], v[82:83], v[4:5], v[114:115]
	v_pk_fma_f32 v[80:81], v[80:81], v[2:3], v[112:113]
	v_lshl_add_u64 v[104:105], v[18:19], 0, s[30:31]
	s_waitcnt vmcnt(2)
; #define PG8_BAR __builtin_amdgcn_s_barrier()
;     ...
;         if (!has_next) break;
; #pragma unroll
;         for (int a = 0; a < 2; ++a)
; #pragma unroll
;             for (int b = 0; b < 2; ++b)
; #pragma unroll
;                 for (int m = 0; m < 4; ++m)
; #pragma unroll
;                     for (int n = 0; n < 2; ++n) acc[a][b][m][n] = (f32x4){0.f, 0.f, 0.f, 0.f};
;         cur = nxt; cA = nA; cB = nB; ++ui;
;         if constexpr (ALIGN_EPI) { if (wr == 1) PG8_BAR; }
;     __device__ __forceinline__ void operator()(const f32x4 (&acc)[2][2][4][2], const Unit& u, int wr, int wc, int fr, int fq) const {
;     ...
;         ER_LOAD(B0, 0); ER_LOAD(B1, 1); ER_STORE(B0, 0); ER_LOAD(B0, 2); ER_STORE(B1, 1); ER_LOAD(B1, 3); ER_STORE(B0, 2); ER_LOAD(B0, 4); ER_STORE(B1, 3); ER_LOAD(B1, 5);
;         ER_STORE(B0, 4); ER_LOAD(B0, 6); ER_STORE(B1, 5); ER_LOAD(B1, 7); ER_STORE(B0, 6); ER_STORE(B1, 7);
	v_lshlrev_b32_e32 v120, 16, v96
	v_lshlrev_b32_e32 v116, 16, v20
	v_and_b32_e32 v117, 0xffff0000, v20
	v_lshlrev_b32_e32 v118, 16, v21
	v_and_b32_e32 v119, 0xffff0000, v21
	s_waitcnt vmcnt(0)
	v_lshlrev_b32_e32 v124, 16, v22
	v_and_b32_e32 v125, 0xffff0000, v22
	v_lshlrev_b32_e32 v126, 16, v23
	v_and_b32_e32 v127, 0xffff0000, v23
	v_pk_fma_f32 v[22:23], v[94:95], v[14:15], v[24:25]
	v_pk_fma_f32 v[20:21], v[92:93], v[16:17], v[106:107]
	v_pk_fma_f32 v[24:25], v[88:89], v[10:11], v[108:109]
	global_store_dwordx4 v[102:103], v[20:23], off
	global_store_dwordx4 v[100:101], v[24:27], off offset:64
	global_store_dwordx4 v[100:101], v[28:31], off offset:512
	global_store_dwordx4 v[100:101], v[80:83], off offset:576
	v_add_co_u32_e32 v20, vcc, s72, v18
	v_pk_fma_f32 v[22:23], v[78:79], v[14:15], v[118:119]
	s_nop 0
	v_addc_co_u32_e32 v21, vcc, 0, v19, vcc
	v_add_co_u32_e32 v78, vcc, s73, v0
	v_and_b32_e32 v121, 0xffff0000, v96
	v_lshlrev_b32_e32 v96, 16, v97
	v_and_b32_e32 v97, 0xffff0000, v97
	global_load_dwordx2 v[24:25], v[20:21], off nt
	global_load_dwordx2 v[26:27], v[104:105], off offset:32 nt
	global_load_dwordx2 v[28:29], v[104:105], off offset:256 nt
	global_load_dwordx2 v[30:31], v[104:105], off offset:288 nt
	v_pk_fma_f32 v[20:21], v[76:77], v[16:17], v[116:117]
	v_addc_co_u32_e32 v79, vcc, 0, v1, vcc
	v_lshlrev_b32_e32 v122, 16, v98
	v_and_b32_e32 v123, 0xffff0000, v98
	v_lshlrev_b32_e32 v98, 16, v99
	v_and_b32_e32 v99, 0xffff0000, v99
	v_lshl_add_u64 v[76:77], v[0:1], 0, s[34:35]
	global_store_dwordx4 v[78:79], v[20:23], off
	s_waitcnt vmcnt(1)
	v_lshlrev_b32_e32 v78, 16, v30
	v_pk_fma_f32 v[22:23], v[74:75], v[12:13], v[96:97]
	v_pk_fma_f32 v[20:21], v[72:73], v[10:11], v[120:121]
	global_store_dwordx4 v[76:77], v[20:23], off offset:64
	v_lshlrev_b32_e32 v72, 16, v24
	v_and_b32_e32 v73, 0xffff0000, v24
	v_pk_fma_f32 v[22:23], v[70:71], v[8:9], v[98:99]
	v_pk_fma_f32 v[20:21], v[68:69], v[6:7], v[122:123]
	global_store_dwordx4 v[76:77], v[20:23], off offset:512
	v_lshl_add_u64 v[70:71], v[0:1], 0, s[40:41]
	v_lshlrev_b32_e32 v24, 16, v25
	v_pk_fma_f32 v[22:23], v[66:67], v[4:5], v[126:127]
	v_pk_fma_f32 v[20:21], v[64:65], v[2:3], v[124:125]
	global_store_dwordx4 v[76:77], v[20:23], off offset:576
	v_lshl_add_u64 v[66:67], v[0:1], 0, s[38:39]
	v_and_b32_e32 v25, 0xffff0000, v25
	v_add_co_u32_e32 v20, vcc, s74, v18
	v_lshlrev_b32_e32 v74, 16, v26
	s_nop 0
	v_addc_co_u32_e32 v21, vcc, 0, v19, vcc
	v_lshl_add_u64 v[18:19], v[18:19], 0, s[36:37]
	global_load_dwordx2 v[20:21], v[20:21], off nt
	s_nop 0
	global_load_dwordx2 v[22:23], v[18:19], off offset:32 nt
	global_load_dwordx2 v[64:65], v[18:19], off offset:256 nt
	s_nop 0
	global_load_dwordx2 v[18:19], v[18:19], off offset:288 nt
	v_add_co_u32_e32 v68, vcc, s75, v0
	v_and_b32_e32 v75, 0xffff0000, v26
	s_nop 0
	v_addc_co_u32_e32 v69, vcc, 0, v1, vcc
	v_add_co_u32_e32 v0, vcc, s76, v0
	v_lshlrev_b32_e32 v26, 16, v27
	v_and_b32_e32 v27, 0xffff0000, v27
	v_lshlrev_b32_e32 v76, 16, v28
	v_and_b32_e32 v77, 0xffff0000, v28
	v_lshlrev_b32_e32 v28, 16, v29
	v_and_b32_e32 v29, 0xffff0000, v29
	v_and_b32_e32 v79, 0xffff0000, v30
	v_lshlrev_b32_e32 v30, 16, v31
	v_and_b32_e32 v31, 0xffff0000, v31
	v_addc_co_u32_e32 v1, vcc, 0, v1, vcc
	v_pk_fma_f32 v[28:29], v[50:51], v[8:9], v[28:29]
	v_pk_fma_f32 v[42:43], v[42:43], v[4:5], v[30:31]
	v_pk_fma_f32 v[40:41], v[40:41], v[2:3], v[78:79]
	s_and_b64 vcc, exec, s[0:1]
	s_mov_b64 s[0:1], -1
	s_waitcnt vmcnt(2)
	v_lshlrev_b32_e32 v84, 16, v22
	v_lshlrev_b32_e32 v80, 16, v20
	v_and_b32_e32 v81, 0xffff0000, v20
	v_lshlrev_b32_e32 v82, 16, v21
	v_and_b32_e32 v83, 0xffff0000, v21
	v_and_b32_e32 v85, 0xffff0000, v22
	v_lshlrev_b32_e32 v86, 16, v23
	v_and_b32_e32 v87, 0xffff0000, v23
	s_waitcnt vmcnt(1)
	v_lshlrev_b32_e32 v88, 16, v64
	v_and_b32_e32 v89, 0xffff0000, v64
	v_lshlrev_b32_e32 v64, 16, v65
	v_and_b32_e32 v65, 0xffff0000, v65
	s_waitcnt vmcnt(0)
	v_lshlrev_b32_e32 v90, 16, v18
	v_and_b32_e32 v91, 0xffff0000, v18
	v_lshlrev_b32_e32 v92, 16, v19
	v_and_b32_e32 v93, 0xffff0000, v19
	v_pk_fma_f32 v[20:21], v[62:63], v[14:15], v[24:25]
	v_pk_fma_f32 v[18:19], v[60:61], v[16:17], v[72:73]
	v_pk_fma_f32 v[24:25], v[58:59], v[12:13], v[26:27]
	v_pk_fma_f32 v[22:23], v[56:57], v[10:11], v[74:75]
	v_pk_fma_f32 v[26:27], v[48:49], v[6:7], v[76:77]
	global_store_dwordx4 v[68:69], v[18:21], off
	global_store_dwordx4 v[66:67], v[22:25], off offset:64
	global_store_dwordx4 v[66:67], v[26:29], off offset:512
	global_store_dwordx4 v[66:67], v[40:43], off offset:576
	v_pk_fma_f32 v[18:19], v[54:55], v[14:15], v[82:83]
	v_pk_fma_f32 v[16:17], v[52:53], v[16:17], v[80:81]
	v_pk_fma_f32 v[12:13], v[46:47], v[12:13], v[86:87]
	v_pk_fma_f32 v[10:11], v[44:45], v[10:11], v[84:85]
	v_pk_fma_f32 v[8:9], v[38:39], v[8:9], v[64:65]
	v_pk_fma_f32 v[6:7], v[36:37], v[6:7], v[88:89]
	v_pk_fma_f32 v[4:5], v[34:35], v[4:5], v[92:93]
	v_pk_fma_f32 v[2:3], v[32:33], v[2:3], v[90:91]
	global_store_dwordx4 v[0:1], v[16:19], off
	global_store_dwordx4 v[70:71], v[10:13], off offset:64
	global_store_dwordx4 v[70:71], v[6:9], off offset:512
	global_store_dwordx4 v[70:71], v[2:5], off offset:576
	s_cbranch_vccnz .LBB0_2636
	s_andn2_b64 vcc, exec, s[6:7]
	s_cbranch_vccnz .LBB0_2635
	s_barrier
	s_branch .LBB0_2635
